# GEMM phases: one static s_setprio raise for the trailing wave half at phase entry, per-MFMA-segment priority toggles removed; on top of v50
# speedup vs baseline: 1.0099x; 1.0099x over previous
; template <class Epi, class Sched, bool ALIGN_EPI = false, bool SP2 = false>
; __device__ __forceinline__ void gemm_phase(PG8_LAS unsigned char* lds, const Gemm g, const Sched& S, const Epi& E, const int tid_in) {
;     ...
;     for (int i = 0; i < 2; ++i) { int R, C; stage_rc(tid * 16 + i * 8192, R, C); const int Rb = Epi::PERM ? ((R & ~31) + perm32(R & 31)) : R;
;         voffA[i] = (unsigned)(R * K + C) * 2u; voffB[i] = (unsigned)(Rb * LDB + C) * 2u; gR[i] = R; gC[i] = C * 2; }
;     const size_t kstep = (size_t)(BK * 2);
;     const size_t hstep = (size_t)HALF * K * 2;
;     const size_t tstep = 2 * hstep; const size_t kstepB = g.btiled ? (size_t)32768 : kstep, hstepB = g.btiled ? (size_t)16384 : hstep;
;     const unsigned ldsw = (unsigned)wid * 1024u;
;     const int aoff = lds_byte(wr * 64 + fr, fq * 8), boff = lds_byte(wc * 32 + fr, fq * 8);
;     ...
;     Unit cur, nxt; int ui = 0;
;     if (!S.next(0, cur)) return;
;     f32x4 acc[2][2][4][2];
; #pragma unroll
;     for (int a = 0; a < 2; ++a)
; #pragma unroll
;         for (int b = 0; b < 2; ++b)
; #pragma unroll
;             for (int m = 0; m < 4; ++m)
; #pragma unroll
;                 for (int n = 0; n < 2; ++n) acc[a][b][m][n] = (f32x4){0.f, 0.f, 0.f, 0.f};
;     bf16x8 At[4][2], B0[2][2], B1[2][2];
;     const char* cA = (const char*)g.A + (Sched::GATHER ? (size_t)0 : (size_t)cur.pm * tstep); if constexpr (Sched::GATHER) PG8_GFILL(vc, 0); const char* cB = (const char*)g.Bt + (size_t)cur.pn * tstep + (size_t)cur.e * g.estride;
;     S.a_ready(cur);
;     if constexpr (SP2) {
;         PG8_STAGE(PG8_SB(0, 0), cB, voffB); PG8_STAGE(PG8_SB(0, 1), cB + hstepB, voffB); PG8_STAGE_A(PG8_SA(0, 0), cA, 0, false); PG8_STAGE_A(PG8_SA(0, 1), cA, 1, false);
;         if (wr == 1) PG8_BAR;
;         PG8_WAIT_V(2); PG8_BAR;
;         PG8_STAGE(PG8_SB(1, 0), cB + kstepB, voffB); PG8_STAGE_A(PG8_SA(1, 0), cA + kstep, 0, false); PG8_STAGE(PG8_SB(1, 1), cB + hstepB + kstepB, voffB);
;         PG8_WAIT_V(6); PG8_BAR;
;     } else {
;         PG8_STAGE(PG8_SB(0, 0), cB, voffB); PG8_STAGE_A(PG8_SA(0, 0), cA, 0, false); PG8_STAGE(PG8_SB(0, 1), cB + hstepB, voffB); PG8_STAGE_A(PG8_SA(0, 1), cA, 1, false);
;         if (wr == 1) PG8_BAR;
;         PG8_WAIT_V(4); PG8_BAR;
;         PG8_STAGE(PG8_SB(1, 0), cB + kstepB, voffB); PG8_STAGE_A(PG8_SA(1, 0), cA + kstep, 0, false); PG8_STAGE(PG8_SB(1, 1), cB + hstepB + kstepB, voffB);
.LBB0_191:
	v_ashrrev_i32_e32 v2, 31, v0
	v_lshrrev_b32_e32 v2, 26, v2
	v_lshlrev_b32_e32 v1, 4, v0
	v_add_u32_e32 v2, v0, v2
	v_bfe_i32 v0, v0, 27, 1
	v_lshrrev_b32_e32 v0, 22, v0
	v_add_u32_e32 v0, v1, v0
	v_and_b32_e32 v0, 0xfffffc00, v0
	v_sub_u32_e32 v0, v1, v0
	v_ashrrev_i32_e32 v5, 6, v2
	v_lshrrev_b32_e32 v2, 4, v0
	v_bitop3_b32 v0, v2, v0, 32 bitop3:0x6c
	v_ashrrev_i32_e32 v3, 31, v0
	v_lshrrev_b32_e32 v3, 26, v3
	v_add_u32_e32 v3, v0, v3
	v_lshlrev_b32_e32 v2, 3, v5
	v_ashrrev_i32_e32 v6, 6, v3
	v_and_b32_e32 v3, 0xc0, v3
	v_and_b32_e32 v2, -16, v2
	v_sub_u32_e32 v0, v0, v3
	v_mov_b32_e32 v3, 1
	v_add_u32_e32 v2, v6, v2
	v_lshlrev_b32_e32 v7, 5, v5
	v_ashrrev_i16_sdwa v0, v3, sext(v0) dst_sel:DWORD dst_unused:UNUSED_PAD src0_sel:DWORD src1_sel:BYTE_0
	s_waitcnt vmcnt(19)
	v_and_b32_e32 v8, 32, v7
	v_bfe_i32 v7, v0, 0, 16
	v_lshlrev_b32_e32 v0, 1, v2
	v_lshrrev_b32_e32 v9, 2, v2
	v_and_b32_e32 v10, 3, v6
	s_mov_b32 s3, 0x1ffffe0
	v_and_b32_e32 v0, 24, v0
	v_and_b32_e32 v9, 4, v9
	v_and_or_b32 v10, v2, s3, v10
	v_or3_b32 v0, v10, v9, v0
	v_add_lshl_u32 v8, v8, v7, 1
	v_lshl_add_u32 v138, v0, 7, v8
	v_add_u32_e32 v0, 0x2000, v1
	v_ashrrev_i32_e32 v1, 31, v0
	v_lshrrev_b32_e32 v1, 22, v1
	v_add_u32_e32 v1, v0, v1
	v_lshl_add_u32 v136, v2, 12, v8
	v_ashrrev_i32_e32 v8, 10, v1
	v_mul_i32_i24_e32 v1, 0x400, v8
	v_sub_u32_e32 v0, v0, v1
	s_load_dwordx2 s[30:31], s[6:7], 0xc8
	v_lshrrev_b32_e32 v1, 4, v0
	v_bitop3_b32 v0, v1, v0, 32 bitop3:0x6c
	v_ashrrev_i32_e32 v2, 31, v0
	v_lshrrev_b32_e32 v2, 26, v2
	v_add_u32_e32 v2, v0, v2
	s_waitcnt lgkmcnt(0)
	s_add_u32 s22, s30, 0x36000000
	v_lshlrev_b32_e32 v1, 3, v8
	v_ashrrev_i32_e32 v9, 6, v2
	v_and_b32_e32 v2, 0xc0, v2
	s_addc_u32 s23, s31, 0
	v_and_b32_e32 v1, -16, v1
	v_sub_u32_e32 v0, v0, v2
	s_add_u32 s24, s30, 0x800000
	v_add_u32_e32 v1, v9, v1
	v_ashrrev_i16_sdwa v0, v3, sext(v0) dst_sel:DWORD dst_unused:UNUSED_PAD src0_sel:DWORD src1_sel:BYTE_0
	v_and_b32_e32 v3, 3, v9
	s_addc_u32 s25, s31, 0
	s_ashr_i32 s5, s4, 6
	v_and_or_b32 v3, v1, s3, v3
	s_ashr_i32 s3, s2, 31
	s_ashr_i32 s51, s50, 31
	s_ashr_i32 s6, s4, 8
	s_lshl_b32 s58, s5, 10
	s_lshl_b64 s[8:9], s[2:3], 20
	s_lshl_b64 s[10:11], s[50:51], 20
	v_lshlrev_b32_e32 v10, 5, v8
	s_add_u32 s52, s24, s10
	v_and_b32_e32 v11, 32, v10
	v_bfe_i32 v10, v0, 0, 16
	v_lshlrev_b32_e32 v0, 1, v1
	v_lshrrev_b32_e32 v2, 2, v1
	s_addc_u32 s53, s25, s11
	s_add_i32 s59, s58, 0
	v_and_b32_e32 v0, 24, v0
	v_and_b32_e32 v2, 4, v2
	s_add_i32 m0, s59, 0x10000
	v_or3_b32 v0, v3, v2, v0
	v_add_lshl_u32 v2, v11, v10, 1
	global_load_lds_dwordx4 v138, s[52:53]
	s_add_i32 m0, s59, 0x12000
	v_lshl_add_u32 v142, v0, 7, v2
	s_add_u32 s10, s52, 0x4000
	global_load_lds_dwordx4 v142, s[52:53]
	s_addc_u32 s11, s53, 0
	s_add_i32 m0, s59, 0x14000
	v_lshl_add_u32 v140, v1, 12, v2
	global_load_lds_dwordx4 v138, s[10:11]
	s_add_i32 m0, s59, 0x16000
	s_add_u32 s54, s22, s8
	s_addc_u32 s55, s23, s9
	s_add_i32 s60, s59, 0x2000
	global_load_lds_dwordx4 v142, s[10:11]
	s_mov_b32 m0, s59
	s_add_u32 s8, s54, 0x80000
	global_load_lds_dwordx4 v136, s[54:55]
	s_mov_b32 m0, s60
	s_addc_u32 s9, s55, 0
	s_add_i32 s61, s59, 0x4000
	global_load_lds_dwordx4 v140, s[54:55]
	s_mov_b32 m0, s61
	s_add_i32 s62, s59, 0x6000
	global_load_lds_dwordx4 v136, s[8:9]
	s_mov_b32 m0, s62
	v_mov_b32_e32 v145, 0
	global_load_lds_dwordx4 v140, s[8:9]
	v_mov_b32_e32 v137, v145
	v_mov_b32_e32 v141, v145
	s_cmp_eq_u32 s6, 1
	s_mov_b32 s7, 0
	v_mov_b32_e32 v139, v145
	v_mov_b32_e32 v143, v145
	v_lshl_add_u64 v[0:1], s[54:55], 0, v[136:137]
	s_cselect_b64 s[8:9], -1, 0
	s_cmp_lg_u32 s6, 1
	v_lshl_add_u64 v[2:3], s[54:55], 0, v[140:141]
	s_setprio 0
	s_cbranch_scc1 .LBB0_193
	s_setprio 1
	s_barrier

; #define PG8_STAGE(bufoff, gbase, voff) do { _Pragma("unroll") for (int _i = 0; _i < 2; ++_i) \
;         __builtin_amdgcn_global_load_lds((const unsigned*)((const char*)(gbase) + (voff)[_i]), (PG8_LAS unsigned*)(lds + (bufoff) + ldsw + _i * 8192), 16, 0, 0); } while (0)
; #define PG8_STAGE_A(bufoff, base, h, isnext) do { if constexpr (Sched::GATHER) { unsigned vv_[2] = {(isnext) ? vn[h][0] : vc[h][0], (isnext) ? vn[h][1] : vc[h][1]}; PG8_STAGE(bufoff, base, vv_); } else { PG8_STAGE(bufoff, (base) + (h) * hstep, voffA); } } while (0)
; #define PG8_LDA(dst, b, h) do { _Pragma("unroll") for (int m = 0; m < 4; ++m) _Pragma("unroll") for (int k = 0; k < 2; ++k) dst[m][k] = *(const PG8_LAS bf16x8*)(lds + PG8_SA(b, h) + aoff + m * 2048 + k * 1024); } while (0)
; #define PG8_LDB(dst, b, h) do { _Pragma("unroll") for (int n = 0; n < 2; ++n) _Pragma("unroll") for (int k = 0; k < 2; ++k) dst[n][k] = *(const PG8_LAS bf16x8*)(lds + PG8_SB(b, h) + boff + n * 2048 + k * 1024); } while (0)
; #define PG8_WAIT_V(n) asm volatile("s_waitcnt vmcnt(" #n ")" ::: "memory")
; #define PG8_WAIT_L(n) asm volatile("s_waitcnt lgkmcnt(" #n ")" ::: "memory")
; template <class Epi, class Sched, bool ALIGN_EPI = false, bool SP2 = false>
; __device__ __forceinline__ void gemm_phase(PG8_LAS unsigned char* lds, const Gemm g, const Sched& S, const Epi& E, const int tid_in) {
;     ...
;         for (int t = (Epi::HAS_MID && seg == 1) ? nt / 2 : 0; t < ((Epi::HAS_MID && seg == 0) ? nt / 2 : nt); t += 2) {
;             const bool last = (t == nt - 2);
;             const char* a1 = cA + (size_t)(t + 1) * kstep;
;             const char* a2 = last ? nA : cA + (size_t)(t + 2) * kstep; const char* b2 = last ? nB : cB + (size_t)(t + 2) * kstepB;
;             const char* a3 = a2 + kstep; const char* b3 = b2 + kstepB;
;             if (last && has_next) S.a_ready(nxt);
;             if constexpr (SP2) {
;             PG8_LDB(B0, 0, 0); PG8_LDB(B1, 0, 1); PG8_SCHED; PG8_LDA(At, 0, 0); PG8_STAGE_A(PG8_SA(1, 1), a1, 1, false);
;             PG8_WAIT_V(8); PG8_WAIT_L(0); PG8_BAR; PG8_MMA(0, 0, At, B0); PG8_MMA(0, 1, At, B1); PG8_BAR; PG8_SCHED;
;             PG8_LDA(At, 0, 1); PG8_STAGE(PG8_SB(0, 0), b2, voffB); PG8_STAGE(PG8_SB(0, 1), b2 + hstepB, voffB); PG8_STAGE_A(PG8_SA(0, 0), a2, 0, last);
;             PG8_WAIT_V(8); PG8_WAIT_L(0); PG8_BAR; PG8_MMA(1, 0, At, B0); PG8_MMA(1, 1, At, B1); PG8_BAR; PG8_SCHED;
.LBB0_204:
	ds_read_b128 v[128:131], v175
	ds_read_b128 v[132:135], v175 offset:1024
	ds_read_b128 v[160:163], v175 offset:2048
	ds_read_b128 v[164:167], v175 offset:3072
	ds_read_b128 v[168:171], v176
	ds_read_b128 v[180:183], v176 offset:1024
	ds_read_b128 v[184:187], v176 offset:2048
	ds_read_b128 v[188:191], v176 offset:3072
	s_add_u32 s4, s52, 0xfff80080
	s_addc_u32 s21, s53, -1
	s_cmp_eq_u32 s20, 28
	s_cselect_b32 s57, s3, s21
	s_cselect_b32 s56, s5, s4
	s_cselect_b32 s55, s6, s19
	s_cselect_b32 s54, s17, s18
	v_lshl_add_u64 v[224:225], s[52:53], 0, v[154:155]
	s_add_i32 m0, s59, 0xc000
	ds_read_b128 v[192:195], v177
	ds_read_b128 v[196:199], v177 offset:1024
	ds_read_b128 v[200:203], v177 offset:2048
	ds_read_b128 v[204:207], v177 offset:3072
	ds_read_b128 v[208:211], v177 offset:4096
	ds_read_b128 v[212:215], v177 offset:5120
	ds_read_b128 v[216:219], v177 offset:6144
	ds_read_b128 v[220:223], v177 offset:7168
	global_load_lds_dwordx4 v[224:225], off
	v_lshl_add_u64 v[224:225], s[52:53], 0, v[156:157]
	s_add_i32 m0, s59, 0xe000
	s_nop 0
	global_load_lds_dwordx4 v[224:225], off
	s_waitcnt vmcnt(8)
	s_waitcnt lgkmcnt(0)
	s_barrier
	s_waitcnt lgkmcnt(0)
	v_mfma_f32_16x16x32_bf16 v[124:127], v[128:131], v[192:195], v[124:127]
	v_mfma_f32_16x16x32_bf16 v[120:123], v[160:163], v[192:195], v[120:123]
	v_mfma_f32_16x16x32_bf16 v[108:111], v[128:131], v[200:203], v[108:111]
	v_mfma_f32_16x16x32_bf16 v[104:107], v[160:163], v[200:203], v[104:107]
	v_mfma_f32_16x16x32_bf16 v[92:95], v[128:131], v[208:211], v[92:95]
	v_mfma_f32_16x16x32_bf16 v[88:91], v[160:163], v[208:211], v[88:91]
	v_mfma_f32_16x16x32_bf16 v[76:79], v[128:131], v[216:219], v[76:79]
	v_mfma_f32_16x16x32_bf16 v[72:75], v[160:163], v[216:219], v[72:75]
	v_mfma_f32_16x16x32_bf16 v[124:127], v[132:135], v[196:199], v[124:127]
	v_mfma_f32_16x16x32_bf16 v[120:123], v[164:167], v[196:199], v[120:123]
	v_mfma_f32_16x16x32_bf16 v[108:111], v[132:135], v[204:207], v[108:111]
	v_mfma_f32_16x16x32_bf16 v[104:107], v[164:167], v[204:207], v[104:107]
	v_mfma_f32_16x16x32_bf16 v[92:95], v[132:135], v[212:215], v[92:95]
	v_mfma_f32_16x16x32_bf16 v[88:91], v[164:167], v[212:215], v[88:91]
	v_mfma_f32_16x16x32_bf16 v[76:79], v[132:135], v[220:223], v[76:79]
	v_mfma_f32_16x16x32_bf16 v[72:75], v[164:167], v[220:223], v[72:75]
	v_mfma_f32_16x16x32_bf16 v[116:119], v[168:171], v[192:195], v[116:119]
	v_mfma_f32_16x16x32_bf16 v[112:115], v[184:187], v[192:195], v[112:115]
	v_mfma_f32_16x16x32_bf16 v[100:103], v[168:171], v[200:203], v[100:103]
	v_mfma_f32_16x16x32_bf16 v[96:99], v[184:187], v[200:203], v[96:99]
	v_mfma_f32_16x16x32_bf16 v[84:87], v[168:171], v[208:211], v[84:87]
	v_mfma_f32_16x16x32_bf16 v[80:83], v[184:187], v[208:211], v[80:83]
	v_mfma_f32_16x16x32_bf16 v[68:71], v[168:171], v[216:219], v[68:71]
	v_mfma_f32_16x16x32_bf16 v[64:67], v[184:187], v[216:219], v[64:67]
	v_mfma_f32_16x16x32_bf16 v[116:119], v[180:183], v[196:199], v[116:119]
	v_mfma_f32_16x16x32_bf16 v[112:115], v[188:191], v[196:199], v[112:115]
	v_mfma_f32_16x16x32_bf16 v[100:103], v[180:183], v[204:207], v[100:103]
	v_mfma_f32_16x16x32_bf16 v[96:99], v[188:191], v[204:207], v[96:99]
	v_mfma_f32_16x16x32_bf16 v[84:87], v[180:183], v[212:215], v[84:87]
	v_mfma_f32_16x16x32_bf16 v[80:83], v[188:191], v[212:215], v[80:83]
	v_mfma_f32_16x16x32_bf16 v[68:71], v[180:183], v[220:223], v[68:71]
	v_mfma_f32_16x16x32_bf16 v[64:67], v[188:191], v[220:223], v[64:67]
	s_barrier
	s_add_i32 s4, s70, s58
	v_lshl_add_u64 v[224:225], s[54:55], 0, v[138:139]
	s_mov_b32 m0, s4
	ds_read_b128 v[192:195], v177 offset:16384
	ds_read_b128 v[196:199], v177 offset:17408
	ds_read_b128 v[200:203], v177 offset:18432
	ds_read_b128 v[204:207], v177 offset:19456
	ds_read_b128 v[208:211], v177 offset:20480
	ds_read_b128 v[212:215], v177 offset:21504
	ds_read_b128 v[216:219], v177 offset:22528
	ds_read_b128 v[220:223], v177 offset:23552
	global_load_lds_dwordx4 v[224:225], off
	s_add_i32 m0, s4, 0x2000
	s_add_u32 s76, s54, 0x4000
	v_lshl_add_u64 v[224:225], s[54:55], 0, v[142:143]
	s_addc_u32 s77, s55, 0
	s_add_i32 s4, s71, s58
	global_load_lds_dwordx4 v[224:225], off
	v_lshl_add_u64 v[224:225], s[76:77], 0, v[138:139]
	s_mov_b32 m0, s4
	v_lshl_add_u64 v[226:227], s[56:57], 0, v[140:141]
	global_load_lds_dwordx4 v[224:225], off
	v_lshl_add_u64 v[224:225], s[76:77], 0, v[142:143]
	s_add_i32 m0, s4, 0x2000
	s_nop 0
	global_load_lds_dwordx4 v[224:225], off
	v_lshl_add_u64 v[224:225], s[56:57], 0, v[136:137]
	s_mov_b32 m0, s59
	s_nop 0
	global_load_lds_dwordx4 v[224:225], off
	s_mov_b32 m0, s60
	s_nop 0
	global_load_lds_dwordx4 v[226:227], off
	s_waitcnt vmcnt(8)
	s_waitcnt lgkmcnt(0)
	s_barrier
; #define PG8_STAGE(bufoff, gbase, voff) do { _Pragma("unroll") for (int _i = 0; _i < 2; ++_i) \
;         __builtin_amdgcn_global_load_lds((const unsigned*)((const char*)(gbase) + (voff)[_i]), (PG8_LAS unsigned*)(lds + (bufoff) + ldsw + _i * 8192), 16, 0, 0); } while (0)
; #define PG8_STAGE_A(bufoff, base, h, isnext) do { if constexpr (Sched::GATHER) { unsigned vv_[2] = {(isnext) ? vn[h][0] : vc[h][0], (isnext) ? vn[h][1] : vc[h][1]}; PG8_STAGE(bufoff, base, vv_); } else { PG8_STAGE(bufoff, (base) + (h) * hstep, voffA); } } while (0)
; #define PG8_LDA(dst, b, h) do { _Pragma("unroll") for (int m = 0; m < 4; ++m) _Pragma("unroll") for (int k = 0; k < 2; ++k) dst[m][k] = *(const PG8_LAS bf16x8*)(lds + PG8_SA(b, h) + aoff + m * 2048 + k * 1024); } while (0)
; #define PG8_LDB(dst, b, h) do { _Pragma("unroll") for (int n = 0; n < 2; ++n) _Pragma("unroll") for (int k = 0; k < 2; ++k) dst[n][k] = *(const PG8_LAS bf16x8*)(lds + PG8_SB(b, h) + boff + n * 2048 + k * 1024); } while (0)
; #define PG8_MMA(ai, bj, At, Bt) do { __builtin_amdgcn_s_setprio(1); _Pragma("unroll") for (int m = 0; m < 4; ++m) _Pragma("unroll") for (int n = 0; n < 2; ++n) _Pragma("unroll") for (int k = 0; k < 2; ++k) \
;         acc[ai][bj][m][n] = __builtin_amdgcn_mfma_f32_16x16x32_bf16(Bt[n][k], At[m][k], acc[ai][bj][m][n], 0, 0, 0); __builtin_amdgcn_s_setprio(0); } while (0)
; #define PG8_WAIT_V(n) asm volatile("s_waitcnt vmcnt(" #n ")" ::: "memory")
; #define PG8_WAIT_L(n) asm volatile("s_waitcnt lgkmcnt(" #n ")" ::: "memory")
; template <class Epi, class Sched, bool ALIGN_EPI = false, bool SP2 = false>
; __device__ __forceinline__ void gemm_phase(PG8_LAS unsigned char* lds, const Gemm g, const Sched& S, const Epi& E, const int tid_in) {
;     ...
;             PG8_WAIT_V(8); PG8_WAIT_L(0); PG8_BAR; PG8_MMA(0, 0, At, B0); PG8_MMA(0, 1, At, B1); PG8_BAR; PG8_SCHED;
;             PG8_LDA(At, 0, 1); PG8_STAGE(PG8_SB(0, 0), b2, voffB); PG8_STAGE(PG8_SB(0, 1), b2 + hstepB, voffB); PG8_STAGE_A(PG8_SA(0, 0), a2, 0, last);
;             PG8_WAIT_V(8); PG8_WAIT_L(0); PG8_BAR; PG8_MMA(1, 0, At, B0); PG8_MMA(1, 1, At, B1); PG8_BAR; PG8_SCHED;
;             PG8_LDB(B0, 1, 0); PG8_LDB(B1, 1, 1); PG8_SCHED; PG8_LDA(At, 1, 0); PG8_STAGE_A(PG8_SA(0, 1), a2, 1, last);
;             PG8_WAIT_V(8); PG8_WAIT_L(0); PG8_BAR; PG8_MMA(0, 0, At, B0); PG8_MMA(0, 1, At, B1); PG8_BAR; PG8_SCHED;
	s_waitcnt lgkmcnt(0)
	v_mfma_f32_16x16x32_bf16 v[60:63], v[128:131], v[192:195], v[60:63]
	v_mfma_f32_16x16x32_bf16 v[56:59], v[160:163], v[192:195], v[56:59]
	v_mfma_f32_16x16x32_bf16 v[44:47], v[128:131], v[200:203], v[44:47]
	v_mfma_f32_16x16x32_bf16 v[40:43], v[160:163], v[200:203], v[40:43]
	v_mfma_f32_16x16x32_bf16 v[28:31], v[128:131], v[208:211], v[28:31]
	v_mfma_f32_16x16x32_bf16 v[24:27], v[160:163], v[208:211], v[24:27]
	v_mfma_f32_16x16x32_bf16 v[12:15], v[128:131], v[216:219], v[12:15]
	v_mfma_f32_16x16x32_bf16 v[8:11], v[160:163], v[216:219], v[8:11]
	v_mfma_f32_16x16x32_bf16 v[60:63], v[132:135], v[196:199], v[60:63]
	v_mfma_f32_16x16x32_bf16 v[56:59], v[164:167], v[196:199], v[56:59]
	v_mfma_f32_16x16x32_bf16 v[44:47], v[132:135], v[204:207], v[44:47]
	v_mfma_f32_16x16x32_bf16 v[40:43], v[164:167], v[204:207], v[40:43]
	v_mfma_f32_16x16x32_bf16 v[28:31], v[132:135], v[212:215], v[28:31]
	v_mfma_f32_16x16x32_bf16 v[24:27], v[164:167], v[212:215], v[24:27]
	v_mfma_f32_16x16x32_bf16 v[12:15], v[132:135], v[220:223], v[12:15]
	v_mfma_f32_16x16x32_bf16 v[8:11], v[164:167], v[220:223], v[8:11]
	v_mfma_f32_16x16x32_bf16 v[52:55], v[168:171], v[192:195], v[52:55]
	v_mfma_f32_16x16x32_bf16 v[48:51], v[184:187], v[192:195], v[48:51]
	v_mfma_f32_16x16x32_bf16 v[36:39], v[168:171], v[200:203], v[36:39]
	v_mfma_f32_16x16x32_bf16 v[32:35], v[184:187], v[200:203], v[32:35]
	v_mfma_f32_16x16x32_bf16 v[20:23], v[168:171], v[208:211], v[20:23]
	v_mfma_f32_16x16x32_bf16 v[16:19], v[184:187], v[208:211], v[16:19]
	v_mfma_f32_16x16x32_bf16 v[4:7], v[168:171], v[216:219], v[4:7]
	v_mfma_f32_16x16x32_bf16 v[0:3], v[184:187], v[216:219], v[0:3]
	v_mfma_f32_16x16x32_bf16 v[52:55], v[180:183], v[196:199], v[52:55]
	v_mfma_f32_16x16x32_bf16 v[48:51], v[188:191], v[196:199], v[48:51]
	v_mfma_f32_16x16x32_bf16 v[36:39], v[180:183], v[204:207], v[36:39]
	v_mfma_f32_16x16x32_bf16 v[32:35], v[188:191], v[204:207], v[32:35]
	v_mfma_f32_16x16x32_bf16 v[20:23], v[180:183], v[212:215], v[20:23]
	v_mfma_f32_16x16x32_bf16 v[16:19], v[188:191], v[212:215], v[16:19]
	v_mfma_f32_16x16x32_bf16 v[4:7], v[180:183], v[220:223], v[4:7]
	v_mfma_f32_16x16x32_bf16 v[0:3], v[188:191], v[220:223], v[0:3]
	s_barrier
	s_add_i32 s4, 0, 0x18000
	s_add_i32 s21, 0, 0x1c000
	v_add_u32_e32 v164, s4, v173
	v_add_u32_e32 v179, s21, v173
	ds_read_b128 v[128:131], v164
	ds_read_b128 v[132:135], v164 offset:1024
	ds_read_b128 v[160:163], v164 offset:2048
	ds_read_b128 v[164:167], v164 offset:3072
	ds_read_b128 v[168:171], v179
	ds_read_b128 v[180:183], v179 offset:1024
	ds_read_b128 v[184:187], v179 offset:2048
	ds_read_b128 v[188:191], v179 offset:3072
	s_add_u32 s56, s56, 0x80000
	s_addc_u32 s57, s57, 0
	s_mov_b32 m0, s61
	v_lshl_add_u64 v[228:229], s[56:57], 0, v[136:137]
	ds_read_b128 v[192:195], v177 offset:32768
	ds_read_b128 v[196:199], v177 offset:33792
	ds_read_b128 v[200:203], v177 offset:34816
	ds_read_b128 v[204:207], v177 offset:35840
	ds_read_b128 v[208:211], v177 offset:36864
	ds_read_b128 v[212:215], v177 offset:37888
	ds_read_b128 v[216:219], v177 offset:38912
	ds_read_b128 v[220:223], v177 offset:39936
	global_load_lds_dwordx4 v[228:229], off
	v_lshl_add_u64 v[228:229], s[56:57], 0, v[140:141]
	s_mov_b32 m0, s62
	s_nop 0
	global_load_lds_dwordx4 v[228:229], off
	s_waitcnt vmcnt(8)
	s_waitcnt lgkmcnt(0)
	s_barrier
	s_waitcnt lgkmcnt(0)
	v_mfma_f32_16x16x32_bf16 v[124:127], v[128:131], v[192:195], v[124:127]
	v_mfma_f32_16x16x32_bf16 v[120:123], v[160:163], v[192:195], v[120:123]
	v_mfma_f32_16x16x32_bf16 v[108:111], v[128:131], v[200:203], v[108:111]
	v_mfma_f32_16x16x32_bf16 v[104:107], v[160:163], v[200:203], v[104:107]
	v_mfma_f32_16x16x32_bf16 v[92:95], v[128:131], v[208:211], v[92:95]
	v_mfma_f32_16x16x32_bf16 v[88:91], v[160:163], v[208:211], v[88:91]
	v_mfma_f32_16x16x32_bf16 v[76:79], v[128:131], v[216:219], v[76:79]
	v_mfma_f32_16x16x32_bf16 v[72:75], v[160:163], v[216:219], v[72:75]
	v_mfma_f32_16x16x32_bf16 v[124:127], v[132:135], v[196:199], v[124:127]
	v_mfma_f32_16x16x32_bf16 v[120:123], v[164:167], v[196:199], v[120:123]
	v_mfma_f32_16x16x32_bf16 v[108:111], v[132:135], v[204:207], v[108:111]
	v_mfma_f32_16x16x32_bf16 v[104:107], v[164:167], v[204:207], v[104:107]
	v_mfma_f32_16x16x32_bf16 v[92:95], v[132:135], v[212:215], v[92:95]
	v_mfma_f32_16x16x32_bf16 v[88:91], v[164:167], v[212:215], v[88:91]
	v_mfma_f32_16x16x32_bf16 v[76:79], v[132:135], v[220:223], v[76:79]
	v_mfma_f32_16x16x32_bf16 v[72:75], v[164:167], v[220:223], v[72:75]
	v_mfma_f32_16x16x32_bf16 v[116:119], v[168:171], v[192:195], v[116:119]
	v_mfma_f32_16x16x32_bf16 v[112:115], v[184:187], v[192:195], v[112:115]
	v_mfma_f32_16x16x32_bf16 v[100:103], v[168:171], v[200:203], v[100:103]
	v_mfma_f32_16x16x32_bf16 v[96:99], v[184:187], v[200:203], v[96:99]
	v_mfma_f32_16x16x32_bf16 v[84:87], v[168:171], v[208:211], v[84:87]
	v_mfma_f32_16x16x32_bf16 v[80:83], v[184:187], v[208:211], v[80:83]
	v_mfma_f32_16x16x32_bf16 v[68:71], v[168:171], v[216:219], v[68:71]
	v_mfma_f32_16x16x32_bf16 v[64:67], v[184:187], v[216:219], v[64:67]
	v_mfma_f32_16x16x32_bf16 v[116:119], v[180:183], v[196:199], v[116:119]
	v_mfma_f32_16x16x32_bf16 v[112:115], v[188:191], v[196:199], v[112:115]
	v_mfma_f32_16x16x32_bf16 v[100:103], v[180:183], v[204:207], v[100:103]
	v_mfma_f32_16x16x32_bf16 v[96:99], v[188:191], v[204:207], v[96:99]
	v_mfma_f32_16x16x32_bf16 v[84:87], v[180:183], v[212:215], v[84:87]
	v_mfma_f32_16x16x32_bf16 v[80:83], v[188:191], v[212:215], v[80:83]
	v_mfma_f32_16x16x32_bf16 v[68:71], v[180:183], v[220:223], v[68:71]
	v_mfma_f32_16x16x32_bf16 v[64:67], v[188:191], v[220:223], v[64:67]
	s_barrier
; #define PG8_STAGE(bufoff, gbase, voff) do { _Pragma("unroll") for (int _i = 0; _i < 2; ++_i) \
;         __builtin_amdgcn_global_load_lds((const unsigned*)((const char*)(gbase) + (voff)[_i]), (PG8_LAS unsigned*)(lds + (bufoff) + ldsw + _i * 8192), 16, 0, 0); } while (0)
; #define PG8_STAGE_A(bufoff, base, h, isnext) do { if constexpr (Sched::GATHER) { unsigned vv_[2] = {(isnext) ? vn[h][0] : vc[h][0], (isnext) ? vn[h][1] : vc[h][1]}; PG8_STAGE(bufoff, base, vv_); } else { PG8_STAGE(bufoff, (base) + (h) * hstep, voffA); } } while (0)
; #define PG8_LDA(dst, b, h) do { _Pragma("unroll") for (int m = 0; m < 4; ++m) _Pragma("unroll") for (int k = 0; k < 2; ++k) dst[m][k] = *(const PG8_LAS bf16x8*)(lds + PG8_SA(b, h) + aoff + m * 2048 + k * 1024); } while (0)
; #define PG8_MMA(ai, bj, At, Bt) do { __builtin_amdgcn_s_setprio(1); _Pragma("unroll") for (int m = 0; m < 4; ++m) _Pragma("unroll") for (int n = 0; n < 2; ++n) _Pragma("unroll") for (int k = 0; k < 2; ++k) \
;         acc[ai][bj][m][n] = __builtin_amdgcn_mfma_f32_16x16x32_bf16(Bt[n][k], At[m][k], acc[ai][bj][m][n], 0, 0, 0); __builtin_amdgcn_s_setprio(0); } while (0)
; #define PG8_WAIT_V(n) asm volatile("s_waitcnt vmcnt(" #n ")" ::: "memory")
; #define PG8_WAIT_L(n) asm volatile("s_waitcnt lgkmcnt(" #n ")" ::: "memory")
; #define PG8_BAR __builtin_amdgcn_s_barrier()
; #define PG8_SCHED __builtin_amdgcn_sched_barrier(0)
; template <class Epi, class Sched, bool ALIGN_EPI = false, bool SP2 = false>
; __device__ __forceinline__ void gemm_phase(PG8_LAS unsigned char* lds, const Gemm g, const Sched& S, const Epi& E, const int tid_in) {
;     ...
;             PG8_WAIT_V(8); PG8_WAIT_L(0); PG8_BAR; PG8_MMA(0, 0, At, B0); PG8_MMA(0, 1, At, B1); PG8_BAR; PG8_SCHED;
;             PG8_LDA(At, 1, 1); PG8_STAGE(PG8_SB(1, 0), b3, voffB); PG8_STAGE(PG8_SB(1, 1), b3 + hstepB, voffB); PG8_STAGE_A(PG8_SA(1, 0), a3, 0, last);
;             PG8_WAIT_V(8); PG8_WAIT_L(0); PG8_BAR; PG8_MMA(1, 0, At, B0); PG8_MMA(1, 1, At, B1); PG8_BAR; PG8_SCHED;
	s_add_u32 s56, s54, 0x8000
	s_addc_u32 s57, s55, 0
	s_add_i32 s4, s4, s58
	v_lshl_add_u64 v[228:229], s[56:57], 0, v[138:139]
	s_mov_b32 m0, s4
	ds_read_b128 v[192:195], v177 offset:49152
	ds_read_b128 v[196:199], v177 offset:50176
	ds_read_b128 v[200:203], v177 offset:51200
	ds_read_b128 v[204:207], v177 offset:52224
	ds_read_b128 v[208:211], v177 offset:53248
	ds_read_b128 v[212:215], v177 offset:54272
	ds_read_b128 v[216:219], v177 offset:55296
	ds_read_b128 v[220:223], v177 offset:56320
	global_load_lds_dwordx4 v[228:229], off
	s_add_i32 m0, s4, 0x2000
	s_add_u32 s54, s54, 0xc000
	v_lshl_add_u64 v[228:229], s[56:57], 0, v[142:143]
	s_addc_u32 s55, s55, 0
	s_add_i32 s4, s21, s58
	global_load_lds_dwordx4 v[228:229], off
	v_lshl_add_u64 v[228:229], s[54:55], 0, v[138:139]
	s_mov_b32 m0, s4
	v_lshl_add_u64 v[224:225], v[224:225], 0, s[12:13]
	global_load_lds_dwordx4 v[228:229], off
	v_lshl_add_u64 v[228:229], s[54:55], 0, v[142:143]
	s_add_i32 m0, s4, 0x2000
	s_nop 0
	global_load_lds_dwordx4 v[228:229], off
	s_mov_b32 m0, s68
	s_nop 0
	global_load_lds_dwordx4 v[224:225], off
	v_lshl_add_u64 v[224:225], v[226:227], 0, s[12:13]
	s_mov_b32 m0, s69
	s_nop 0
	global_load_lds_dwordx4 v[224:225], off
	s_waitcnt vmcnt(8)
	s_waitcnt lgkmcnt(0)
	s_barrier
	s_waitcnt lgkmcnt(0)
	v_mfma_f32_16x16x32_bf16 v[60:63], v[128:131], v[192:195], v[60:63]
	v_mfma_f32_16x16x32_bf16 v[56:59], v[160:163], v[192:195], v[56:59]
	v_mfma_f32_16x16x32_bf16 v[44:47], v[128:131], v[200:203], v[44:47]
	v_mfma_f32_16x16x32_bf16 v[40:43], v[160:163], v[200:203], v[40:43]
	v_mfma_f32_16x16x32_bf16 v[28:31], v[128:131], v[208:211], v[28:31]
	v_mfma_f32_16x16x32_bf16 v[24:27], v[160:163], v[208:211], v[24:27]
	v_mfma_f32_16x16x32_bf16 v[12:15], v[128:131], v[216:219], v[12:15]
	v_mfma_f32_16x16x32_bf16 v[8:11], v[160:163], v[216:219], v[8:11]
	v_mfma_f32_16x16x32_bf16 v[60:63], v[132:135], v[196:199], v[60:63]
	v_mfma_f32_16x16x32_bf16 v[56:59], v[164:167], v[196:199], v[56:59]
	v_mfma_f32_16x16x32_bf16 v[44:47], v[132:135], v[204:207], v[44:47]
	v_mfma_f32_16x16x32_bf16 v[40:43], v[164:167], v[204:207], v[40:43]
	v_mfma_f32_16x16x32_bf16 v[28:31], v[132:135], v[212:215], v[28:31]
	v_mfma_f32_16x16x32_bf16 v[24:27], v[164:167], v[212:215], v[24:27]
	v_mfma_f32_16x16x32_bf16 v[12:15], v[132:135], v[220:223], v[12:15]
	v_mfma_f32_16x16x32_bf16 v[8:11], v[164:167], v[220:223], v[8:11]
	v_mfma_f32_16x16x32_bf16 v[52:55], v[168:171], v[192:195], v[52:55]
	v_mfma_f32_16x16x32_bf16 v[48:51], v[184:187], v[192:195], v[48:51]
	v_mfma_f32_16x16x32_bf16 v[36:39], v[168:171], v[200:203], v[36:39]
	v_mfma_f32_16x16x32_bf16 v[32:35], v[184:187], v[200:203], v[32:35]
	v_mfma_f32_16x16x32_bf16 v[20:23], v[168:171], v[208:211], v[20:23]
	v_mfma_f32_16x16x32_bf16 v[16:19], v[184:187], v[208:211], v[16:19]
	v_mfma_f32_16x16x32_bf16 v[4:7], v[168:171], v[216:219], v[4:7]
	v_mfma_f32_16x16x32_bf16 v[0:3], v[184:187], v[216:219], v[0:3]
	v_mfma_f32_16x16x32_bf16 v[52:55], v[180:183], v[196:199], v[52:55]
	v_mfma_f32_16x16x32_bf16 v[48:51], v[188:191], v[196:199], v[48:51]
	v_mfma_f32_16x16x32_bf16 v[36:39], v[180:183], v[204:207], v[36:39]
	v_mfma_f32_16x16x32_bf16 v[32:35], v[188:191], v[204:207], v[32:35]
	v_mfma_f32_16x16x32_bf16 v[20:23], v[180:183], v[212:215], v[20:23]
	v_mfma_f32_16x16x32_bf16 v[16:19], v[188:191], v[212:215], v[16:19]
	v_mfma_f32_16x16x32_bf16 v[4:7], v[180:183], v[220:223], v[4:7]
	v_mfma_f32_16x16x32_bf16 v[0:3], v[188:191], v[220:223], v[0:3]
	s_barrier
	s_add_i32 s20, s20, 2
	s_add_u32 s18, s18, 0x10000
	s_addc_u32 s19, s19, 0
	s_add_u32 s52, s52, 0x100
	s_addc_u32 s53, s53, 0
	s_cmp_gt_u32 s20, 29
	s_cbranch_scc0 .LBB0_204
	s_and_b64 vcc, exec, s[26:27]
	s_cbranch_vccz .LBB0_249
	s_barrier
	v_lshl_add_u32 v160, s2, 8, v172
	s_cmp_gt_i32 s50, 15
	s_mov_b64 s[2:3], -1
	s_cbranch_scc1 .LBB0_250

; #define PG8_BAR __builtin_amdgcn_s_barrier()
;     __host__ __device__ bool next(int i, Unit& u) const {
;         if (i + i0 >= imax) return false; const long L = (long)(i + i0) * G + c; if (L >= nwg) return false;
;         int wgid = (int)L; { const int q = nwg / NXCD, r = nwg % NXCD, xcd = wgid % NXCD, off = wgid / NXCD; wgid = (xcd < r ? xcd * (q + 1) : r * (q + 1) + (xcd - r) * q) + off; }
;         const int nig = WGM * nN, gid = wgid / nig, fm = gid * WGM, gsz = (nM - fm) < WGM ? (nM - fm) : WGM;
;         u.pm = fm + ((wgid % nig) % gsz); u.pn = (wgid % nig) / gsz; u.e = 0; return true;
; template <class Epi, class Sched, bool ALIGN_EPI = false, bool SP2 = false>
; __device__ __forceinline__ void gemm_phase(PG8_LAS unsigned char* lds, const Gemm g, const Sched& S, const Epi& E, const int tid_in) {
;     ...
;     Unit cur, nxt; int ui = 0;
;     if (!S.next(0, cur)) return;
;     f32x4 acc[2][2][4][2];
; #pragma unroll
;     for (int a = 0; a < 2; ++a)
; #pragma unroll
;         for (int b = 0; b < 2; ++b)
; #pragma unroll
;             for (int m = 0; m < 4; ++m)
; #pragma unroll
;                 for (int n = 0; n < 2; ++n) acc[a][b][m][n] = (f32x4){0.f, 0.f, 0.f, 0.f};
;     bf16x8 At[4][2], B0[2][2], B1[2][2];
;     const char* cA = (const char*)g.A + (Sched::GATHER ? (size_t)0 : (size_t)cur.pm * tstep); if constexpr (Sched::GATHER) PG8_GFILL(vc, 0); const char* cB = (const char*)g.Bt + (size_t)cur.pn * tstep + (size_t)cur.e * g.estride;
;     S.a_ready(cur);
;     if constexpr (SP2) {
;         PG8_STAGE(PG8_SB(0, 0), cB, voffB); PG8_STAGE(PG8_SB(0, 1), cB + hstepB, voffB); PG8_STAGE_A(PG8_SA(0, 0), cA, 0, false); PG8_STAGE_A(PG8_SA(0, 1), cA, 1, false);
;         if (wr == 1) PG8_BAR;
;         PG8_WAIT_V(2); PG8_BAR;
;         PG8_STAGE(PG8_SB(1, 0), cB + kstepB, voffB); PG8_STAGE_A(PG8_SA(1, 0), cA + kstep, 0, false); PG8_STAGE(PG8_SB(1, 1), cB + hstepB + kstepB, voffB);
;         PG8_WAIT_V(6); PG8_BAR;
;     } else {
;         PG8_STAGE(PG8_SB(0, 0), cB, voffB); PG8_STAGE_A(PG8_SA(0, 0), cA, 0, false); PG8_STAGE(PG8_SB(0, 1), cB + hstepB, voffB); PG8_STAGE_A(PG8_SA(0, 1), cA, 1, false);
;         if (wr == 1) PG8_BAR;
;         PG8_WAIT_V(4); PG8_BAR;
;         PG8_STAGE(PG8_SB(1, 0), cB + kstepB, voffB); PG8_STAGE_A(PG8_SA(1, 0), cA + kstep, 0, false); PG8_STAGE(PG8_SB(1, 1), cB + hstepB + kstepB, voffB);
;         PG8_WAIT_V(6); PG8_BAR;
.LBB0_767:
	s_cmp_lt_i32 s84, 6
	s_cselect_b64 s[2:3], -1, 0
	s_cmp_gt_i32 s85, 5
	s_cselect_b64 s[4:5], -1, 0
	s_and_b64 s[2:3], s[2:3], s[4:5]
	s_andn2_b64 vcc, exec, s[2:3]
	s_cbranch_vccnz .LBB0_845
	s_mov_b64 s[2:3], s[0:1]
	s_waitcnt vmcnt(0)
	v_mbcnt_lo_u32_b32 v1, -1, 0
	v_mbcnt_hi_u32_b32 v1, -1, v1
	s_cmpk_gt_i32 s81, 0xff
	v_add_u32_e32 v0, s33, v1
	s_nop 0
	v_readfirstlane_b32 s4, v0
	s_cbranch_scc1 .LBB0_795
	v_lshlrev_b32_e32 v2, 4, v0
	v_add_u32_e32 v3, 0x2000, v2
	s_waitcnt lgkmcnt(0)
	v_ashrrev_i32_e32 v4, 31, v3
	v_lshrrev_b32_e32 v4, 22, v4
	v_add_u32_e32 v4, v3, v4
	v_ashrrev_i32_e32 v6, 10, v4
	v_mul_i32_i24_e32 v4, 0x400, v6
	v_sub_u32_e32 v3, v3, v4
	v_lshrrev_b32_e32 v4, 4, v3
	v_bitop3_b32 v3, v4, v3, 32 bitop3:0x6c
	v_ashrrev_i32_e32 v4, 31, v3
	v_lshrrev_b32_e32 v4, 26, v4
	v_add_u32_e32 v4, v3, v4
	v_lshlrev_b32_e32 v5, 3, v6
	v_ashrrev_i32_e32 v7, 6, v4
	v_and_b32_e32 v5, -16, v5
	v_add_u32_e32 v5, v7, v5
	s_load_dwordx2 s[12:13], s[2:3], 0xc8
	v_and_b32_e32 v8, 3, v7
	s_mov_b32 s2, 0x1ffffe0
	v_lshrrev_b32_e32 v9, 2, v5
	v_lshlrev_b32_e32 v10, 1, v5
	v_and_b32_e32 v4, 0xc0, v4
	v_and_or_b32 v8, v5, s2, v8
	v_and_b32_e32 v9, 4, v9
	v_and_b32_e32 v10, 24, v10
	v_sub_u32_e32 v3, v3, v4
	v_mov_b32_e32 v4, 1
	v_or3_b32 v9, v8, v9, v10
	v_lshlrev_b32_e32 v8, 5, v6
	v_ashrrev_i16_sdwa v3, v4, sext(v3) dst_sel:DWORD dst_unused:UNUSED_PAD src0_sel:DWORD src1_sel:BYTE_0
	v_and_b32_e32 v10, 32, v8
	v_bfe_i32 v8, v3, 0, 16
	v_add_lshl_u32 v3, v10, v8, 1
	v_lshl_add_u32 v132, v9, 7, v3
	v_lshl_add_u32 v134, v5, 13, v3
	v_bfe_i32 v3, v0, 27, 1
	v_lshrrev_b32_e32 v3, 22, v3
	v_add_u32_e32 v3, v2, v3
	v_and_b32_e32 v3, 0xfffffc00, v3
	v_sub_u32_e32 v2, v2, v3
	v_lshrrev_b32_e32 v3, 4, v2
	v_ashrrev_i32_e32 v5, 31, v0
	v_bitop3_b32 v2, v3, v2, 32 bitop3:0x6c
	v_lshrrev_b32_e32 v5, 26, v5
	v_ashrrev_i32_e32 v3, 31, v2
	v_add_u32_e32 v0, v0, v5
	s_waitcnt lgkmcnt(0)
	s_add_u32 s17, s12, 0x4c000000
	v_lshrrev_b32_e32 v3, 26, v3
	v_ashrrev_i32_e32 v10, 6, v0
	s_addc_u32 s54, s13, 0
	v_add_u32_e32 v3, v2, v3
	v_lshlrev_b32_e32 v0, 3, v10
	s_add_u32 s55, s12, 0x4800000
	v_ashrrev_i32_e32 v9, 6, v3
	v_and_b32_e32 v0, -16, v0
	s_addc_u32 s56, s13, 0
	v_add_u32_e32 v0, v9, v0
	v_and_b32_e32 v5, 3, v9
	s_ashr_i32 s58, s81, 31
	v_and_or_b32 v5, v0, s2, v5
	s_lshr_b32 s2, s58, 29
	s_add_i32 s2, s81, s2
	s_and_b32 s3, s2, -8
	s_ashr_i32 s14, s4, 6
	s_sub_i32 s3, s81, s3
	s_ashr_i32 s5, s4, 8
	s_lshl_b32 s57, s14, 10
	s_lshl_b32 s7, s3, 5
	s_ashr_i32 s2, s2, 3
	s_mul_i32 s6, s3, 33
	s_cmp_lt_i32 s3, 0
	s_cselect_b32 s3, s6, s7
	s_add_i32 s2, s3, s2
	s_ashr_i32 s3, s2, 31
	s_lshr_b32 s3, s3, 26
	s_add_i32 s3, s2, s3
	v_lshrrev_b32_e32 v11, 2, v0
	v_lshlrev_b32_e32 v12, 1, v0
	v_and_b32_e32 v3, 0xc0, v3
	s_ashr_i32 s6, s3, 6
	v_and_b32_e32 v11, 4, v11
	v_and_b32_e32 v12, 24, v12
	v_sub_u32_e32 v2, v2, v3
	s_lshl_b32 s6, s6, 3
	v_or3_b32 v5, v5, v11, v12
	v_lshlrev_b32_e32 v11, 5, v10
	v_ashrrev_i16_sdwa v2, v4, sext(v2) dst_sel:DWORD dst_unused:UNUSED_PAD src0_sel:DWORD src1_sel:BYTE_0
	s_sub_i32 s7, 32, s6
	v_and_b32_e32 v12, 32, v11
	v_bfe_i32 v11, v2, 0, 16
	s_min_u32 s7, s7, 8
	s_andn2_b32 s3, s3, 63
	v_add_lshl_u32 v2, v12, v11, 1
	s_sub_i32 s8, s2, s3
	v_cvt_f32_ubyte0_e32 v4, s7
	v_lshl_add_u32 v136, v5, 7, v2
	v_cvt_f32_i32_e32 v3, s8
	v_rcp_iflag_f32_e32 v5, v4
	v_lshl_add_u32 v138, v0, 13, v2
	s_ashr_i32 s2, s8, 30
	s_or_b32 s9, s2, 1
	v_mul_f32_e32 v0, v3, v5
	v_trunc_f32_e32 v0, v0
	v_fma_f32 v2, -v0, v4, v3
	v_cvt_i32_f32_e32 v0, v0
	v_cmp_ge_f32_e64 s[2:3], |v2|, v4
	s_and_b64 s[2:3], s[2:3], exec
	s_cselect_b32 s2, s9, 0
	v_readfirstlane_b32 s3, v0
	s_add_i32 s26, s3, s2
	s_mul_i32 s2, s26, s7
	s_sub_i32 s2, s8, s2
	s_sext_i32_i8 s2, s2
	s_add_i32 s2, s6, s2
	s_ashr_i32 s3, s2, 31
	s_bfe_i64 s[8:9], s[26:27], 0x80000
	s_lshl_b64 s[6:7], s[2:3], 21
	s_lshl_b64 s[8:9], s[8:9], 21
	s_add_u32 s42, s55, s8
	s_addc_u32 s43, s56, s9
	s_add_i32 s59, s57, 0
	s_add_i32 m0, s59, 0x10000
	v_mov_b32_e32 v0, 0
	global_load_lds_dwordx4 v136, s[42:43]
	s_add_i32 m0, s59, 0x12000
	s_add_u32 s8, s42, 0x4000
	global_load_lds_dwordx4 v132, s[42:43]
	s_addc_u32 s9, s43, 0
	s_add_i32 m0, s59, 0x14000
	v_mov_b32_e32 v139, v0
	global_load_lds_dwordx4 v136, s[8:9]
	s_add_i32 m0, s59, 0x16000
	s_add_u32 s44, s17, s6
	s_addc_u32 s45, s54, s7
	s_add_i32 s60, s59, 0x2000
	global_load_lds_dwordx4 v132, s[8:9]
	s_mov_b32 m0, s59
	s_add_u32 s6, s44, 0x100000
	global_load_lds_dwordx4 v138, s[44:45]
	s_mov_b32 m0, s60
	s_addc_u32 s7, s45, 0
	s_add_i32 s61, s59, 0x4000
	global_load_lds_dwordx4 v134, s[44:45]
	s_mov_b32 m0, s61
	s_add_i32 s62, s59, 0x6000
	global_load_lds_dwordx4 v138, s[6:7]
	s_mov_b32 m0, s62
	v_mov_b32_e32 v135, v0
	global_load_lds_dwordx4 v134, s[6:7]
	s_cmp_eq_u32 s5, 1
	s_mov_b32 s3, 0
	v_mov_b32_e32 v137, v0
	v_mov_b32_e32 v133, v0
	s_mov_b64 s[6:7], 0x4000
	v_lshl_add_u64 v[4:5], s[44:45], 0, v[138:139]
	v_lshl_add_u64 v[2:3], s[44:45], 0, v[134:135]
	s_cselect_b64 s[8:9], -1, 0
	s_cmp_lg_u32 s5, 1
	s_movk_i32 s63, 0x4000
	s_setprio 0
	s_cbranch_scc1 .LBB0_771
	s_setprio 1
	s_barrier

; #define PG8_STAGE(bufoff, gbase, voff) do { _Pragma("unroll") for (int _i = 0; _i < 2; ++_i) \
;         __builtin_amdgcn_global_load_lds((const unsigned*)((const char*)(gbase) + (voff)[_i]), (PG8_LAS unsigned*)(lds + (bufoff) + ldsw + _i * 8192), 16, 0, 0); } while (0)
; #define PG8_STAGE_A(bufoff, base, h, isnext) do { if constexpr (Sched::GATHER) { unsigned vv_[2] = {(isnext) ? vn[h][0] : vc[h][0], (isnext) ? vn[h][1] : vc[h][1]}; PG8_STAGE(bufoff, base, vv_); } else { PG8_STAGE(bufoff, (base) + (h) * hstep, voffA); } } while (0)
; #define PG8_LDA(dst, b, h) do { _Pragma("unroll") for (int m = 0; m < 4; ++m) _Pragma("unroll") for (int k = 0; k < 2; ++k) dst[m][k] = *(const PG8_LAS bf16x8*)(lds + PG8_SA(b, h) + aoff + m * 2048 + k * 1024); } while (0)
; #define PG8_LDB(dst, b, h) do { _Pragma("unroll") for (int n = 0; n < 2; ++n) _Pragma("unroll") for (int k = 0; k < 2; ++k) dst[n][k] = *(const PG8_LAS bf16x8*)(lds + PG8_SB(b, h) + boff + n * 2048 + k * 1024); } while (0)
; #define PG8_WAIT_V(n) asm volatile("s_waitcnt vmcnt(" #n ")" ::: "memory")
; #define PG8_WAIT_L(n) asm volatile("s_waitcnt lgkmcnt(" #n ")" ::: "memory")
; #define PG8_BAR __builtin_amdgcn_s_barrier()
; #define PG8_SCHED __builtin_amdgcn_sched_barrier(0)
; template <class Epi, class Sched, bool ALIGN_EPI = false, bool SP2 = false>
; __device__ __forceinline__ void gemm_phase(PG8_LAS unsigned char* lds, const Gemm g, const Sched& S, const Epi& E, const int tid_in) {
;     ...
;             const bool last = (t == nt - 2);
;             const char* a1 = cA + (size_t)(t + 1) * kstep;
;             const char* a2 = last ? nA : cA + (size_t)(t + 2) * kstep; const char* b2 = last ? nB : cB + (size_t)(t + 2) * kstepB;
;             const char* a3 = a2 + kstep; const char* b3 = b2 + kstepB;
;             if (last && has_next) S.a_ready(nxt);
;             if constexpr (SP2) {
;             PG8_LDB(B0, 0, 0); PG8_LDB(B1, 0, 1); PG8_SCHED; PG8_LDA(At, 0, 0); PG8_STAGE_A(PG8_SA(1, 1), a1, 1, false);
;             PG8_WAIT_V(8); PG8_WAIT_L(0); PG8_BAR; PG8_MMA(0, 0, At, B0); PG8_MMA(0, 1, At, B1); PG8_BAR; PG8_SCHED;
;             PG8_LDA(At, 0, 1); PG8_STAGE(PG8_SB(0, 0), b2, voffB); PG8_STAGE(PG8_SB(0, 1), b2 + hstepB, voffB); PG8_STAGE_A(PG8_SA(0, 0), a2, 0, last);
;             PG8_WAIT_V(8); PG8_WAIT_L(0); PG8_BAR; PG8_MMA(1, 0, At, B0); PG8_MMA(1, 1, At, B1); PG8_BAR; PG8_SCHED;
.LBB0_788:
	v_add_u32_e32 v1, s71, v163
	ds_read_b128 v[166:169], v1
	ds_read_b128 v[170:173], v1 offset:1024
	ds_read_b128 v[174:177], v1 offset:2048
	ds_read_b128 v[178:181], v1 offset:3072
	v_add_u32_e32 v1, s72, v163
	ds_read_b128 v[182:185], v1
	ds_read_b128 v[186:189], v1 offset:1024
	ds_read_b128 v[190:193], v1 offset:2048
	ds_read_b128 v[194:197], v1 offset:3072
	s_add_i32 s4, s4, 2
	s_add_u32 s20, s48, s2
	s_addc_u32 s21, s49, 0
	s_cmp_eq_u32 s2, s46
	s_cselect_b32 s53, s22, s21
	s_cselect_b32 s52, s23, s20
	s_cselect_b32 s51, s24, s19
	s_cselect_b32 s50, s25, s18
	v_lshl_add_u64 v[230:231], v[160:161], 0, s[2:3]
	s_add_i32 m0, s59, 0xc000
	ds_read_b128 v[198:201], v165
	ds_read_b128 v[202:205], v165 offset:1024
	ds_read_b128 v[206:209], v165 offset:2048
	ds_read_b128 v[210:213], v165 offset:3072
	ds_read_b128 v[214:217], v165 offset:4096
	ds_read_b128 v[218:221], v165 offset:5120
	ds_read_b128 v[222:225], v165 offset:6144
	ds_read_b128 v[226:229], v165 offset:7168
	global_load_lds_dwordx4 v[230:231], off
	v_lshl_add_u64 v[230:231], v[2:3], 0, s[2:3]
	s_add_i32 m0, s59, 0xe000
	s_nop 0
	global_load_lds_dwordx4 v[230:231], off
	s_waitcnt vmcnt(8)
	s_waitcnt lgkmcnt(0)
	s_barrier
	s_waitcnt lgkmcnt(0)
	v_mfma_f32_16x16x32_bf16 v[128:131], v[166:169], v[198:201], v[128:131]
	v_mfma_f32_16x16x32_bf16 v[124:127], v[174:177], v[198:201], v[124:127]
	v_mfma_f32_16x16x32_bf16 v[112:115], v[166:169], v[206:209], v[112:115]
	v_mfma_f32_16x16x32_bf16 v[108:111], v[174:177], v[206:209], v[108:111]
	v_mfma_f32_16x16x32_bf16 v[96:99], v[166:169], v[214:217], v[96:99]
	v_mfma_f32_16x16x32_bf16 v[92:95], v[174:177], v[214:217], v[92:95]
	v_mfma_f32_16x16x32_bf16 v[80:83], v[166:169], v[222:225], v[80:83]
	v_mfma_f32_16x16x32_bf16 v[76:79], v[174:177], v[222:225], v[76:79]
	v_mfma_f32_16x16x32_bf16 v[128:131], v[170:173], v[202:205], v[128:131]
	v_mfma_f32_16x16x32_bf16 v[124:127], v[178:181], v[202:205], v[124:127]
	v_mfma_f32_16x16x32_bf16 v[112:115], v[170:173], v[210:213], v[112:115]
	v_mfma_f32_16x16x32_bf16 v[108:111], v[178:181], v[210:213], v[108:111]
	v_mfma_f32_16x16x32_bf16 v[96:99], v[170:173], v[218:221], v[96:99]
	v_mfma_f32_16x16x32_bf16 v[92:95], v[178:181], v[218:221], v[92:95]
	v_mfma_f32_16x16x32_bf16 v[80:83], v[170:173], v[226:229], v[80:83]
	v_mfma_f32_16x16x32_bf16 v[76:79], v[178:181], v[226:229], v[76:79]
	v_mfma_f32_16x16x32_bf16 v[120:123], v[182:185], v[198:201], v[120:123]
	v_mfma_f32_16x16x32_bf16 v[116:119], v[190:193], v[198:201], v[116:119]
	v_mfma_f32_16x16x32_bf16 v[104:107], v[182:185], v[206:209], v[104:107]
	v_mfma_f32_16x16x32_bf16 v[100:103], v[190:193], v[206:209], v[100:103]
	v_mfma_f32_16x16x32_bf16 v[88:91], v[182:185], v[214:217], v[88:91]
	v_mfma_f32_16x16x32_bf16 v[84:87], v[190:193], v[214:217], v[84:87]
	v_mfma_f32_16x16x32_bf16 v[72:75], v[182:185], v[222:225], v[72:75]
	v_mfma_f32_16x16x32_bf16 v[68:71], v[190:193], v[222:225], v[68:71]
	v_mfma_f32_16x16x32_bf16 v[120:123], v[186:189], v[202:205], v[120:123]
	v_mfma_f32_16x16x32_bf16 v[116:119], v[194:197], v[202:205], v[116:119]
	v_mfma_f32_16x16x32_bf16 v[104:107], v[186:189], v[210:213], v[104:107]
	v_mfma_f32_16x16x32_bf16 v[100:103], v[194:197], v[210:213], v[100:103]
	v_mfma_f32_16x16x32_bf16 v[88:91], v[186:189], v[218:221], v[88:91]
	v_mfma_f32_16x16x32_bf16 v[84:87], v[194:197], v[218:221], v[84:87]
	v_mfma_f32_16x16x32_bf16 v[72:75], v[186:189], v[226:229], v[72:75]
	v_mfma_f32_16x16x32_bf16 v[68:71], v[194:197], v[226:229], v[68:71]
	s_barrier
	s_add_i32 s20, s71, s57
	v_lshl_add_u64 v[230:231], s[50:51], 0, v[136:137]
	s_mov_b32 m0, s20
	ds_read_b128 v[198:201], v165 offset:16384
	ds_read_b128 v[202:205], v165 offset:17408
	ds_read_b128 v[206:209], v165 offset:18432
	ds_read_b128 v[210:213], v165 offset:19456
	ds_read_b128 v[214:217], v165 offset:20480
	ds_read_b128 v[218:221], v165 offset:21504
	ds_read_b128 v[222:225], v165 offset:22528
	ds_read_b128 v[226:229], v165 offset:23552
	global_load_lds_dwordx4 v[230:231], off
	s_add_i32 m0, s20, 0x2000
	s_add_u32 s20, s50, 0x4000
	v_lshl_add_u64 v[230:231], s[50:51], 0, v[132:133]
	s_addc_u32 s21, s51, 0
	s_add_i32 s66, s72, s57
	global_load_lds_dwordx4 v[230:231], off
	v_lshl_add_u64 v[230:231], s[20:21], 0, v[136:137]
	s_mov_b32 m0, s66
	v_lshl_add_u64 v[232:233], s[52:53], 0, v[134:135]
	global_load_lds_dwordx4 v[230:231], off
	v_lshl_add_u64 v[230:231], s[20:21], 0, v[132:133]
	s_add_i32 m0, s66, 0x2000
	s_nop 0
	global_load_lds_dwordx4 v[230:231], off
	v_lshl_add_u64 v[230:231], s[52:53], 0, v[138:139]
	s_mov_b32 m0, s59
	s_nop 0
	global_load_lds_dwordx4 v[230:231], off
	s_mov_b32 m0, s60
	s_nop 0
	global_load_lds_dwordx4 v[232:233], off
	s_waitcnt vmcnt(8)
	s_waitcnt lgkmcnt(0)
	s_barrier
; #define PG8_STAGE_A(bufoff, base, h, isnext) do { if constexpr (Sched::GATHER) { unsigned vv_[2] = {(isnext) ? vn[h][0] : vc[h][0], (isnext) ? vn[h][1] : vc[h][1]}; PG8_STAGE(bufoff, base, vv_); } else { PG8_STAGE(bufoff, (base) + (h) * hstep, voffA); } } while (0)
; #define PG8_LDA(dst, b, h) do { _Pragma("unroll") for (int m = 0; m < 4; ++m) _Pragma("unroll") for (int k = 0; k < 2; ++k) dst[m][k] = *(const PG8_LAS bf16x8*)(lds + PG8_SA(b, h) + aoff + m * 2048 + k * 1024); } while (0)
; #define PG8_LDB(dst, b, h) do { _Pragma("unroll") for (int n = 0; n < 2; ++n) _Pragma("unroll") for (int k = 0; k < 2; ++k) dst[n][k] = *(const PG8_LAS bf16x8*)(lds + PG8_SB(b, h) + boff + n * 2048 + k * 1024); } while (0)
; #define PG8_MMA(ai, bj, At, Bt) do { __builtin_amdgcn_s_setprio(1); _Pragma("unroll") for (int m = 0; m < 4; ++m) _Pragma("unroll") for (int n = 0; n < 2; ++n) _Pragma("unroll") for (int k = 0; k < 2; ++k) \
;         acc[ai][bj][m][n] = __builtin_amdgcn_mfma_f32_16x16x32_bf16(Bt[n][k], At[m][k], acc[ai][bj][m][n], 0, 0, 0); __builtin_amdgcn_s_setprio(0); } while (0)
; #define PG8_WAIT_V(n) asm volatile("s_waitcnt vmcnt(" #n ")" ::: "memory")
; #define PG8_WAIT_L(n) asm volatile("s_waitcnt lgkmcnt(" #n ")" ::: "memory")
; #define PG8_BAR __builtin_amdgcn_s_barrier()
; #define PG8_SCHED __builtin_amdgcn_sched_barrier(0)
; template <class Epi, class Sched, bool ALIGN_EPI = false, bool SP2 = false>
; __device__ __forceinline__ void gemm_phase(PG8_LAS unsigned char* lds, const Gemm g, const Sched& S, const Epi& E, const int tid_in) {
;     ...
;             PG8_WAIT_V(8); PG8_WAIT_L(0); PG8_BAR; PG8_MMA(1, 0, At, B0); PG8_MMA(1, 1, At, B1); PG8_BAR; PG8_SCHED;
;             PG8_LDB(B0, 1, 0); PG8_LDB(B1, 1, 1); PG8_SCHED; PG8_LDA(At, 1, 0); PG8_STAGE_A(PG8_SA(0, 1), a2, 1, last);
;             PG8_WAIT_V(8); PG8_WAIT_L(0); PG8_BAR; PG8_MMA(0, 0, At, B0); PG8_MMA(0, 1, At, B1); PG8_BAR; PG8_SCHED;
	s_waitcnt lgkmcnt(0)
	v_mfma_f32_16x16x32_bf16 v[64:67], v[166:169], v[198:201], v[64:67]
	v_mfma_f32_16x16x32_bf16 v[60:63], v[174:177], v[198:201], v[60:63]
	v_mfma_f32_16x16x32_bf16 v[48:51], v[166:169], v[206:209], v[48:51]
	v_mfma_f32_16x16x32_bf16 v[44:47], v[174:177], v[206:209], v[44:47]
	v_mfma_f32_16x16x32_bf16 v[32:35], v[166:169], v[214:217], v[32:35]
	v_mfma_f32_16x16x32_bf16 v[28:31], v[174:177], v[214:217], v[28:31]
	v_mfma_f32_16x16x32_bf16 v[16:19], v[166:169], v[222:225], v[16:19]
	v_mfma_f32_16x16x32_bf16 v[12:15], v[174:177], v[222:225], v[12:15]
	v_mfma_f32_16x16x32_bf16 v[64:67], v[170:173], v[202:205], v[64:67]
	v_mfma_f32_16x16x32_bf16 v[60:63], v[178:181], v[202:205], v[60:63]
	v_mfma_f32_16x16x32_bf16 v[48:51], v[170:173], v[210:213], v[48:51]
	v_mfma_f32_16x16x32_bf16 v[44:47], v[178:181], v[210:213], v[44:47]
	v_mfma_f32_16x16x32_bf16 v[32:35], v[170:173], v[218:221], v[32:35]
	v_mfma_f32_16x16x32_bf16 v[28:31], v[178:181], v[218:221], v[28:31]
	v_mfma_f32_16x16x32_bf16 v[16:19], v[170:173], v[226:229], v[16:19]
	v_mfma_f32_16x16x32_bf16 v[12:15], v[178:181], v[226:229], v[12:15]
	v_mfma_f32_16x16x32_bf16 v[56:59], v[182:185], v[198:201], v[56:59]
	v_mfma_f32_16x16x32_bf16 v[52:55], v[190:193], v[198:201], v[52:55]
	v_mfma_f32_16x16x32_bf16 v[40:43], v[182:185], v[206:209], v[40:43]
	v_mfma_f32_16x16x32_bf16 v[36:39], v[190:193], v[206:209], v[36:39]
	v_mfma_f32_16x16x32_bf16 v[24:27], v[182:185], v[214:217], v[24:27]
	v_mfma_f32_16x16x32_bf16 v[20:23], v[190:193], v[214:217], v[20:23]
	v_mfma_f32_16x16x32_bf16 v[8:11], v[182:185], v[222:225], v[8:11]
	v_mfma_f32_16x16x32_bf16 v[4:7], v[190:193], v[222:225], v[4:7]
	v_mfma_f32_16x16x32_bf16 v[56:59], v[186:189], v[202:205], v[56:59]
	v_mfma_f32_16x16x32_bf16 v[52:55], v[194:197], v[202:205], v[52:55]
	v_mfma_f32_16x16x32_bf16 v[40:43], v[186:189], v[210:213], v[40:43]
	v_mfma_f32_16x16x32_bf16 v[36:39], v[194:197], v[210:213], v[36:39]
	v_mfma_f32_16x16x32_bf16 v[24:27], v[186:189], v[218:221], v[24:27]
	v_mfma_f32_16x16x32_bf16 v[20:23], v[194:197], v[218:221], v[20:23]
	v_mfma_f32_16x16x32_bf16 v[8:11], v[186:189], v[226:229], v[8:11]
	v_mfma_f32_16x16x32_bf16 v[4:7], v[194:197], v[226:229], v[4:7]
	s_barrier
	s_add_i32 s66, 0, 0x18000
	v_add_u32_e32 v1, s66, v163
	s_add_i32 s67, 0, 0x1c000
	ds_read_b128 v[166:169], v1
	ds_read_b128 v[170:173], v1 offset:1024
	ds_read_b128 v[174:177], v1 offset:2048
	ds_read_b128 v[178:181], v1 offset:3072
	v_add_u32_e32 v1, s67, v163
	ds_read_b128 v[182:185], v1
	ds_read_b128 v[186:189], v1 offset:1024
	ds_read_b128 v[190:193], v1 offset:2048
	ds_read_b128 v[194:197], v1 offset:3072
	s_add_u32 s20, s52, 0x100000
	s_addc_u32 s21, s53, 0
	s_mov_b32 m0, s61
	v_lshl_add_u64 v[234:235], s[20:21], 0, v[138:139]
	ds_read_b128 v[198:201], v165 offset:32768
	ds_read_b128 v[202:205], v165 offset:33792
	ds_read_b128 v[206:209], v165 offset:34816
	ds_read_b128 v[210:213], v165 offset:35840
	ds_read_b128 v[214:217], v165 offset:36864
	ds_read_b128 v[218:221], v165 offset:37888
	ds_read_b128 v[222:225], v165 offset:38912
	ds_read_b128 v[226:229], v165 offset:39936
	global_load_lds_dwordx4 v[234:235], off
	v_lshl_add_u64 v[234:235], s[20:21], 0, v[134:135]
	s_mov_b32 m0, s62
	s_nop 0
	global_load_lds_dwordx4 v[234:235], off
	s_waitcnt vmcnt(8)
	s_waitcnt lgkmcnt(0)
	s_barrier
	s_waitcnt lgkmcnt(0)
	v_mfma_f32_16x16x32_bf16 v[128:131], v[166:169], v[198:201], v[128:131]
	v_mfma_f32_16x16x32_bf16 v[124:127], v[174:177], v[198:201], v[124:127]
	v_mfma_f32_16x16x32_bf16 v[112:115], v[166:169], v[206:209], v[112:115]
	v_mfma_f32_16x16x32_bf16 v[108:111], v[174:177], v[206:209], v[108:111]
	v_mfma_f32_16x16x32_bf16 v[96:99], v[166:169], v[214:217], v[96:99]
	v_mfma_f32_16x16x32_bf16 v[92:95], v[174:177], v[214:217], v[92:95]
	v_mfma_f32_16x16x32_bf16 v[80:83], v[166:169], v[222:225], v[80:83]
	v_mfma_f32_16x16x32_bf16 v[76:79], v[174:177], v[222:225], v[76:79]
	v_mfma_f32_16x16x32_bf16 v[128:131], v[170:173], v[202:205], v[128:131]
	v_mfma_f32_16x16x32_bf16 v[124:127], v[178:181], v[202:205], v[124:127]
	v_mfma_f32_16x16x32_bf16 v[112:115], v[170:173], v[210:213], v[112:115]
	v_mfma_f32_16x16x32_bf16 v[108:111], v[178:181], v[210:213], v[108:111]
	v_mfma_f32_16x16x32_bf16 v[96:99], v[170:173], v[218:221], v[96:99]
	v_mfma_f32_16x16x32_bf16 v[92:95], v[178:181], v[218:221], v[92:95]
	v_mfma_f32_16x16x32_bf16 v[80:83], v[170:173], v[226:229], v[80:83]
	v_mfma_f32_16x16x32_bf16 v[76:79], v[178:181], v[226:229], v[76:79]
	v_mfma_f32_16x16x32_bf16 v[120:123], v[182:185], v[198:201], v[120:123]
	v_mfma_f32_16x16x32_bf16 v[116:119], v[190:193], v[198:201], v[116:119]
	v_mfma_f32_16x16x32_bf16 v[104:107], v[182:185], v[206:209], v[104:107]
	v_mfma_f32_16x16x32_bf16 v[100:103], v[190:193], v[206:209], v[100:103]
	v_mfma_f32_16x16x32_bf16 v[88:91], v[182:185], v[214:217], v[88:91]
	v_mfma_f32_16x16x32_bf16 v[84:87], v[190:193], v[214:217], v[84:87]
	v_mfma_f32_16x16x32_bf16 v[72:75], v[182:185], v[222:225], v[72:75]
	v_mfma_f32_16x16x32_bf16 v[68:71], v[190:193], v[222:225], v[68:71]
	v_mfma_f32_16x16x32_bf16 v[120:123], v[186:189], v[202:205], v[120:123]
	v_mfma_f32_16x16x32_bf16 v[116:119], v[194:197], v[202:205], v[116:119]
	v_mfma_f32_16x16x32_bf16 v[104:107], v[186:189], v[210:213], v[104:107]
	v_mfma_f32_16x16x32_bf16 v[100:103], v[194:197], v[210:213], v[100:103]
	v_mfma_f32_16x16x32_bf16 v[88:91], v[186:189], v[218:221], v[88:91]
	v_mfma_f32_16x16x32_bf16 v[84:87], v[194:197], v[218:221], v[84:87]
	v_mfma_f32_16x16x32_bf16 v[72:75], v[186:189], v[226:229], v[72:75]
	v_mfma_f32_16x16x32_bf16 v[68:71], v[194:197], v[226:229], v[68:71]
	s_barrier
; #define PG8_STAGE(bufoff, gbase, voff) do { _Pragma("unroll") for (int _i = 0; _i < 2; ++_i) \
;         __builtin_amdgcn_global_load_lds((const unsigned*)((const char*)(gbase) + (voff)[_i]), (PG8_LAS unsigned*)(lds + (bufoff) + ldsw + _i * 8192), 16, 0, 0); } while (0)
; #define PG8_STAGE_A(bufoff, base, h, isnext) do { if constexpr (Sched::GATHER) { unsigned vv_[2] = {(isnext) ? vn[h][0] : vc[h][0], (isnext) ? vn[h][1] : vc[h][1]}; PG8_STAGE(bufoff, base, vv_); } else { PG8_STAGE(bufoff, (base) + (h) * hstep, voffA); } } while (0)
; #define PG8_LDA(dst, b, h) do { _Pragma("unroll") for (int m = 0; m < 4; ++m) _Pragma("unroll") for (int k = 0; k < 2; ++k) dst[m][k] = *(const PG8_LAS bf16x8*)(lds + PG8_SA(b, h) + aoff + m * 2048 + k * 1024); } while (0)
; #define PG8_MMA(ai, bj, At, Bt) do { __builtin_amdgcn_s_setprio(1); _Pragma("unroll") for (int m = 0; m < 4; ++m) _Pragma("unroll") for (int n = 0; n < 2; ++n) _Pragma("unroll") for (int k = 0; k < 2; ++k) \
;         acc[ai][bj][m][n] = __builtin_amdgcn_mfma_f32_16x16x32_bf16(Bt[n][k], At[m][k], acc[ai][bj][m][n], 0, 0, 0); __builtin_amdgcn_s_setprio(0); } while (0)
; #define PG8_WAIT_V(n) asm volatile("s_waitcnt vmcnt(" #n ")" ::: "memory")
; #define PG8_WAIT_L(n) asm volatile("s_waitcnt lgkmcnt(" #n ")" ::: "memory")
; #define PG8_BAR __builtin_amdgcn_s_barrier()
; #define PG8_SCHED __builtin_amdgcn_sched_barrier(0)
; template <class Epi, class Sched, bool ALIGN_EPI = false, bool SP2 = false>
; __device__ __forceinline__ void gemm_phase(PG8_LAS unsigned char* lds, const Gemm g, const Sched& S, const Epi& E, const int tid_in) {
;     ...
;         for (int t = (Epi::HAS_MID && seg == 1) ? nt / 2 : 0; t < ((Epi::HAS_MID && seg == 0) ? nt / 2 : nt); t += 2) {
;     ...
;             PG8_LDA(At, 1, 1); PG8_STAGE(PG8_SB(1, 0), b3, voffB); PG8_STAGE(PG8_SB(1, 1), b3 + hstepB, voffB); PG8_STAGE_A(PG8_SA(1, 0), a3, 0, last);
;             PG8_WAIT_V(8); PG8_WAIT_L(0); PG8_BAR; PG8_MMA(1, 0, At, B0); PG8_MMA(1, 1, At, B1); PG8_BAR; PG8_SCHED;
	s_add_u32 s20, s50, 0x8000
	s_addc_u32 s21, s51, 0
	s_add_i32 s52, s66, s57
	v_lshl_add_u64 v[234:235], s[20:21], 0, v[136:137]
	s_mov_b32 m0, s52
	ds_read_b128 v[198:201], v165 offset:49152
	ds_read_b128 v[202:205], v165 offset:50176
	ds_read_b128 v[206:209], v165 offset:51200
	ds_read_b128 v[210:213], v165 offset:52224
	ds_read_b128 v[214:217], v165 offset:53248
	ds_read_b128 v[218:221], v165 offset:54272
	ds_read_b128 v[222:225], v165 offset:55296
	ds_read_b128 v[226:229], v165 offset:56320
	global_load_lds_dwordx4 v[234:235], off
	s_add_i32 m0, s52, 0x2000
	v_lshl_add_u64 v[234:235], s[20:21], 0, v[132:133]
	s_add_u32 s20, s50, 0xc000
	s_addc_u32 s21, s51, 0
	s_add_i32 s50, s67, s57
	global_load_lds_dwordx4 v[234:235], off
	v_lshl_add_u64 v[234:235], s[20:21], 0, v[136:137]
	s_mov_b32 m0, s50
	v_lshl_add_u64 v[230:231], v[230:231], 0, s[14:15]
	global_load_lds_dwordx4 v[234:235], off
	v_lshl_add_u64 v[234:235], s[20:21], 0, v[132:133]
	s_add_i32 m0, s50, 0x2000
	s_nop 0
	global_load_lds_dwordx4 v[234:235], off
	s_mov_b32 m0, s65
	s_nop 0
	global_load_lds_dwordx4 v[230:231], off
	v_lshl_add_u64 v[230:231], v[232:233], 0, s[14:15]
	s_mov_b32 m0, s68
	s_nop 0
	global_load_lds_dwordx4 v[230:231], off
	s_waitcnt vmcnt(8)
	s_waitcnt lgkmcnt(0)
	s_barrier
	s_waitcnt lgkmcnt(0)
	v_mfma_f32_16x16x32_bf16 v[64:67], v[166:169], v[198:201], v[64:67]
	v_mfma_f32_16x16x32_bf16 v[60:63], v[174:177], v[198:201], v[60:63]
	v_mfma_f32_16x16x32_bf16 v[48:51], v[166:169], v[206:209], v[48:51]
	v_mfma_f32_16x16x32_bf16 v[44:47], v[174:177], v[206:209], v[44:47]
	v_mfma_f32_16x16x32_bf16 v[32:35], v[166:169], v[214:217], v[32:35]
	v_mfma_f32_16x16x32_bf16 v[28:31], v[174:177], v[214:217], v[28:31]
	v_mfma_f32_16x16x32_bf16 v[16:19], v[166:169], v[222:225], v[16:19]
	v_mfma_f32_16x16x32_bf16 v[12:15], v[174:177], v[222:225], v[12:15]
	v_mfma_f32_16x16x32_bf16 v[64:67], v[170:173], v[202:205], v[64:67]
	v_mfma_f32_16x16x32_bf16 v[60:63], v[178:181], v[202:205], v[60:63]
	v_mfma_f32_16x16x32_bf16 v[48:51], v[170:173], v[210:213], v[48:51]
	v_mfma_f32_16x16x32_bf16 v[44:47], v[178:181], v[210:213], v[44:47]
	v_mfma_f32_16x16x32_bf16 v[32:35], v[170:173], v[218:221], v[32:35]
	v_mfma_f32_16x16x32_bf16 v[28:31], v[178:181], v[218:221], v[28:31]
	v_mfma_f32_16x16x32_bf16 v[16:19], v[170:173], v[226:229], v[16:19]
	v_mfma_f32_16x16x32_bf16 v[12:15], v[178:181], v[226:229], v[12:15]
	v_mfma_f32_16x16x32_bf16 v[56:59], v[182:185], v[198:201], v[56:59]
	v_mfma_f32_16x16x32_bf16 v[52:55], v[190:193], v[198:201], v[52:55]
	v_mfma_f32_16x16x32_bf16 v[40:43], v[182:185], v[206:209], v[40:43]
	v_mfma_f32_16x16x32_bf16 v[36:39], v[190:193], v[206:209], v[36:39]
	v_mfma_f32_16x16x32_bf16 v[24:27], v[182:185], v[214:217], v[24:27]
	v_mfma_f32_16x16x32_bf16 v[20:23], v[190:193], v[214:217], v[20:23]
	v_mfma_f32_16x16x32_bf16 v[8:11], v[182:185], v[222:225], v[8:11]
	v_mfma_f32_16x16x32_bf16 v[4:7], v[190:193], v[222:225], v[4:7]
	v_mfma_f32_16x16x32_bf16 v[56:59], v[186:189], v[202:205], v[56:59]
	v_mfma_f32_16x16x32_bf16 v[52:55], v[194:197], v[202:205], v[52:55]
	v_mfma_f32_16x16x32_bf16 v[40:43], v[186:189], v[210:213], v[40:43]
	v_mfma_f32_16x16x32_bf16 v[36:39], v[194:197], v[210:213], v[36:39]
	v_mfma_f32_16x16x32_bf16 v[24:27], v[186:189], v[218:221], v[24:27]
	v_mfma_f32_16x16x32_bf16 v[20:23], v[194:197], v[218:221], v[20:23]
	v_mfma_f32_16x16x32_bf16 v[8:11], v[186:189], v[226:229], v[8:11]
	v_mfma_f32_16x16x32_bf16 v[4:7], v[194:197], v[226:229], v[4:7]
	s_barrier
	s_add_u32 s18, s18, 0x10000
	s_addc_u32 s19, s19, 0
	s_add_u32 s48, s48, 0x100
	s_addc_u32 s49, s49, 0
	s_add_u32 s46, s46, 0xffffff00
	s_addc_u32 s47, s47, -1
	v_lshl_add_u64 v[160:161], v[160:161], 0, s[28:29]
	s_cmp_ge_u32 s4, s5
	v_lshl_add_u64 v[2:3], v[2:3], 0, s[28:29]
	s_cbranch_scc0 .LBB0_788
	s_branch .LBB0_783

; #define PG8_BAR __builtin_amdgcn_s_barrier()
;     __host__ __device__ bool next(int i, Unit& u) const {
;         if (i + i0 >= imax) return false; const long L = (long)(i + i0) * G + c; if (L >= nwg) return false;
; template <class Epi, class Sched, bool ALIGN_EPI = false, bool SP2 = false>
; __device__ __forceinline__ void gemm_phase(PG8_LAS unsigned char* lds, const Gemm g, const Sched& S, const Epi& E, const int tid_in) {
;     const int tid = tid_in, wid = __builtin_amdgcn_readfirstlane(tid >> 6), lane = tid & 63, wr = wid >> 2, wc = wid & 3, fr = lane & 15, fq = lane >> 4;
;     const int K = g.K, nt = K / BK, LDB = g.btiled ? 64 : K;
;     unsigned voffA[2], voffB[2]; unsigned vc[2][2] = {{0u, 0u}, {0u, 0u}}, vn[2][2] = {{0u, 0u}, {0u, 0u}}; int gR[2], gC[2];
; #pragma unroll
;     for (int i = 0; i < 2; ++i) { int R, C; stage_rc(tid * 16 + i * 8192, R, C); const int Rb = Epi::PERM ? ((R & ~31) + perm32(R & 31)) : R;
;         voffA[i] = (unsigned)(R * K + C) * 2u; voffB[i] = (unsigned)(Rb * LDB + C) * 2u; gR[i] = R; gC[i] = C * 2; }
;     const size_t kstep = (size_t)(BK * 2);
;     const size_t hstep = (size_t)HALF * K * 2;
;     const size_t tstep = 2 * hstep; const size_t kstepB = g.btiled ? (size_t)32768 : kstep, hstepB = g.btiled ? (size_t)16384 : hstep;
;     const unsigned ldsw = (unsigned)wid * 1024u;
;     const int aoff = lds_byte(wr * 64 + fr, fq * 8), boff = lds_byte(wc * 32 + fr, fq * 8);
;     ...
;     Unit cur, nxt; int ui = 0;
;     if (!S.next(0, cur)) return;
;     f32x4 acc[2][2][4][2];
; #pragma unroll
;     for (int a = 0; a < 2; ++a)
; #pragma unroll
;         for (int b = 0; b < 2; ++b)
; #pragma unroll
;             for (int m = 0; m < 4; ++m)
; #pragma unroll
;                 for (int n = 0; n < 2; ++n) acc[a][b][m][n] = (f32x4){0.f, 0.f, 0.f, 0.f};
;     bf16x8 At[4][2], B0[2][2], B1[2][2];
;     const char* cA = (const char*)g.A + (Sched::GATHER ? (size_t)0 : (size_t)cur.pm * tstep); if constexpr (Sched::GATHER) PG8_GFILL(vc, 0); const char* cB = (const char*)g.Bt + (size_t)cur.pn * tstep + (size_t)cur.e * g.estride;
;     S.a_ready(cur);
;     if constexpr (SP2) {
;         PG8_STAGE(PG8_SB(0, 0), cB, voffB); PG8_STAGE(PG8_SB(0, 1), cB + hstepB, voffB); PG8_STAGE_A(PG8_SA(0, 0), cA, 0, false); PG8_STAGE_A(PG8_SA(0, 1), cA, 1, false);
;         if (wr == 1) PG8_BAR;
.LBB0_845:
	s_cmp_lt_i32 s84, 8
	s_cselect_b64 s[2:3], -1, 0
	s_cmp_gt_i32 s85, 7
	s_cselect_b64 s[4:5], -1, 0
	s_and_b64 s[2:3], s[2:3], s[4:5]
	s_andn2_b64 vcc, exec, s[2:3]
	s_cbranch_vccnz .LBB0_917
	s_mov_b64 s[6:7], s[0:1]
	s_waitcnt vmcnt(0) lgkmcnt(0)
	v_mbcnt_lo_u32_b32 v4, -1, 0
	v_mbcnt_hi_u32_b32 v4, -1, v4
	s_cmpk_gt_i32 s81, 0xff
	v_add_u32_e32 v0, s33, v4
	s_nop 0
	v_readfirstlane_b32 s4, v0
	s_cbranch_scc1 .LBB0_867
	v_lshlrev_b32_e32 v1, 4, v0
	v_add_u32_e32 v2, 0x2000, v1
	v_ashrrev_i32_e32 v3, 31, v2
	v_lshrrev_b32_e32 v3, 22, v3
	v_add_u32_e32 v3, v2, v3
	v_ashrrev_i32_e32 v5, 10, v3
	v_mul_i32_i24_e32 v6, 0x400, v5
	v_sub_u32_e32 v2, v2, v6
	v_lshrrev_b32_e32 v6, 4, v2
	v_bitop3_b32 v2, v6, v2, 32 bitop3:0x6c
	v_ashrrev_i32_e32 v6, 31, v2
	v_lshrrev_b32_e32 v6, 26, v6
	v_add_u32_e32 v7, v2, v6
	v_ashrrev_i32_e32 v6, 6, v7
	v_and_b32_e32 v7, 0xc0, v7
	v_sub_u32_e32 v2, v2, v7
	v_mov_b32_e32 v10, 1
	s_load_dwordx2 s[10:11], s[6:7], 0xc8
	s_load_dwordx2 s[2:3], s[6:7], 0x0
	v_lshlrev_b32_e32 v3, 5, v5
	v_ashrrev_i16_sdwa v2, v10, sext(v2) dst_sel:DWORD dst_unused:UNUSED_PAD src0_sel:DWORD src1_sel:BYTE_0
	v_and_b32_e32 v3, 32, v3
	v_bfe_i32 v7, v2, 0, 16
	v_add_u32_e32 v2, v3, v7
	v_lshlrev_b32_e32 v3, 3, v5
	v_and_b32_e32 v3, -16, v3
	s_waitcnt lgkmcnt(0)
	s_add_u32 s17, s10, 0x54000000
	v_add_u32_e32 v3, v6, v3
	s_addc_u32 s22, s11, 0
	v_lshlrev_b32_e32 v8, 7, v3
	s_add_u32 s23, s10, 0x5800000
	v_lshl_add_u32 v144, v2, 1, v8
	s_movk_i32 s8, 0xf80
	v_ashrrev_i32_e32 v2, 31, v0
	s_addc_u32 s24, s11, 0
	v_mad_u64_u32 v[146:147], s[6:7], v3, s8, v[144:145]
	v_lshrrev_b32_e32 v2, 26, v2
	s_ashr_i32 s54, s81, 31
	v_add_u32_e32 v2, v0, v2
	v_bfe_i32 v0, v0, 27, 1
	s_lshr_b32 s6, s54, 29
	v_lshrrev_b32_e32 v0, 22, v0
	s_add_i32 s6, s81, s6
	v_add_u32_e32 v0, v1, v0
	s_and_b32 s7, s6, -8
	s_ashr_i32 s5, s4, 6
	v_and_b32_e32 v0, 0xfffffc00, v0
	s_sub_i32 s7, s81, s7
	s_ashr_i32 s15, s4, 8
	s_lshl_b32 s25, s5, 10
	v_sub_u32_e32 v0, v1, v0
	s_lshl_b32 s12, s7, 5
	s_ashr_i32 s6, s6, 3
	v_lshrrev_b32_e32 v1, 4, v0
	s_mul_i32 s9, s7, 33
	s_cmp_lt_i32 s7, 0
	v_bitop3_b32 v0, v1, v0, 32 bitop3:0x6c
	s_cselect_b32 s7, s9, s12
	v_ashrrev_i32_e32 v1, 31, v0
	s_add_i32 s6, s7, s6
	v_lshrrev_b32_e32 v1, 26, v1
	s_ashr_i32 s7, s6, 31
	v_add_u32_e32 v1, v0, v1
	s_lshr_b32 s7, s7, 26
	v_ashrrev_i32_e32 v8, 6, v2
	v_ashrrev_i32_e32 v9, 6, v1
	v_and_b32_e32 v1, 0xc0, v1
	s_add_i32 s7, s6, s7
	v_sub_u32_e32 v0, v0, v1
	v_lshlrev_b32_e32 v1, 3, v8
	s_ashr_i32 s9, s7, 6
	v_lshlrev_b32_e32 v2, 5, v8
	v_ashrrev_i16_sdwa v0, v10, sext(v0) dst_sel:DWORD dst_unused:UNUSED_PAD src0_sel:DWORD src1_sel:BYTE_0
	v_and_b32_e32 v1, -16, v1
	s_lshl_b32 s9, s9, 3
	v_and_b32_e32 v2, 32, v2
	v_bfe_i32 v10, v0, 0, 16
	v_add_u32_e32 v1, v9, v1
	s_sub_i32 s12, 32, s9
	v_add_u32_e32 v0, v2, v10
	v_lshlrev_b32_e32 v2, 7, v1
	s_min_u32 s12, s12, 8
	s_andn2_b32 s7, s7, 63
	v_lshl_add_u32 v148, v0, 1, v2
	s_sub_i32 s13, s6, s7
	v_cvt_f32_ubyte0_e32 v2, s12
	v_cvt_f32_i32_e32 v0, s13
	v_rcp_iflag_f32_e32 v3, v2
	v_mad_u64_u32 v[150:151], s[6:7], v1, s8, v[148:149]
	s_ashr_i32 s6, s13, 30
	v_mul_f32_e32 v1, v0, v3
	v_trunc_f32_e32 v1, v1
	v_fma_f32 v0, -v1, v2, v0
	v_cvt_i32_f32_e32 v1, v1
	s_or_b32 s8, s6, 1
	v_cmp_ge_f32_e64 s[6:7], |v0|, v2
	s_and_b64 s[6:7], s[6:7], exec
	s_cselect_b32 s6, s8, 0
	v_readfirstlane_b32 s7, v1
	s_add_i32 s14, s7, s6
	s_mul_i32 s6, s14, s12
	s_sub_i32 s6, s13, s6
	s_sext_i32_i8 s6, s6
	s_add_i32 s46, s9, s6
	s_ashr_i32 s47, s46, 31
	s_bfe_i64 s[8:9], s[14:15], 0x80000
	s_lshl_b64 s[6:7], s[46:47], 20
	s_lshl_b64 s[8:9], s[8:9], 20
	s_add_u32 s48, s23, s8
	s_addc_u32 s49, s24, s9
	s_add_i32 s47, s25, 0
	s_add_i32 m0, s47, 0x10000
	v_mov_b32_e32 v149, 0
	global_load_lds_dwordx4 v148, s[48:49]
	s_add_i32 m0, s47, 0x12000
	s_add_u32 s8, s48, 0x4000
	global_load_lds_dwordx4 v144, s[48:49]
	s_addc_u32 s9, s49, 0
	s_add_i32 m0, s47, 0x14000
	v_mov_b32_e32 v151, v149
	global_load_lds_dwordx4 v148, s[8:9]
	s_add_i32 m0, s47, 0x16000
	s_add_u32 s50, s17, s6
	s_addc_u32 s51, s22, s7
	s_add_i32 s18, s47, 0x2000
	global_load_lds_dwordx4 v144, s[8:9]
	s_mov_b32 m0, s47
	s_add_u32 s6, s50, 0x80000
	global_load_lds_dwordx4 v150, s[50:51]
	s_mov_b32 m0, s18
	s_addc_u32 s7, s51, 0
	s_add_i32 s19, s47, 0x4000
	global_load_lds_dwordx4 v146, s[50:51]
	s_mov_b32 m0, s19
	s_add_i32 s55, s47, 0x6000
	global_load_lds_dwordx4 v150, s[6:7]
	s_mov_b32 m0, s55
	v_mov_b32_e32 v147, v149
	global_load_lds_dwordx4 v146, s[6:7]
	s_cmp_eq_u32 s15, 1
	s_mov_b32 s56, 0
	v_mov_b32_e32 v145, v149
	v_lshl_add_u64 v[0:1], s[50:51], 0, v[150:151]
	s_cselect_b64 s[6:7], -1, 0
	s_cmp_lg_u32 s15, 1
	v_lshl_add_u64 v[2:3], s[50:51], 0, v[146:147]
	s_setprio 0
	s_cbranch_scc1 .LBB0_849
	s_setprio 1
	s_barrier

; #define PG8_STAGE(bufoff, gbase, voff) do { _Pragma("unroll") for (int _i = 0; _i < 2; ++_i) \
;         __builtin_amdgcn_global_load_lds((const unsigned*)((const char*)(gbase) + (voff)[_i]), (PG8_LAS unsigned*)(lds + (bufoff) + ldsw + _i * 8192), 16, 0, 0); } while (0)
; #define PG8_STAGE_A(bufoff, base, h, isnext) do { if constexpr (Sched::GATHER) { unsigned vv_[2] = {(isnext) ? vn[h][0] : vc[h][0], (isnext) ? vn[h][1] : vc[h][1]}; PG8_STAGE(bufoff, base, vv_); } else { PG8_STAGE(bufoff, (base) + (h) * hstep, voffA); } } while (0)
; #define PG8_LDA(dst, b, h) do { _Pragma("unroll") for (int m = 0; m < 4; ++m) _Pragma("unroll") for (int k = 0; k < 2; ++k) dst[m][k] = *(const PG8_LAS bf16x8*)(lds + PG8_SA(b, h) + aoff + m * 2048 + k * 1024); } while (0)
; #define PG8_LDB(dst, b, h) do { _Pragma("unroll") for (int n = 0; n < 2; ++n) _Pragma("unroll") for (int k = 0; k < 2; ++k) dst[n][k] = *(const PG8_LAS bf16x8*)(lds + PG8_SB(b, h) + boff + n * 2048 + k * 1024); } while (0)
; #define PG8_WAIT_V(n) asm volatile("s_waitcnt vmcnt(" #n ")" ::: "memory")
; #define PG8_WAIT_L(n) asm volatile("s_waitcnt lgkmcnt(" #n ")" ::: "memory")
; #define PG8_BAR __builtin_amdgcn_s_barrier()
; #define PG8_SCHED __builtin_amdgcn_sched_barrier(0)
; template <class Epi, class Sched, bool ALIGN_EPI = false, bool SP2 = false>
; __device__ __forceinline__ void gemm_phase(PG8_LAS unsigned char* lds, const Gemm g, const Sched& S, const Epi& E, const int tid_in) {
;     ...
;             const bool last = (t == nt - 2);
;             const char* a1 = cA + (size_t)(t + 1) * kstep;
;             const char* a2 = last ? nA : cA + (size_t)(t + 2) * kstep; const char* b2 = last ? nB : cB + (size_t)(t + 2) * kstepB;
;             const char* a3 = a2 + kstep; const char* b3 = b2 + kstepB;
;             if (last && has_next) S.a_ready(nxt);
;             if constexpr (SP2) {
;             PG8_LDB(B0, 0, 0); PG8_LDB(B1, 0, 1); PG8_SCHED; PG8_LDA(At, 0, 0); PG8_STAGE_A(PG8_SA(1, 1), a1, 1, false);
;             PG8_WAIT_V(8); PG8_WAIT_L(0); PG8_BAR; PG8_MMA(0, 0, At, B0); PG8_MMA(0, 1, At, B1); PG8_BAR; PG8_SCHED;
;             PG8_LDA(At, 0, 1); PG8_STAGE(PG8_SB(0, 0), b2, voffB); PG8_STAGE(PG8_SB(0, 1), b2 + hstepB, voffB); PG8_STAGE_A(PG8_SA(0, 0), a2, 0, last);
;             PG8_WAIT_V(8); PG8_WAIT_L(0); PG8_BAR; PG8_MMA(1, 0, At, B0); PG8_MMA(1, 1, At, B1); PG8_BAR; PG8_SCHED;
.LBB0_860:
	ds_read_b128 v[128:131], v167
	ds_read_b128 v[132:135], v167 offset:1024
	ds_read_b128 v[136:139], v167 offset:2048
	ds_read_b128 v[140:143], v167 offset:3072
	ds_read_b128 v[158:161], v168
	ds_read_b128 v[170:173], v168 offset:1024
	ds_read_b128 v[174:177], v168 offset:2048
	ds_read_b128 v[178:181], v168 offset:3072
	s_add_u32 s4, s48, 0xfff80080
	s_addc_u32 s50, s49, -1
	s_cmp_eq_u32 s68, 28
	s_cselect_b32 s53, s20, s50
	s_cselect_b32 s52, s21, s4
	s_cselect_b32 s51, s37, s67
	s_cselect_b32 s50, s39, s66
	v_lshl_add_u64 v[162:163], s[48:49], 0, v[152:153]
	s_add_i32 m0, s47, 0xc000
	ds_read_b128 v[182:185], v169
	ds_read_b128 v[186:189], v169 offset:1024
	ds_read_b128 v[190:193], v169 offset:2048
	ds_read_b128 v[194:197], v169 offset:3072
	ds_read_b128 v[198:201], v169 offset:4096
	ds_read_b128 v[202:205], v169 offset:5120
	ds_read_b128 v[206:209], v169 offset:6144
	ds_read_b128 v[210:213], v169 offset:7168
	global_load_lds_dwordx4 v[162:163], off
	v_lshl_add_u64 v[162:163], s[48:49], 0, v[154:155]
	s_add_i32 m0, s47, 0xe000
	s_nop 0
	global_load_lds_dwordx4 v[162:163], off
	s_waitcnt vmcnt(8)
	s_waitcnt lgkmcnt(0)
	s_barrier
	s_waitcnt lgkmcnt(0)
	v_mfma_f32_16x16x32_bf16 v[124:127], v[128:131], v[182:185], v[124:127]
	v_mfma_f32_16x16x32_bf16 v[120:123], v[136:139], v[182:185], v[120:123]
	v_mfma_f32_16x16x32_bf16 v[112:115], v[128:131], v[190:193], v[112:115]
	v_mfma_f32_16x16x32_bf16 v[104:107], v[136:139], v[190:193], v[104:107]
	v_mfma_f32_16x16x32_bf16 v[96:99], v[128:131], v[198:201], v[96:99]
	v_mfma_f32_16x16x32_bf16 v[88:91], v[136:139], v[198:201], v[88:91]
	v_mfma_f32_16x16x32_bf16 v[80:83], v[128:131], v[206:209], v[80:83]
	v_mfma_f32_16x16x32_bf16 v[72:75], v[136:139], v[206:209], v[72:75]
	v_mfma_f32_16x16x32_bf16 v[124:127], v[132:135], v[186:189], v[124:127]
	v_mfma_f32_16x16x32_bf16 v[120:123], v[140:143], v[186:189], v[120:123]
	v_mfma_f32_16x16x32_bf16 v[112:115], v[132:135], v[194:197], v[112:115]
	v_mfma_f32_16x16x32_bf16 v[104:107], v[140:143], v[194:197], v[104:107]
	v_mfma_f32_16x16x32_bf16 v[96:99], v[132:135], v[202:205], v[96:99]
	v_mfma_f32_16x16x32_bf16 v[88:91], v[140:143], v[202:205], v[88:91]
	v_mfma_f32_16x16x32_bf16 v[80:83], v[132:135], v[210:213], v[80:83]
	v_mfma_f32_16x16x32_bf16 v[72:75], v[140:143], v[210:213], v[72:75]
	v_mfma_f32_16x16x32_bf16 v[116:119], v[158:161], v[182:185], v[116:119]
	v_mfma_f32_16x16x32_bf16 v[108:111], v[174:177], v[182:185], v[108:111]
	v_mfma_f32_16x16x32_bf16 v[100:103], v[158:161], v[190:193], v[100:103]
	v_mfma_f32_16x16x32_bf16 v[92:95], v[174:177], v[190:193], v[92:95]
	v_mfma_f32_16x16x32_bf16 v[84:87], v[158:161], v[198:201], v[84:87]
	v_mfma_f32_16x16x32_bf16 v[76:79], v[174:177], v[198:201], v[76:79]
	v_mfma_f32_16x16x32_bf16 v[68:71], v[158:161], v[206:209], v[68:71]
	v_mfma_f32_16x16x32_bf16 v[64:67], v[174:177], v[206:209], v[64:67]
	v_mfma_f32_16x16x32_bf16 v[116:119], v[170:173], v[186:189], v[116:119]
	v_mfma_f32_16x16x32_bf16 v[108:111], v[178:181], v[186:189], v[108:111]
	v_mfma_f32_16x16x32_bf16 v[100:103], v[170:173], v[194:197], v[100:103]
	v_mfma_f32_16x16x32_bf16 v[92:95], v[178:181], v[194:197], v[92:95]
	v_mfma_f32_16x16x32_bf16 v[84:87], v[170:173], v[202:205], v[84:87]
	v_mfma_f32_16x16x32_bf16 v[76:79], v[178:181], v[202:205], v[76:79]
	v_mfma_f32_16x16x32_bf16 v[68:71], v[170:173], v[210:213], v[68:71]
	v_mfma_f32_16x16x32_bf16 v[64:67], v[178:181], v[210:213], v[64:67]
	s_barrier
	s_add_i32 s4, s60, s25
	v_lshl_add_u64 v[162:163], s[50:51], 0, v[148:149]
	s_mov_b32 m0, s4
	ds_read_b128 v[182:185], v169 offset:16384
	ds_read_b128 v[186:189], v169 offset:17408
	ds_read_b128 v[190:193], v169 offset:18432
	ds_read_b128 v[194:197], v169 offset:19456
	ds_read_b128 v[198:201], v169 offset:20480
	ds_read_b128 v[202:205], v169 offset:21504
	ds_read_b128 v[206:209], v169 offset:22528
	ds_read_b128 v[210:213], v169 offset:23552
	global_load_lds_dwordx4 v[162:163], off
	s_add_i32 m0, s4, 0x2000
	s_add_u32 s70, s50, 0x4000
	v_lshl_add_u64 v[162:163], s[50:51], 0, v[144:145]
	s_addc_u32 s71, s51, 0
	s_add_i32 s4, s61, s25
	global_load_lds_dwordx4 v[162:163], off
	v_lshl_add_u64 v[162:163], s[70:71], 0, v[148:149]
	s_mov_b32 m0, s4
	v_lshl_add_u64 v[214:215], s[52:53], 0, v[146:147]
	global_load_lds_dwordx4 v[162:163], off
	v_lshl_add_u64 v[162:163], s[70:71], 0, v[144:145]
	s_add_i32 m0, s4, 0x2000
	s_nop 0
	global_load_lds_dwordx4 v[162:163], off
	v_lshl_add_u64 v[162:163], s[52:53], 0, v[150:151]
	s_mov_b32 m0, s47
	s_nop 0
	global_load_lds_dwordx4 v[162:163], off
	s_mov_b32 m0, s18
	s_nop 0
	global_load_lds_dwordx4 v[214:215], off
	s_waitcnt vmcnt(8)
	s_waitcnt lgkmcnt(0)
	s_barrier
; #define PG8_STAGE_A(bufoff, base, h, isnext) do { if constexpr (Sched::GATHER) { unsigned vv_[2] = {(isnext) ? vn[h][0] : vc[h][0], (isnext) ? vn[h][1] : vc[h][1]}; PG8_STAGE(bufoff, base, vv_); } else { PG8_STAGE(bufoff, (base) + (h) * hstep, voffA); } } while (0)
; #define PG8_LDA(dst, b, h) do { _Pragma("unroll") for (int m = 0; m < 4; ++m) _Pragma("unroll") for (int k = 0; k < 2; ++k) dst[m][k] = *(const PG8_LAS bf16x8*)(lds + PG8_SA(b, h) + aoff + m * 2048 + k * 1024); } while (0)
; #define PG8_LDB(dst, b, h) do { _Pragma("unroll") for (int n = 0; n < 2; ++n) _Pragma("unroll") for (int k = 0; k < 2; ++k) dst[n][k] = *(const PG8_LAS bf16x8*)(lds + PG8_SB(b, h) + boff + n * 2048 + k * 1024); } while (0)
; #define PG8_MMA(ai, bj, At, Bt) do { __builtin_amdgcn_s_setprio(1); _Pragma("unroll") for (int m = 0; m < 4; ++m) _Pragma("unroll") for (int n = 0; n < 2; ++n) _Pragma("unroll") for (int k = 0; k < 2; ++k) \
;         acc[ai][bj][m][n] = __builtin_amdgcn_mfma_f32_16x16x32_bf16(Bt[n][k], At[m][k], acc[ai][bj][m][n], 0, 0, 0); __builtin_amdgcn_s_setprio(0); } while (0)
; #define PG8_WAIT_V(n) asm volatile("s_waitcnt vmcnt(" #n ")" ::: "memory")
; #define PG8_WAIT_L(n) asm volatile("s_waitcnt lgkmcnt(" #n ")" ::: "memory")
; #define PG8_BAR __builtin_amdgcn_s_barrier()
; #define PG8_SCHED __builtin_amdgcn_sched_barrier(0)
; template <class Epi, class Sched, bool ALIGN_EPI = false, bool SP2 = false>
; __device__ __forceinline__ void gemm_phase(PG8_LAS unsigned char* lds, const Gemm g, const Sched& S, const Epi& E, const int tid_in) {
;     ...
;             PG8_WAIT_V(8); PG8_WAIT_L(0); PG8_BAR; PG8_MMA(1, 0, At, B0); PG8_MMA(1, 1, At, B1); PG8_BAR; PG8_SCHED;
;             PG8_LDB(B0, 1, 0); PG8_LDB(B1, 1, 1); PG8_SCHED; PG8_LDA(At, 1, 0); PG8_STAGE_A(PG8_SA(0, 1), a2, 1, last);
;             PG8_WAIT_V(8); PG8_WAIT_L(0); PG8_BAR; PG8_MMA(0, 0, At, B0); PG8_MMA(0, 1, At, B1); PG8_BAR; PG8_SCHED;
	s_waitcnt lgkmcnt(0)
	v_mfma_f32_16x16x32_bf16 v[60:63], v[128:131], v[182:185], v[60:63]
	v_mfma_f32_16x16x32_bf16 v[56:59], v[136:139], v[182:185], v[56:59]
	v_mfma_f32_16x16x32_bf16 v[48:51], v[128:131], v[190:193], v[48:51]
	v_mfma_f32_16x16x32_bf16 v[40:43], v[136:139], v[190:193], v[40:43]
	v_mfma_f32_16x16x32_bf16 v[32:35], v[128:131], v[198:201], v[32:35]
	v_mfma_f32_16x16x32_bf16 v[24:27], v[136:139], v[198:201], v[24:27]
	v_mfma_f32_16x16x32_bf16 v[16:19], v[128:131], v[206:209], v[16:19]
	v_mfma_f32_16x16x32_bf16 v[8:11], v[136:139], v[206:209], v[8:11]
	v_mfma_f32_16x16x32_bf16 v[60:63], v[132:135], v[186:189], v[60:63]
	v_mfma_f32_16x16x32_bf16 v[56:59], v[140:143], v[186:189], v[56:59]
	v_mfma_f32_16x16x32_bf16 v[48:51], v[132:135], v[194:197], v[48:51]
	v_mfma_f32_16x16x32_bf16 v[40:43], v[140:143], v[194:197], v[40:43]
	v_mfma_f32_16x16x32_bf16 v[32:35], v[132:135], v[202:205], v[32:35]
	v_mfma_f32_16x16x32_bf16 v[24:27], v[140:143], v[202:205], v[24:27]
	v_mfma_f32_16x16x32_bf16 v[16:19], v[132:135], v[210:213], v[16:19]
	v_mfma_f32_16x16x32_bf16 v[8:11], v[140:143], v[210:213], v[8:11]
	v_mfma_f32_16x16x32_bf16 v[52:55], v[158:161], v[182:185], v[52:55]
	v_mfma_f32_16x16x32_bf16 v[44:47], v[174:177], v[182:185], v[44:47]
	v_mfma_f32_16x16x32_bf16 v[36:39], v[158:161], v[190:193], v[36:39]
	v_mfma_f32_16x16x32_bf16 v[28:31], v[174:177], v[190:193], v[28:31]
	v_mfma_f32_16x16x32_bf16 v[20:23], v[158:161], v[198:201], v[20:23]
	v_mfma_f32_16x16x32_bf16 v[12:15], v[174:177], v[198:201], v[12:15]
	v_mfma_f32_16x16x32_bf16 v[4:7], v[158:161], v[206:209], v[4:7]
	v_mfma_f32_16x16x32_bf16 v[0:3], v[174:177], v[206:209], v[0:3]
	v_mfma_f32_16x16x32_bf16 v[52:55], v[170:173], v[186:189], v[52:55]
	v_mfma_f32_16x16x32_bf16 v[44:47], v[178:181], v[186:189], v[44:47]
	v_mfma_f32_16x16x32_bf16 v[36:39], v[170:173], v[194:197], v[36:39]
	v_mfma_f32_16x16x32_bf16 v[28:31], v[178:181], v[194:197], v[28:31]
	v_mfma_f32_16x16x32_bf16 v[20:23], v[170:173], v[202:205], v[20:23]
	v_mfma_f32_16x16x32_bf16 v[12:15], v[178:181], v[202:205], v[12:15]
	v_mfma_f32_16x16x32_bf16 v[4:7], v[170:173], v[210:213], v[4:7]
	v_mfma_f32_16x16x32_bf16 v[0:3], v[178:181], v[210:213], v[0:3]
	s_barrier
	s_add_i32 s4, 0, 0x18000
	s_add_i32 s69, 0, 0x1c000
	v_add_u32_e32 v140, s4, v165
	v_add_u32_e32 v178, s69, v165
	ds_read_b128 v[128:131], v140
	ds_read_b128 v[132:135], v140 offset:1024
	ds_read_b128 v[136:139], v140 offset:2048
	ds_read_b128 v[140:143], v140 offset:3072
	ds_read_b128 v[158:161], v178
	ds_read_b128 v[170:173], v178 offset:1024
	ds_read_b128 v[174:177], v178 offset:2048
	ds_read_b128 v[178:181], v178 offset:3072
	s_add_u32 s52, s52, 0x80000
	s_addc_u32 s53, s53, 0
	s_mov_b32 m0, s19
	v_lshl_add_u64 v[216:217], s[52:53], 0, v[150:151]
	ds_read_b128 v[182:185], v169 offset:32768
	ds_read_b128 v[186:189], v169 offset:33792
	ds_read_b128 v[190:193], v169 offset:34816
	ds_read_b128 v[194:197], v169 offset:35840
	ds_read_b128 v[198:201], v169 offset:36864
	ds_read_b128 v[202:205], v169 offset:37888
	ds_read_b128 v[206:209], v169 offset:38912
	ds_read_b128 v[210:213], v169 offset:39936
	global_load_lds_dwordx4 v[216:217], off
	v_lshl_add_u64 v[216:217], s[52:53], 0, v[146:147]
	s_mov_b32 m0, s55
	s_nop 0
	global_load_lds_dwordx4 v[216:217], off
	s_waitcnt vmcnt(8)
	s_waitcnt lgkmcnt(0)
	s_barrier
	s_waitcnt lgkmcnt(0)
	v_mfma_f32_16x16x32_bf16 v[124:127], v[128:131], v[182:185], v[124:127]
	v_mfma_f32_16x16x32_bf16 v[120:123], v[136:139], v[182:185], v[120:123]
	v_mfma_f32_16x16x32_bf16 v[112:115], v[128:131], v[190:193], v[112:115]
	v_mfma_f32_16x16x32_bf16 v[104:107], v[136:139], v[190:193], v[104:107]
	v_mfma_f32_16x16x32_bf16 v[96:99], v[128:131], v[198:201], v[96:99]
	v_mfma_f32_16x16x32_bf16 v[88:91], v[136:139], v[198:201], v[88:91]
	v_mfma_f32_16x16x32_bf16 v[80:83], v[128:131], v[206:209], v[80:83]
	v_mfma_f32_16x16x32_bf16 v[72:75], v[136:139], v[206:209], v[72:75]
	v_mfma_f32_16x16x32_bf16 v[124:127], v[132:135], v[186:189], v[124:127]
	v_mfma_f32_16x16x32_bf16 v[120:123], v[140:143], v[186:189], v[120:123]
	v_mfma_f32_16x16x32_bf16 v[112:115], v[132:135], v[194:197], v[112:115]
	v_mfma_f32_16x16x32_bf16 v[104:107], v[140:143], v[194:197], v[104:107]
	v_mfma_f32_16x16x32_bf16 v[96:99], v[132:135], v[202:205], v[96:99]
	v_mfma_f32_16x16x32_bf16 v[88:91], v[140:143], v[202:205], v[88:91]
	v_mfma_f32_16x16x32_bf16 v[80:83], v[132:135], v[210:213], v[80:83]
	v_mfma_f32_16x16x32_bf16 v[72:75], v[140:143], v[210:213], v[72:75]
	v_mfma_f32_16x16x32_bf16 v[116:119], v[158:161], v[182:185], v[116:119]
	v_mfma_f32_16x16x32_bf16 v[108:111], v[174:177], v[182:185], v[108:111]
	v_mfma_f32_16x16x32_bf16 v[100:103], v[158:161], v[190:193], v[100:103]
	v_mfma_f32_16x16x32_bf16 v[92:95], v[174:177], v[190:193], v[92:95]
	v_mfma_f32_16x16x32_bf16 v[84:87], v[158:161], v[198:201], v[84:87]
	v_mfma_f32_16x16x32_bf16 v[76:79], v[174:177], v[198:201], v[76:79]
	v_mfma_f32_16x16x32_bf16 v[68:71], v[158:161], v[206:209], v[68:71]
	v_mfma_f32_16x16x32_bf16 v[64:67], v[174:177], v[206:209], v[64:67]
	v_mfma_f32_16x16x32_bf16 v[116:119], v[170:173], v[186:189], v[116:119]
	v_mfma_f32_16x16x32_bf16 v[108:111], v[178:181], v[186:189], v[108:111]
	v_mfma_f32_16x16x32_bf16 v[100:103], v[170:173], v[194:197], v[100:103]
	v_mfma_f32_16x16x32_bf16 v[92:95], v[178:181], v[194:197], v[92:95]
	v_mfma_f32_16x16x32_bf16 v[84:87], v[170:173], v[202:205], v[84:87]
	v_mfma_f32_16x16x32_bf16 v[76:79], v[178:181], v[202:205], v[76:79]
	v_mfma_f32_16x16x32_bf16 v[68:71], v[170:173], v[210:213], v[68:71]
	v_mfma_f32_16x16x32_bf16 v[64:67], v[178:181], v[210:213], v[64:67]
	s_barrier
; #define PG8_STAGE(bufoff, gbase, voff) do { _Pragma("unroll") for (int _i = 0; _i < 2; ++_i) \
;         __builtin_amdgcn_global_load_lds((const unsigned*)((const char*)(gbase) + (voff)[_i]), (PG8_LAS unsigned*)(lds + (bufoff) + ldsw + _i * 8192), 16, 0, 0); } while (0)
; #define PG8_STAGE_A(bufoff, base, h, isnext) do { if constexpr (Sched::GATHER) { unsigned vv_[2] = {(isnext) ? vn[h][0] : vc[h][0], (isnext) ? vn[h][1] : vc[h][1]}; PG8_STAGE(bufoff, base, vv_); } else { PG8_STAGE(bufoff, (base) + (h) * hstep, voffA); } } while (0)
; #define PG8_LDA(dst, b, h) do { _Pragma("unroll") for (int m = 0; m < 4; ++m) _Pragma("unroll") for (int k = 0; k < 2; ++k) dst[m][k] = *(const PG8_LAS bf16x8*)(lds + PG8_SA(b, h) + aoff + m * 2048 + k * 1024); } while (0)
; #define PG8_MMA(ai, bj, At, Bt) do { __builtin_amdgcn_s_setprio(1); _Pragma("unroll") for (int m = 0; m < 4; ++m) _Pragma("unroll") for (int n = 0; n < 2; ++n) _Pragma("unroll") for (int k = 0; k < 2; ++k) \
;         acc[ai][bj][m][n] = __builtin_amdgcn_mfma_f32_16x16x32_bf16(Bt[n][k], At[m][k], acc[ai][bj][m][n], 0, 0, 0); __builtin_amdgcn_s_setprio(0); } while (0)
; #define PG8_WAIT_V(n) asm volatile("s_waitcnt vmcnt(" #n ")" ::: "memory")
; #define PG8_WAIT_L(n) asm volatile("s_waitcnt lgkmcnt(" #n ")" ::: "memory")
; #define PG8_BAR __builtin_amdgcn_s_barrier()
; #define PG8_SCHED __builtin_amdgcn_sched_barrier(0)
; template <class Epi, class Sched, bool ALIGN_EPI = false, bool SP2 = false>
; __device__ __forceinline__ void gemm_phase(PG8_LAS unsigned char* lds, const Gemm g, const Sched& S, const Epi& E, const int tid_in) {
;     ...
;         for (int t = (Epi::HAS_MID && seg == 1) ? nt / 2 : 0; t < ((Epi::HAS_MID && seg == 0) ? nt / 2 : nt); t += 2) {
;     ...
;             PG8_LDA(At, 1, 1); PG8_STAGE(PG8_SB(1, 0), b3, voffB); PG8_STAGE(PG8_SB(1, 1), b3 + hstepB, voffB); PG8_STAGE_A(PG8_SA(1, 0), a3, 0, last);
;             PG8_WAIT_V(8); PG8_WAIT_L(0); PG8_BAR; PG8_MMA(1, 0, At, B0); PG8_MMA(1, 1, At, B1); PG8_BAR; PG8_SCHED;
	s_add_u32 s52, s50, 0x8000
	s_addc_u32 s53, s51, 0
	s_add_i32 s4, s4, s25
	v_lshl_add_u64 v[216:217], s[52:53], 0, v[148:149]
	s_mov_b32 m0, s4
	ds_read_b128 v[182:185], v169 offset:49152
	ds_read_b128 v[186:189], v169 offset:50176
	ds_read_b128 v[190:193], v169 offset:51200
	ds_read_b128 v[194:197], v169 offset:52224
	ds_read_b128 v[198:201], v169 offset:53248
	ds_read_b128 v[202:205], v169 offset:54272
	ds_read_b128 v[206:209], v169 offset:55296
	ds_read_b128 v[210:213], v169 offset:56320
	global_load_lds_dwordx4 v[216:217], off
	s_add_i32 m0, s4, 0x2000
	s_add_u32 s50, s50, 0xc000
	v_lshl_add_u64 v[216:217], s[52:53], 0, v[144:145]
	s_addc_u32 s51, s51, 0
	s_add_i32 s4, s69, s25
	global_load_lds_dwordx4 v[216:217], off
	v_lshl_add_u64 v[216:217], s[50:51], 0, v[148:149]
	s_mov_b32 m0, s4
	v_lshl_add_u64 v[162:163], v[162:163], 0, s[12:13]
	global_load_lds_dwordx4 v[216:217], off
	v_lshl_add_u64 v[216:217], s[50:51], 0, v[144:145]
	s_add_i32 m0, s4, 0x2000
	s_nop 0
	global_load_lds_dwordx4 v[216:217], off
	s_mov_b32 m0, s58
	s_nop 0
	global_load_lds_dwordx4 v[162:163], off
	v_lshl_add_u64 v[162:163], v[214:215], 0, s[12:13]
	s_mov_b32 m0, s59
	s_nop 0
	global_load_lds_dwordx4 v[162:163], off
	s_waitcnt vmcnt(8)
	s_waitcnt lgkmcnt(0)
	s_barrier
	s_waitcnt lgkmcnt(0)
	v_mfma_f32_16x16x32_bf16 v[60:63], v[128:131], v[182:185], v[60:63]
	v_mfma_f32_16x16x32_bf16 v[56:59], v[136:139], v[182:185], v[56:59]
	v_mfma_f32_16x16x32_bf16 v[48:51], v[128:131], v[190:193], v[48:51]
	v_mfma_f32_16x16x32_bf16 v[40:43], v[136:139], v[190:193], v[40:43]
	v_mfma_f32_16x16x32_bf16 v[32:35], v[128:131], v[198:201], v[32:35]
	v_mfma_f32_16x16x32_bf16 v[24:27], v[136:139], v[198:201], v[24:27]
	v_mfma_f32_16x16x32_bf16 v[16:19], v[128:131], v[206:209], v[16:19]
	v_mfma_f32_16x16x32_bf16 v[8:11], v[136:139], v[206:209], v[8:11]
	v_mfma_f32_16x16x32_bf16 v[60:63], v[132:135], v[186:189], v[60:63]
	v_mfma_f32_16x16x32_bf16 v[56:59], v[140:143], v[186:189], v[56:59]
	v_mfma_f32_16x16x32_bf16 v[48:51], v[132:135], v[194:197], v[48:51]
	v_mfma_f32_16x16x32_bf16 v[40:43], v[140:143], v[194:197], v[40:43]
	v_mfma_f32_16x16x32_bf16 v[32:35], v[132:135], v[202:205], v[32:35]
	v_mfma_f32_16x16x32_bf16 v[24:27], v[140:143], v[202:205], v[24:27]
	v_mfma_f32_16x16x32_bf16 v[16:19], v[132:135], v[210:213], v[16:19]
	v_mfma_f32_16x16x32_bf16 v[8:11], v[140:143], v[210:213], v[8:11]
	v_mfma_f32_16x16x32_bf16 v[52:55], v[158:161], v[182:185], v[52:55]
	v_mfma_f32_16x16x32_bf16 v[44:47], v[174:177], v[182:185], v[44:47]
	v_mfma_f32_16x16x32_bf16 v[36:39], v[158:161], v[190:193], v[36:39]
	v_mfma_f32_16x16x32_bf16 v[28:31], v[174:177], v[190:193], v[28:31]
	v_mfma_f32_16x16x32_bf16 v[20:23], v[158:161], v[198:201], v[20:23]
	v_mfma_f32_16x16x32_bf16 v[12:15], v[174:177], v[198:201], v[12:15]
	v_mfma_f32_16x16x32_bf16 v[4:7], v[158:161], v[206:209], v[4:7]
	v_mfma_f32_16x16x32_bf16 v[0:3], v[174:177], v[206:209], v[0:3]
	v_mfma_f32_16x16x32_bf16 v[52:55], v[170:173], v[186:189], v[52:55]
	v_mfma_f32_16x16x32_bf16 v[44:47], v[178:181], v[186:189], v[44:47]
	v_mfma_f32_16x16x32_bf16 v[36:39], v[170:173], v[194:197], v[36:39]
	v_mfma_f32_16x16x32_bf16 v[28:31], v[178:181], v[194:197], v[28:31]
	v_mfma_f32_16x16x32_bf16 v[20:23], v[170:173], v[202:205], v[20:23]
	v_mfma_f32_16x16x32_bf16 v[12:15], v[178:181], v[202:205], v[12:15]
	v_mfma_f32_16x16x32_bf16 v[4:7], v[170:173], v[210:213], v[4:7]
	v_mfma_f32_16x16x32_bf16 v[0:3], v[178:181], v[210:213], v[0:3]
	s_barrier
	s_add_i32 s68, s68, 2
	s_add_u32 s66, s66, 0x10000
	s_addc_u32 s67, s67, 0
	s_add_u32 s48, s48, 0x100
	s_addc_u32 s49, s49, 0
	s_cmp_gt_u32 s68, 29
	s_cbranch_scc0 .LBB0_860
	s_and_b64 vcc, exec, s[14:15]
	s_cbranch_vccz .LBB0_863
	s_barrier

; #define PG8_BAR __builtin_amdgcn_s_barrier()
;     __device__ __forceinline__ bool next(int i, Unit& u) const {
;         if (i + i0 >= imax) return false; const long L = (long)(i + i0) * G + c; if (L >= nwg) return false;
; template <class Epi, class Sched, bool ALIGN_EPI = false, bool SP2 = false>
; __device__ __forceinline__ void gemm_phase(PG8_LAS unsigned char* lds, const Gemm g, const Sched& S, const Epi& E, const int tid_in) {
;     const int tid = tid_in, wid = __builtin_amdgcn_readfirstlane(tid >> 6), lane = tid & 63, wr = wid >> 2, wc = wid & 3, fr = lane & 15, fq = lane >> 4;
;     const int K = g.K, nt = K / BK, LDB = g.btiled ? 64 : K;
;     unsigned voffA[2], voffB[2]; unsigned vc[2][2] = {{0u, 0u}, {0u, 0u}}, vn[2][2] = {{0u, 0u}, {0u, 0u}}; int gR[2], gC[2];
; #pragma unroll
;     for (int i = 0; i < 2; ++i) { int R, C; stage_rc(tid * 16 + i * 8192, R, C); const int Rb = Epi::PERM ? ((R & ~31) + perm32(R & 31)) : R;
;         voffA[i] = (unsigned)(R * K + C) * 2u; voffB[i] = (unsigned)(Rb * LDB + C) * 2u; gR[i] = R; gC[i] = C * 2; }
;     const size_t kstep = (size_t)(BK * 2);
;     const size_t hstep = (size_t)HALF * K * 2;
;     const size_t tstep = 2 * hstep; const size_t kstepB = g.btiled ? (size_t)32768 : kstep, hstepB = g.btiled ? (size_t)16384 : hstep;
;     const unsigned ldsw = (unsigned)wid * 1024u;
;     const int aoff = lds_byte(wr * 64 + fr, fq * 8), boff = lds_byte(wc * 32 + fr, fq * 8);
;     ...
;     Unit cur, nxt; int ui = 0;
;     if (!S.next(0, cur)) return;
;     f32x4 acc[2][2][4][2];
; #pragma unroll
;     for (int a = 0; a < 2; ++a)
; #pragma unroll
;         for (int b = 0; b < 2; ++b)
; #pragma unroll
;             for (int m = 0; m < 4; ++m)
; #pragma unroll
;                 for (int n = 0; n < 2; ++n) acc[a][b][m][n] = (f32x4){0.f, 0.f, 0.f, 0.f};
;     bf16x8 At[4][2], B0[2][2], B1[2][2];
;     const char* cA = (const char*)g.A + (Sched::GATHER ? (size_t)0 : (size_t)cur.pm * tstep); if constexpr (Sched::GATHER) PG8_GFILL(vc, 0); const char* cB = (const char*)g.Bt + (size_t)cur.pn * tstep + (size_t)cur.e * g.estride;
;     S.a_ready(cur);
;     if constexpr (SP2) {
;         PG8_STAGE(PG8_SB(0, 0), cB, voffB); PG8_STAGE(PG8_SB(0, 1), cB + hstepB, voffB); PG8_STAGE_A(PG8_SA(0, 0), cA, 0, false); PG8_STAGE_A(PG8_SA(0, 1), cA, 1, false);
;         if (wr == 1) PG8_BAR;
.LBB0_2190:
	s_add_u32 s14, s8, 0x36000000
	s_addc_u32 s15, s9, 0
	s_add_u32 s64, s8, 0x6000000
	s_addc_u32 s65, s9, 0
	s_ashr_i32 s2, s81, 3
	s_mul_i32 s2, s2, 9
	s_waitcnt lgkmcnt(0)
	s_barrier
	s_load_dwordx2 s[12:13], s[12:13], 0xa0
	s_ashr_i32 s68, s2, 5
	s_add_u32 s26, s8, 0x64000000
	s_addc_u32 s27, s9, 0
	s_cmp_lt_i32 s68, 1
	s_cbranch_scc1 .LBB0_2210
	v_mbcnt_lo_u32_b32 v2, -1, 0
	v_mbcnt_hi_u32_b32 v2, -1, v2
	s_andn2_b64 vcc, exec, s[28:29]
	v_add_u32_e32 v0, s33, v2
	s_nop 0
	v_readfirstlane_b32 s2, v0
	s_cbranch_vccnz .LBB0_2210
	v_ashrrev_i32_e32 v3, 31, v0
	v_lshrrev_b32_e32 v3, 26, v3
	v_lshlrev_b32_e32 v1, 4, v0
	v_add_u32_e32 v3, v0, v3
	v_bfe_i32 v0, v0, 27, 1
	v_lshrrev_b32_e32 v0, 22, v0
	v_add_u32_e32 v0, v1, v0
	v_and_b32_e32 v0, 0xfffffc00, v0
	v_sub_u32_e32 v0, v1, v0
	v_lshrrev_b32_e32 v4, 4, v0
	v_bitop3_b32 v0, v4, v0, 32 bitop3:0x6c
	v_ashrrev_i32_e32 v5, 31, v0
	v_ashrrev_i32_e32 v3, 6, v3
	v_lshrrev_b32_e32 v5, 26, v5
	v_lshlrev_b32_e32 v4, 3, v3
	v_add_u32_e32 v5, v0, v5
	v_and_b32_e32 v4, -16, v4
	v_ashrrev_i32_e32 v6, 6, v5
	v_add_u32_e32 v160, v6, v4
	v_and_b32_e32 v4, 0xc0, v5
	v_sub_u32_e32 v0, v0, v4
	v_mov_b32_e32 v4, 1
	v_lshlrev_b32_e32 v3, 5, v3
	v_ashrrev_i16_sdwa v0, v4, sext(v0) dst_sel:DWORD dst_unused:UNUSED_PAD src0_sel:DWORD src1_sel:BYTE_0
	v_and_b32_e32 v3, 32, v3
	v_bfe_i32 v0, v0, 0, 16
	v_add_lshl_u32 v161, v3, v0, 1
	v_add_u32_e32 v0, 0x2000, v1
	v_ashrrev_i32_e32 v1, 31, v0
	v_lshrrev_b32_e32 v1, 22, v1
	v_add_u32_e32 v1, v0, v1
	v_ashrrev_i32_e32 v1, 10, v1
	v_mul_i32_i24_e32 v3, 0x400, v1
	v_sub_u32_e32 v0, v0, v3
	v_lshrrev_b32_e32 v3, 4, v0
	v_bitop3_b32 v0, v3, v0, 32 bitop3:0x6c
	s_ashr_i32 s4, s2, 6
	s_ashr_i32 s3, s2, 8
	v_ashrrev_i32_e32 v5, 31, v0
	s_lshl_b32 s22, s4, 10
	s_or_b32 s23, s63, 1
	v_lshrrev_b32_e32 v5, 26, v5
	s_cmp_lt_i32 s5, 0
	v_lshlrev_b32_e32 v3, 3, v1
	v_add_u32_e32 v5, v0, v5
	s_cselect_b32 s20, s23, s63
	v_and_b32_e32 v3, -16, v3
	v_ashrrev_i32_e32 v7, 6, v5
	s_mul_i32 s5, s20, s5
	v_add_u32_e32 v162, v7, v3
	v_and_b32_e32 v3, 0xc0, v5
	s_add_i32 s20, s5, s18
	v_sub_u32_e32 v0, v0, v3
	s_ashr_i32 s5, s20, 31
	v_lshlrev_b32_e32 v1, 5, v1
	v_ashrrev_i16_sdwa v0, v4, sext(v0) dst_sel:DWORD dst_unused:UNUSED_PAD src0_sel:DWORD src1_sel:BYTE_0
	s_lshr_b32 s5, s5, 28
	v_and_b32_e32 v1, 32, v1
	v_bfe_i32 v0, v0, 0, 16
	s_add_i32 s5, s20, s5
	v_add_lshl_u32 v163, v1, v0, 1
	v_and_b32_e32 v0, 3, v7
	s_mov_b32 s19, 0x1ffffe0
	v_lshrrev_b32_e32 v1, 2, v162
	v_lshlrev_b32_e32 v3, 1, v162
	s_ashr_i32 s5, s5, 4
	v_and_or_b32 v0, v162, s19, v0
	v_and_b32_e32 v1, 4, v1
	v_and_b32_e32 v3, 24, v3
	s_lshl_b32 s5, s5, 2
	s_add_i32 s24, 0, 0x26c00
	v_or3_b32 v0, v0, v1, v3
	s_add_i32 s5, s24, s5
	v_lshl_add_u32 v144, v0, 7, v163
	v_mov_b32_e32 v0, s5
	ds_read_b32 v88, v0
	v_and_b32_e32 v0, 3, v6
	v_and_or_b32 v3, v160, s19, v0
	v_lshrrev_b32_e32 v0, 2, v160
	v_and_b32_e32 v4, 4, v0
	s_waitcnt lgkmcnt(0)
	v_lshlrev_b32_e32 v0, 2, v88
	v_add_u32_e32 v0, s24, v0
	ds_read2st64_b32 v[0:1], v0 offset0:4 offset1:5
	v_lshlrev_b32_e32 v5, 1, v160
	v_and_b32_e32 v5, 24, v5
	v_or3_b32 v3, v3, v4, v5
	v_lshl_add_u32 v146, v3, 7, v161
	s_waitcnt lgkmcnt(0)
	v_readfirstlane_b32 s5, v1
	s_addk_i32 s5, 0xff
	s_ashr_i32 s5, s5, 8
	s_abs_i32 s21, s5
	v_cvt_f32_u32_e32 v1, s21
	v_readfirstlane_b32 s18, v0
	s_ashr_i32 s18, s18, 8
	s_sub_i32 s28, 0, s21
	v_rcp_iflag_f32_e32 v0, v1
	s_lshl_b32 s19, s18, 4
	s_sub_i32 s19, s20, s19
	s_abs_i32 s25, s19
	v_mul_f32_e32 v0, 0x4f7ffffe, v0
	v_cvt_u32_f32_e32 v0, v0
	s_xor_b32 s20, s19, s5
	s_ashr_i32 s20, s20, 31
	v_lshlrev_b32_e32 v3, 2, v162
	v_readfirstlane_b32 s29, v0
	s_mul_i32 s28, s28, s29
	s_mul_hi_u32 s28, s29, s28
	s_add_i32 s29, s29, s28
	s_mul_hi_u32 s28, s25, s29
	s_mul_i32 s29, s28, s21
	s_sub_i32 s25, s25, s29
	s_add_i32 s29, s28, 1
	s_sub_i32 s30, s25, s21
	s_cmp_ge_u32 s25, s21
	s_cselect_b32 s28, s29, s28
	s_cselect_b32 s25, s30, s25
	s_add_i32 s29, s28, 1
	s_cmp_ge_u32 s25, s21
	s_cselect_b32 s21, s29, s28
	v_lshlrev_b32_e32 v0, 2, v160
	s_add_i32 s25, 0, 0x20000
	v_add_u32_e32 v1, s25, v0
	v_add_u32_e32 v4, s25, v3
	s_add_i32 s25, 0, 0x20200
	s_xor_b32 s21, s21, s20
	v_add_u32_e32 v0, s25, v0
	v_add_u32_e32 v3, s25, v3
	ds_read_b32 v1, v1
	ds_read_b32 v4, v4
	ds_read_b32 v0, v0
	ds_read_b32 v3, v3
	s_sub_i32 s56, s21, s20
	s_ashr_i32 s57, s56, 31
	s_lshl_b64 s[20:21], s[56:57], 20
	v_ashrrev_i32_e32 v89, 31, v88
	s_add_u32 s20, s64, s20
	s_waitcnt lgkmcnt(3)
	v_lshl_add_u32 v148, v1, 12, v161
	s_waitcnt lgkmcnt(1)
	v_lshl_add_u32 v92, v0, 12, v161
	s_addc_u32 s21, s65, s21
	v_lshlrev_b64 v[0:1], 24, v[88:89]
	v_lshl_add_u64 v[0:1], s[20:21], 0, v[0:1]
	s_add_i32 s25, s22, 0
	s_add_i32 m0, s25, 0x10000
	v_readfirstlane_b32 s20, v0
	v_readfirstlane_b32 s21, v1
	s_mov_b64 s[28:29], 0x4000
	v_lshl_add_u32 v94, v4, 12, v163
	v_lshl_add_u64 v[4:5], v[0:1], 0, s[28:29]
	s_add_i32 s57, s25, 0x2000
	s_add_i32 s67, s25, 0x4000
	global_load_lds_dwordx4 v146, s[20:21]
	s_add_i32 m0, s25, 0x12000
	s_add_i32 s69, s25, 0x6000
	global_load_lds_dwordx4 v144, s[20:21]
	s_add_i32 m0, s25, 0x14000
	v_readfirstlane_b32 s20, v4
	v_readfirstlane_b32 s21, v5
	s_waitcnt lgkmcnt(0)
	v_lshl_add_u32 v90, v3, 12, v163
	v_mov_b32_e32 v149, 0
	s_mov_b32 s70, 0
	v_mov_b32_e32 v147, v149
	v_mov_b32_e32 v145, v149
	global_load_lds_dwordx4 v146, s[20:21]
	s_add_i32 m0, s25, 0x16000
	s_cmp_eq_u32 s3, 1
	global_load_lds_dwordx4 v144, s[20:21]
	s_mov_b32 m0, s25
	s_cselect_b64 s[30:31], -1, 0
	global_load_lds_dwordx4 v148, s[14:15]
	s_mov_b32 m0, s57
	s_cmp_lg_u32 s3, 1
	global_load_lds_dwordx4 v94, s[14:15]
	s_mov_b32 m0, s67
	v_mov_b32_e32 v95, v149
	global_load_lds_dwordx4 v92, s[14:15]
	s_mov_b32 m0, s69
	s_nop 0
	global_load_lds_dwordx4 v90, s[14:15]
	s_setprio 0
	s_cbranch_scc1 .LBB0_2194
	s_setprio 1
	s_barrier

; #define PG8_STAGE(bufoff, gbase, voff) do { _Pragma("unroll") for (int _i = 0; _i < 2; ++_i) \
;         __builtin_amdgcn_global_load_lds((const unsigned*)((const char*)(gbase) + (voff)[_i]), (PG8_LAS unsigned*)(lds + (bufoff) + ldsw + _i * 8192), 16, 0, 0); } while (0)
; #define PG8_STAGE_A(bufoff, base, h, isnext) do { if constexpr (Sched::GATHER) { unsigned vv_[2] = {(isnext) ? vn[h][0] : vc[h][0], (isnext) ? vn[h][1] : vc[h][1]}; PG8_STAGE(bufoff, base, vv_); } else { PG8_STAGE(bufoff, (base) + (h) * hstep, voffA); } } while (0)
; #define PG8_LDA(dst, b, h) do { _Pragma("unroll") for (int m = 0; m < 4; ++m) _Pragma("unroll") for (int k = 0; k < 2; ++k) dst[m][k] = *(const PG8_LAS bf16x8*)(lds + PG8_SA(b, h) + aoff + m * 2048 + k * 1024); } while (0)
; #define PG8_LDB(dst, b, h) do { _Pragma("unroll") for (int n = 0; n < 2; ++n) _Pragma("unroll") for (int k = 0; k < 2; ++k) dst[n][k] = *(const PG8_LAS bf16x8*)(lds + PG8_SB(b, h) + boff + n * 2048 + k * 1024); } while (0)
; #define PG8_WAIT_V(n) asm volatile("s_waitcnt vmcnt(" #n ")" ::: "memory")
; #define PG8_WAIT_L(n) asm volatile("s_waitcnt lgkmcnt(" #n ")" ::: "memory")
; #define PG8_BAR __builtin_amdgcn_s_barrier()
; #define PG8_SCHED __builtin_amdgcn_sched_barrier(0)
; template <class Epi, class Sched, bool ALIGN_EPI = false, bool SP2 = false>
; __device__ __forceinline__ void gemm_phase(PG8_LAS unsigned char* lds, const Gemm g, const Sched& S, const Epi& E, const int tid_in) {
;     ...
;             const bool last = (t == nt - 2);
;             const char* a1 = cA + (size_t)(t + 1) * kstep;
;             const char* a2 = last ? nA : cA + (size_t)(t + 2) * kstep; const char* b2 = last ? nB : cB + (size_t)(t + 2) * kstepB;
;             const char* a3 = a2 + kstep; const char* b3 = b2 + kstepB;
;             if (last && has_next) S.a_ready(nxt);
;             if constexpr (SP2) {
;             PG8_LDB(B0, 0, 0); PG8_LDB(B1, 0, 1); PG8_SCHED; PG8_LDA(At, 0, 0); PG8_STAGE_A(PG8_SA(1, 1), a1, 1, false);
;             PG8_WAIT_V(8); PG8_WAIT_L(0); PG8_BAR; PG8_MMA(0, 0, At, B0); PG8_MMA(0, 1, At, B1); PG8_BAR; PG8_SCHED;
;             PG8_LDA(At, 0, 1); PG8_STAGE(PG8_SB(0, 0), b2, voffB); PG8_STAGE(PG8_SB(0, 1), b2 + hstepB, voffB); PG8_STAGE_A(PG8_SA(0, 0), a2, 0, last);
;             PG8_WAIT_V(8); PG8_WAIT_L(0); PG8_BAR; PG8_MMA(1, 0, At, B0); PG8_MMA(1, 1, At, B1); PG8_BAR; PG8_SCHED;
.LBB0_2203:
	s_add_u32 s4, s8, s58
	ds_read_b128 v[154:157], v167
	ds_read_b128 v[176:179], v167 offset:1024
	ds_read_b128 v[180:183], v167 offset:2048
	ds_read_b128 v[184:187], v167 offset:3072
	ds_read_b128 v[188:191], v168
	ds_read_b128 v[192:195], v168 offset:1024
	ds_read_b128 v[196:199], v168 offset:2048
	ds_read_b128 v[200:203], v168 offset:3072
	s_addc_u32 s19, s9, s59
	s_add_u32 s4, s4, 0x36000100
	s_addc_u32 s19, s19, 0
	s_cmpk_eq_i32 s58, 0xf00
	s_cselect_b64 vcc, -1, 0
	s_and_b64 s[20:21], vcc, exec
	v_cndmask_b32_e32 v159, v105, v95, vcc
	s_cselect_b32 s61, s15, s19
	s_cselect_b32 s60, s14, s4
	v_cndmask_b32_e32 v158, v104, v110, vcc
	v_lshl_add_u64 v[236:237], v[108:109], 0, s[58:59]
	s_add_i32 m0, s25, 0xc000
	ds_read_b128 v[204:207], v169
	ds_read_b128 v[208:211], v169 offset:1024
	ds_read_b128 v[212:215], v169 offset:2048
	ds_read_b128 v[216:219], v169 offset:3072
	ds_read_b128 v[220:223], v169 offset:4096
	ds_read_b128 v[224:227], v169 offset:5120
	ds_read_b128 v[228:231], v169 offset:6144
	ds_read_b128 v[232:235], v169 offset:7168
	global_load_lds_dwordx4 v[236:237], off
	v_lshl_add_u64 v[236:237], v[106:107], 0, s[58:59]
	s_add_i32 m0, s25, 0xe000
	s_nop 0
	global_load_lds_dwordx4 v[236:237], off
	s_waitcnt vmcnt(8)
	s_waitcnt lgkmcnt(0)
	s_barrier
	s_waitcnt lgkmcnt(0)
	v_mfma_f32_16x16x32_bf16 v[140:143], v[154:157], v[204:207], v[140:143]
	v_mfma_f32_16x16x32_bf16 v[136:139], v[180:183], v[204:207], v[136:139]
	v_mfma_f32_16x16x32_bf16 v[124:127], v[154:157], v[212:215], v[124:127]
	v_mfma_f32_16x16x32_bf16 v[120:123], v[180:183], v[212:215], v[120:123]
	v_mfma_f32_16x16x32_bf16 v[100:103], v[154:157], v[220:223], v[100:103]
	v_mfma_f32_16x16x32_bf16 v[96:99], v[180:183], v[220:223], v[96:99]
	v_mfma_f32_16x16x32_bf16 v[76:79], v[154:157], v[228:231], v[76:79]
	v_mfma_f32_16x16x32_bf16 v[72:75], v[180:183], v[228:231], v[72:75]
	v_mfma_f32_16x16x32_bf16 v[140:143], v[176:179], v[208:211], v[140:143]
	v_mfma_f32_16x16x32_bf16 v[136:139], v[184:187], v[208:211], v[136:139]
	v_mfma_f32_16x16x32_bf16 v[124:127], v[176:179], v[216:219], v[124:127]
	v_mfma_f32_16x16x32_bf16 v[120:123], v[184:187], v[216:219], v[120:123]
	v_mfma_f32_16x16x32_bf16 v[100:103], v[176:179], v[224:227], v[100:103]
	v_mfma_f32_16x16x32_bf16 v[96:99], v[184:187], v[224:227], v[96:99]
	v_mfma_f32_16x16x32_bf16 v[76:79], v[176:179], v[232:235], v[76:79]
	v_mfma_f32_16x16x32_bf16 v[72:75], v[184:187], v[232:235], v[72:75]
	v_mfma_f32_16x16x32_bf16 v[132:135], v[188:191], v[204:207], v[132:135]
	v_mfma_f32_16x16x32_bf16 v[128:131], v[196:199], v[204:207], v[128:131]
	v_mfma_f32_16x16x32_bf16 v[116:119], v[188:191], v[212:215], v[116:119]
	v_mfma_f32_16x16x32_bf16 v[112:115], v[196:199], v[212:215], v[112:115]
	v_mfma_f32_16x16x32_bf16 v[84:87], v[188:191], v[220:223], v[84:87]
	v_mfma_f32_16x16x32_bf16 v[80:83], v[196:199], v[220:223], v[80:83]
	v_mfma_f32_16x16x32_bf16 v[68:71], v[188:191], v[228:231], v[68:71]
	v_mfma_f32_16x16x32_bf16 v[64:67], v[196:199], v[228:231], v[64:67]
	v_mfma_f32_16x16x32_bf16 v[132:135], v[192:195], v[208:211], v[132:135]
	v_mfma_f32_16x16x32_bf16 v[128:131], v[200:203], v[208:211], v[128:131]
	v_mfma_f32_16x16x32_bf16 v[116:119], v[192:195], v[216:219], v[116:119]
	v_mfma_f32_16x16x32_bf16 v[112:115], v[200:203], v[216:219], v[112:115]
	v_mfma_f32_16x16x32_bf16 v[84:87], v[192:195], v[224:227], v[84:87]
	v_mfma_f32_16x16x32_bf16 v[80:83], v[200:203], v[224:227], v[80:83]
	v_mfma_f32_16x16x32_bf16 v[68:71], v[192:195], v[232:235], v[68:71]
	v_mfma_f32_16x16x32_bf16 v[64:67], v[200:203], v[232:235], v[64:67]
	s_barrier
	s_add_i32 s4, s73, s22
	v_lshl_add_u64 v[236:237], v[158:159], 0, v[146:147]
	s_mov_b32 m0, s4
	ds_read_b128 v[204:207], v169 offset:16384
	ds_read_b128 v[208:211], v169 offset:17408
	ds_read_b128 v[212:215], v169 offset:18432
	ds_read_b128 v[216:219], v169 offset:19456
	ds_read_b128 v[220:223], v169 offset:20480
	ds_read_b128 v[224:227], v169 offset:21504
	ds_read_b128 v[228:231], v169 offset:22528
	ds_read_b128 v[232:235], v169 offset:23552
	global_load_lds_dwordx4 v[236:237], off
	v_lshl_add_u64 v[236:237], v[158:159], 0, v[144:145]
	s_add_i32 m0, s4, 0x2000
	s_add_i32 s4, s74, s22
	global_load_lds_dwordx4 v[236:237], off
	v_lshl_add_u64 v[236:237], v[158:159], 0, s[28:29]
	v_lshl_add_u64 v[238:239], v[236:237], 0, v[146:147]
	s_mov_b32 m0, s4
	v_lshl_add_u64 v[236:237], v[236:237], 0, v[144:145]
	global_load_lds_dwordx4 v[238:239], off
	s_add_i32 m0, s4, 0x2000
	v_cndmask_b32_e32 v148, v89, v171, vcc
	global_load_lds_dwordx4 v[236:237], off
	s_mov_b32 m0, s25
	v_cndmask_b32_e32 v236, v94, v172, vcc
	global_load_lds_dwordx4 v148, s[60:61]
	s_mov_b32 m0, s57
	v_mov_b32_e32 v237, v149
	global_load_lds_dwordx4 v236, s[60:61]
	s_waitcnt vmcnt(8)
	s_waitcnt lgkmcnt(0)
	v_lshl_add_u64 v[238:239], s[60:61], 0, v[148:149]
	v_lshl_add_u64 v[236:237], s[60:61], 0, v[236:237]
	s_barrier
; #define PG8_STAGE_A(bufoff, base, h, isnext) do { if constexpr (Sched::GATHER) { unsigned vv_[2] = {(isnext) ? vn[h][0] : vc[h][0], (isnext) ? vn[h][1] : vc[h][1]}; PG8_STAGE(bufoff, base, vv_); } else { PG8_STAGE(bufoff, (base) + (h) * hstep, voffA); } } while (0)
; #define PG8_LDA(dst, b, h) do { _Pragma("unroll") for (int m = 0; m < 4; ++m) _Pragma("unroll") for (int k = 0; k < 2; ++k) dst[m][k] = *(const PG8_LAS bf16x8*)(lds + PG8_SA(b, h) + aoff + m * 2048 + k * 1024); } while (0)
; #define PG8_LDB(dst, b, h) do { _Pragma("unroll") for (int n = 0; n < 2; ++n) _Pragma("unroll") for (int k = 0; k < 2; ++k) dst[n][k] = *(const PG8_LAS bf16x8*)(lds + PG8_SB(b, h) + boff + n * 2048 + k * 1024); } while (0)
; #define PG8_MMA(ai, bj, At, Bt) do { __builtin_amdgcn_s_setprio(1); _Pragma("unroll") for (int m = 0; m < 4; ++m) _Pragma("unroll") for (int n = 0; n < 2; ++n) _Pragma("unroll") for (int k = 0; k < 2; ++k) \
;         acc[ai][bj][m][n] = __builtin_amdgcn_mfma_f32_16x16x32_bf16(Bt[n][k], At[m][k], acc[ai][bj][m][n], 0, 0, 0); __builtin_amdgcn_s_setprio(0); } while (0)
; #define PG8_WAIT_V(n) asm volatile("s_waitcnt vmcnt(" #n ")" ::: "memory")
; #define PG8_WAIT_L(n) asm volatile("s_waitcnt lgkmcnt(" #n ")" ::: "memory")
; #define PG8_BAR __builtin_amdgcn_s_barrier()
; #define PG8_SCHED __builtin_amdgcn_sched_barrier(0)
; template <class Epi, class Sched, bool ALIGN_EPI = false, bool SP2 = false>
; __device__ __forceinline__ void gemm_phase(PG8_LAS unsigned char* lds, const Gemm g, const Sched& S, const Epi& E, const int tid_in) {
;     ...
;             PG8_WAIT_V(8); PG8_WAIT_L(0); PG8_BAR; PG8_MMA(1, 0, At, B0); PG8_MMA(1, 1, At, B1); PG8_BAR; PG8_SCHED;
;             PG8_LDB(B0, 1, 0); PG8_LDB(B1, 1, 1); PG8_SCHED; PG8_LDA(At, 1, 0); PG8_STAGE_A(PG8_SA(0, 1), a2, 1, last);
;             PG8_WAIT_V(8); PG8_WAIT_L(0); PG8_BAR; PG8_MMA(0, 0, At, B0); PG8_MMA(0, 1, At, B1); PG8_BAR; PG8_SCHED;
	s_waitcnt lgkmcnt(0)
	v_mfma_f32_16x16x32_bf16 v[60:63], v[154:157], v[204:207], v[60:63]
	v_mfma_f32_16x16x32_bf16 v[56:59], v[180:183], v[204:207], v[56:59]
	v_mfma_f32_16x16x32_bf16 v[44:47], v[154:157], v[212:215], v[44:47]
	v_mfma_f32_16x16x32_bf16 v[32:35], v[180:183], v[212:215], v[32:35]
	v_mfma_f32_16x16x32_bf16 v[20:23], v[154:157], v[220:223], v[20:23]
	v_mfma_f32_16x16x32_bf16 v[16:19], v[180:183], v[220:223], v[16:19]
	v_mfma_f32_16x16x32_bf16 v[4:7], v[154:157], v[228:231], v[4:7]
	v_mfma_f32_16x16x32_bf16 v[0:3], v[180:183], v[228:231], v[0:3]
	v_mfma_f32_16x16x32_bf16 v[60:63], v[176:179], v[208:211], v[60:63]
	v_mfma_f32_16x16x32_bf16 v[56:59], v[184:187], v[208:211], v[56:59]
	v_mfma_f32_16x16x32_bf16 v[44:47], v[176:179], v[216:219], v[44:47]
	v_mfma_f32_16x16x32_bf16 v[32:35], v[184:187], v[216:219], v[32:35]
	v_mfma_f32_16x16x32_bf16 v[20:23], v[176:179], v[224:227], v[20:23]
	v_mfma_f32_16x16x32_bf16 v[16:19], v[184:187], v[224:227], v[16:19]
	v_mfma_f32_16x16x32_bf16 v[4:7], v[176:179], v[232:235], v[4:7]
	v_mfma_f32_16x16x32_bf16 v[0:3], v[184:187], v[232:235], v[0:3]
	v_mfma_f32_16x16x32_bf16 v[52:55], v[188:191], v[204:207], v[52:55]
	v_mfma_f32_16x16x32_bf16 v[48:51], v[196:199], v[204:207], v[48:51]
	v_mfma_f32_16x16x32_bf16 v[36:39], v[188:191], v[212:215], v[36:39]
	v_mfma_f32_16x16x32_bf16 v[40:43], v[196:199], v[212:215], v[40:43]
	v_mfma_f32_16x16x32_bf16 v[24:27], v[188:191], v[220:223], v[24:27]
	v_mfma_f32_16x16x32_bf16 v[28:31], v[196:199], v[220:223], v[28:31]
	v_mfma_f32_16x16x32_bf16 v[8:11], v[188:191], v[228:231], v[8:11]
	v_mfma_f32_16x16x32_bf16 v[12:15], v[196:199], v[228:231], v[12:15]
	v_mfma_f32_16x16x32_bf16 v[52:55], v[192:195], v[208:211], v[52:55]
	v_mfma_f32_16x16x32_bf16 v[48:51], v[200:203], v[208:211], v[48:51]
	v_mfma_f32_16x16x32_bf16 v[36:39], v[192:195], v[216:219], v[36:39]
	v_mfma_f32_16x16x32_bf16 v[40:43], v[200:203], v[216:219], v[40:43]
	v_mfma_f32_16x16x32_bf16 v[24:27], v[192:195], v[224:227], v[24:27]
	v_mfma_f32_16x16x32_bf16 v[28:31], v[200:203], v[224:227], v[28:31]
	v_mfma_f32_16x16x32_bf16 v[8:11], v[192:195], v[232:235], v[8:11]
	v_mfma_f32_16x16x32_bf16 v[12:15], v[200:203], v[232:235], v[12:15]
	s_barrier
	s_add_i32 s4, 0, 0x18000
	v_add_u32_e32 v91, s4, v165
	s_add_i32 s19, 0, 0x1c000
	ds_read_b128 v[154:157], v91
	ds_read_b128 v[176:179], v91 offset:1024
	ds_read_b128 v[180:183], v91 offset:2048
	ds_read_b128 v[184:187], v91 offset:3072
	v_add_u32_e32 v91, s19, v165
	ds_read_b128 v[188:191], v91
	ds_read_b128 v[192:195], v91 offset:1024
	ds_read_b128 v[196:199], v91 offset:2048
	ds_read_b128 v[200:203], v91 offset:3072
	s_mov_b32 m0, s67
	v_cndmask_b32_e32 v91, v92, v173, vcc
	ds_read_b128 v[204:207], v169 offset:32768
	ds_read_b128 v[208:211], v169 offset:33792
	ds_read_b128 v[212:215], v169 offset:34816
	ds_read_b128 v[216:219], v169 offset:35840
	ds_read_b128 v[220:223], v169 offset:36864
	ds_read_b128 v[224:227], v169 offset:37888
	ds_read_b128 v[228:231], v169 offset:38912
	ds_read_b128 v[232:235], v169 offset:39936
	v_cndmask_b32_e32 v93, v90, v174, vcc
	global_load_lds_dwordx4 v91, s[60:61]
	s_mov_b32 m0, s69
	s_nop 0
	global_load_lds_dwordx4 v93, s[60:61]
	s_waitcnt vmcnt(8)
	s_waitcnt lgkmcnt(0)
	s_barrier
	s_waitcnt lgkmcnt(0)
	v_mfma_f32_16x16x32_bf16 v[140:143], v[154:157], v[204:207], v[140:143]
	v_mfma_f32_16x16x32_bf16 v[136:139], v[180:183], v[204:207], v[136:139]
	v_mfma_f32_16x16x32_bf16 v[124:127], v[154:157], v[212:215], v[124:127]
	v_mfma_f32_16x16x32_bf16 v[120:123], v[180:183], v[212:215], v[120:123]
	v_mfma_f32_16x16x32_bf16 v[100:103], v[154:157], v[220:223], v[100:103]
	v_mfma_f32_16x16x32_bf16 v[96:99], v[180:183], v[220:223], v[96:99]
	v_mfma_f32_16x16x32_bf16 v[76:79], v[154:157], v[228:231], v[76:79]
	v_mfma_f32_16x16x32_bf16 v[72:75], v[180:183], v[228:231], v[72:75]
	v_mfma_f32_16x16x32_bf16 v[140:143], v[176:179], v[208:211], v[140:143]
	v_mfma_f32_16x16x32_bf16 v[136:139], v[184:187], v[208:211], v[136:139]
	v_mfma_f32_16x16x32_bf16 v[124:127], v[176:179], v[216:219], v[124:127]
	v_mfma_f32_16x16x32_bf16 v[120:123], v[184:187], v[216:219], v[120:123]
	v_mfma_f32_16x16x32_bf16 v[100:103], v[176:179], v[224:227], v[100:103]
	v_mfma_f32_16x16x32_bf16 v[96:99], v[184:187], v[224:227], v[96:99]
	v_mfma_f32_16x16x32_bf16 v[76:79], v[176:179], v[232:235], v[76:79]
	v_mfma_f32_16x16x32_bf16 v[72:75], v[184:187], v[232:235], v[72:75]
	v_mfma_f32_16x16x32_bf16 v[132:135], v[188:191], v[204:207], v[132:135]
	v_mfma_f32_16x16x32_bf16 v[128:131], v[196:199], v[204:207], v[128:131]
	v_mfma_f32_16x16x32_bf16 v[116:119], v[188:191], v[212:215], v[116:119]
	v_mfma_f32_16x16x32_bf16 v[112:115], v[196:199], v[212:215], v[112:115]
	v_mfma_f32_16x16x32_bf16 v[84:87], v[188:191], v[220:223], v[84:87]
	v_mfma_f32_16x16x32_bf16 v[80:83], v[196:199], v[220:223], v[80:83]
	v_mfma_f32_16x16x32_bf16 v[68:71], v[188:191], v[228:231], v[68:71]
	v_mfma_f32_16x16x32_bf16 v[64:67], v[196:199], v[228:231], v[64:67]
	v_mfma_f32_16x16x32_bf16 v[132:135], v[192:195], v[208:211], v[132:135]
	v_mfma_f32_16x16x32_bf16 v[128:131], v[200:203], v[208:211], v[128:131]
	v_mfma_f32_16x16x32_bf16 v[116:119], v[192:195], v[216:219], v[116:119]
	v_mfma_f32_16x16x32_bf16 v[112:115], v[200:203], v[216:219], v[112:115]
	v_mfma_f32_16x16x32_bf16 v[84:87], v[192:195], v[224:227], v[84:87]
	v_mfma_f32_16x16x32_bf16 v[80:83], v[200:203], v[224:227], v[80:83]
	v_mfma_f32_16x16x32_bf16 v[68:71], v[192:195], v[232:235], v[68:71]
	v_mfma_f32_16x16x32_bf16 v[64:67], v[200:203], v[232:235], v[64:67]
	s_barrier
; #define PG8_STAGE(bufoff, gbase, voff) do { _Pragma("unroll") for (int _i = 0; _i < 2; ++_i) \
;         __builtin_amdgcn_global_load_lds((const unsigned*)((const char*)(gbase) + (voff)[_i]), (PG8_LAS unsigned*)(lds + (bufoff) + ldsw + _i * 8192), 16, 0, 0); } while (0)
; #define PG8_STAGE_A(bufoff, base, h, isnext) do { if constexpr (Sched::GATHER) { unsigned vv_[2] = {(isnext) ? vn[h][0] : vc[h][0], (isnext) ? vn[h][1] : vc[h][1]}; PG8_STAGE(bufoff, base, vv_); } else { PG8_STAGE(bufoff, (base) + (h) * hstep, voffA); } } while (0)
; #define PG8_LDA(dst, b, h) do { _Pragma("unroll") for (int m = 0; m < 4; ++m) _Pragma("unroll") for (int k = 0; k < 2; ++k) dst[m][k] = *(const PG8_LAS bf16x8*)(lds + PG8_SA(b, h) + aoff + m * 2048 + k * 1024); } while (0)
; #define PG8_MMA(ai, bj, At, Bt) do { __builtin_amdgcn_s_setprio(1); _Pragma("unroll") for (int m = 0; m < 4; ++m) _Pragma("unroll") for (int n = 0; n < 2; ++n) _Pragma("unroll") for (int k = 0; k < 2; ++k) \
;         acc[ai][bj][m][n] = __builtin_amdgcn_mfma_f32_16x16x32_bf16(Bt[n][k], At[m][k], acc[ai][bj][m][n], 0, 0, 0); __builtin_amdgcn_s_setprio(0); } while (0)
; #define PG8_WAIT_V(n) asm volatile("s_waitcnt vmcnt(" #n ")" ::: "memory")
; #define PG8_WAIT_L(n) asm volatile("s_waitcnt lgkmcnt(" #n ")" ::: "memory")
; #define PG8_BAR __builtin_amdgcn_s_barrier()
; #define PG8_SCHED __builtin_amdgcn_sched_barrier(0)
; template <class Epi, class Sched, bool ALIGN_EPI = false, bool SP2 = false>
; __device__ __forceinline__ void gemm_phase(PG8_LAS unsigned char* lds, const Gemm g, const Sched& S, const Epi& E, const int tid_in) {
;     ...
;         for (int t = (Epi::HAS_MID && seg == 1) ? nt / 2 : 0; t < ((Epi::HAS_MID && seg == 0) ? nt / 2 : nt); t += 2) {
;     ...
;             PG8_LDA(At, 1, 1); PG8_STAGE(PG8_SB(1, 0), b3, voffB); PG8_STAGE(PG8_SB(1, 1), b3 + hstepB, voffB); PG8_STAGE_A(PG8_SA(1, 0), a3, 0, last);
;             PG8_WAIT_V(8); PG8_WAIT_L(0); PG8_BAR; PG8_MMA(1, 0, At, B0); PG8_MMA(1, 1, At, B1); PG8_BAR; PG8_SCHED;
	v_lshl_add_u64 v[240:241], v[158:159], 0, s[34:35]
	s_add_i32 s4, s4, s22
	v_lshl_add_u64 v[242:243], v[240:241], 0, v[146:147]
	s_mov_b32 m0, s4
	ds_read_b128 v[204:207], v169 offset:49152
	ds_read_b128 v[208:211], v169 offset:50176
	ds_read_b128 v[212:215], v169 offset:51200
	ds_read_b128 v[216:219], v169 offset:52224
	ds_read_b128 v[220:223], v169 offset:53248
	ds_read_b128 v[224:227], v169 offset:54272
	ds_read_b128 v[228:231], v169 offset:55296
	ds_read_b128 v[232:235], v169 offset:56320
	global_load_lds_dwordx4 v[242:243], off
	v_lshl_add_u64 v[240:241], v[240:241], 0, v[144:145]
	s_add_i32 m0, s4, 0x2000
	v_lshl_add_u64 v[158:159], v[158:159], 0, s[38:39]
	s_add_i32 s4, s19, s22
	global_load_lds_dwordx4 v[240:241], off
	v_lshl_add_u64 v[240:241], v[158:159], 0, v[146:147]
	s_mov_b32 m0, s4
	v_lshl_add_u64 v[158:159], v[158:159], 0, v[144:145]
	global_load_lds_dwordx4 v[240:241], off
	s_add_i32 m0, s4, 0x2000
	s_nop 0
	global_load_lds_dwordx4 v[158:159], off
	v_lshl_add_u64 v[158:159], v[238:239], 0, s[44:45]
	s_mov_b32 m0, s71
	s_nop 0
	global_load_lds_dwordx4 v[158:159], off
	v_lshl_add_u64 v[158:159], v[236:237], 0, s[44:45]
	s_mov_b32 m0, s72
	s_nop 0
	global_load_lds_dwordx4 v[158:159], off
	s_waitcnt vmcnt(8)
	s_waitcnt lgkmcnt(0)
	s_barrier
	s_waitcnt lgkmcnt(0)
	v_mfma_f32_16x16x32_bf16 v[60:63], v[154:157], v[204:207], v[60:63]
	v_mfma_f32_16x16x32_bf16 v[56:59], v[180:183], v[204:207], v[56:59]
	v_mfma_f32_16x16x32_bf16 v[44:47], v[154:157], v[212:215], v[44:47]
	v_mfma_f32_16x16x32_bf16 v[32:35], v[180:183], v[212:215], v[32:35]
	v_mfma_f32_16x16x32_bf16 v[20:23], v[154:157], v[220:223], v[20:23]
	v_mfma_f32_16x16x32_bf16 v[16:19], v[180:183], v[220:223], v[16:19]
	v_mfma_f32_16x16x32_bf16 v[4:7], v[154:157], v[228:231], v[4:7]
	v_mfma_f32_16x16x32_bf16 v[0:3], v[180:183], v[228:231], v[0:3]
	v_mfma_f32_16x16x32_bf16 v[60:63], v[176:179], v[208:211], v[60:63]
	v_mfma_f32_16x16x32_bf16 v[56:59], v[184:187], v[208:211], v[56:59]
	v_mfma_f32_16x16x32_bf16 v[44:47], v[176:179], v[216:219], v[44:47]
	v_mfma_f32_16x16x32_bf16 v[32:35], v[184:187], v[216:219], v[32:35]
	v_mfma_f32_16x16x32_bf16 v[20:23], v[176:179], v[224:227], v[20:23]
	v_mfma_f32_16x16x32_bf16 v[16:19], v[184:187], v[224:227], v[16:19]
	v_mfma_f32_16x16x32_bf16 v[4:7], v[176:179], v[232:235], v[4:7]
	v_mfma_f32_16x16x32_bf16 v[0:3], v[184:187], v[232:235], v[0:3]
	v_mfma_f32_16x16x32_bf16 v[52:55], v[188:191], v[204:207], v[52:55]
	v_mfma_f32_16x16x32_bf16 v[48:51], v[196:199], v[204:207], v[48:51]
	v_mfma_f32_16x16x32_bf16 v[36:39], v[188:191], v[212:215], v[36:39]
	v_mfma_f32_16x16x32_bf16 v[40:43], v[196:199], v[212:215], v[40:43]
	v_mfma_f32_16x16x32_bf16 v[24:27], v[188:191], v[220:223], v[24:27]
	v_mfma_f32_16x16x32_bf16 v[28:31], v[196:199], v[220:223], v[28:31]
	v_mfma_f32_16x16x32_bf16 v[8:11], v[188:191], v[228:231], v[8:11]
	v_mfma_f32_16x16x32_bf16 v[12:15], v[196:199], v[228:231], v[12:15]
	v_mfma_f32_16x16x32_bf16 v[52:55], v[192:195], v[208:211], v[52:55]
	v_mfma_f32_16x16x32_bf16 v[48:51], v[200:203], v[208:211], v[48:51]
	v_mfma_f32_16x16x32_bf16 v[36:39], v[192:195], v[216:219], v[36:39]
	v_mfma_f32_16x16x32_bf16 v[40:43], v[200:203], v[216:219], v[40:43]
	v_mfma_f32_16x16x32_bf16 v[24:27], v[192:195], v[224:227], v[24:27]
	v_mfma_f32_16x16x32_bf16 v[28:31], v[200:203], v[224:227], v[28:31]
	v_mfma_f32_16x16x32_bf16 v[8:11], v[192:195], v[232:235], v[8:11]
	v_mfma_f32_16x16x32_bf16 v[12:15], v[200:203], v[232:235], v[12:15]
	s_barrier
	s_add_i32 s18, s18, 2
	s_add_u32 s58, s58, 0x100
	s_addc_u32 s59, s59, 0
	s_cmp_gt_u32 s18, 29
	v_lshl_add_u64 v[104:105], v[104:105], 0, s[42:43]
	s_cbranch_scc0 .LBB0_2203
	s_and_b64 vcc, exec, s[40:41]
	s_cbranch_vccz .LBB0_2206
	s_barrier

; #define PG8_BAR __builtin_amdgcn_s_barrier()
;     __device__ __forceinline__ bool next(int i, Unit& u) const {
;         if (i + i0 >= imax) return false; const long L = (long)(i + i0) * G + c; if (L >= nwg) return false;
; template <class Epi, class Sched, bool ALIGN_EPI = false, bool SP2 = false>
; __device__ __forceinline__ void gemm_phase(PG8_LAS unsigned char* lds, const Gemm g, const Sched& S, const Epi& E, const int tid_in) {
;     const int tid = tid_in, wid = __builtin_amdgcn_readfirstlane(tid >> 6), lane = tid & 63, wr = wid >> 2, wc = wid & 3, fr = lane & 15, fq = lane >> 4;
;     const int K = g.K, nt = K / BK, LDB = g.btiled ? 64 : K;
;     unsigned voffA[2], voffB[2]; unsigned vc[2][2] = {{0u, 0u}, {0u, 0u}}, vn[2][2] = {{0u, 0u}, {0u, 0u}}; int gR[2], gC[2];
; #pragma unroll
;     for (int i = 0; i < 2; ++i) { int R, C; stage_rc(tid * 16 + i * 8192, R, C); const int Rb = Epi::PERM ? ((R & ~31) + perm32(R & 31)) : R;
;         voffA[i] = (unsigned)(R * K + C) * 2u; voffB[i] = (unsigned)(Rb * LDB + C) * 2u; gR[i] = R; gC[i] = C * 2; }
;     const size_t kstep = (size_t)(BK * 2);
;     const size_t hstep = (size_t)HALF * K * 2;
;     const size_t tstep = 2 * hstep; const size_t kstepB = g.btiled ? (size_t)32768 : kstep, hstepB = g.btiled ? (size_t)16384 : hstep;
;     const unsigned ldsw = (unsigned)wid * 1024u;
;     const int aoff = lds_byte(wr * 64 + fr, fq * 8), boff = lds_byte(wc * 32 + fr, fq * 8);
;     ...
;     Unit cur, nxt; int ui = 0;
;     if (!S.next(0, cur)) return;
;     f32x4 acc[2][2][4][2];
; #pragma unroll
;     for (int a = 0; a < 2; ++a)
; #pragma unroll
;         for (int b = 0; b < 2; ++b)
; #pragma unroll
;             for (int m = 0; m < 4; ++m)
; #pragma unroll
;                 for (int n = 0; n < 2; ++n) acc[a][b][m][n] = (f32x4){0.f, 0.f, 0.f, 0.f};
;     bf16x8 At[4][2], B0[2][2], B1[2][2];
;     const char* cA = (const char*)g.A + (Sched::GATHER ? (size_t)0 : (size_t)cur.pm * tstep); if constexpr (Sched::GATHER) PG8_GFILL(vc, 0); const char* cB = (const char*)g.Bt + (size_t)cur.pn * tstep + (size_t)cur.e * g.estride;
;     S.a_ready(cur);
;     if constexpr (SP2) {
;         PG8_STAGE(PG8_SB(0, 0), cB, voffB); PG8_STAGE(PG8_SB(0, 1), cB + hstepB, voffB); PG8_STAGE_A(PG8_SA(0, 0), cA, 0, false); PG8_STAGE_A(PG8_SA(0, 1), cA, 1, false);
;         if (wr == 1) PG8_BAR;
.LBB0_2288:
	s_mul_i32 s2, s16, s68
	s_mul_hi_i32 s3, s16, s68
	s_add_u32 s2, s2, s81
	s_addc_u32 s3, s3, s62
	s_waitcnt vmcnt(21)
	v_mov_b64_e32 v[4:5], s[10:11]
	s_waitcnt lgkmcnt(0)
	s_barrier
	v_mbcnt_lo_u32_b32 v2, -1, 0
	v_mbcnt_hi_u32_b32 v2, -1, v2
	v_cmp_ge_i64_e32 vcc, s[2:3], v[4:5]
	v_add_u32_e32 v0, s33, v2
	s_nop 0
	v_readfirstlane_b32 s4, v0
	s_cbranch_vccnz .LBB0_2307
	v_ashrrev_i32_e32 v3, 31, v0
	v_lshrrev_b32_e32 v3, 26, v3
	v_lshlrev_b32_e32 v1, 4, v0
	v_add_u32_e32 v3, v0, v3
	v_bfe_i32 v0, v0, 27, 1
	v_lshrrev_b32_e32 v0, 22, v0
	v_add_u32_e32 v0, v1, v0
	v_and_b32_e32 v0, 0xfffffc00, v0
	v_sub_u32_e32 v0, v1, v0
	v_lshrrev_b32_e32 v4, 4, v0
	v_bitop3_b32 v0, v4, v0, 32 bitop3:0x6c
	v_ashrrev_i32_e32 v5, 31, v0
	v_ashrrev_i32_e32 v3, 6, v3
	v_lshrrev_b32_e32 v5, 26, v5
	v_lshlrev_b32_e32 v4, 3, v3
	v_add_u32_e32 v5, v0, v5
	v_and_b32_e32 v4, -16, v4
	v_ashrrev_i32_e32 v6, 6, v5
	v_add_u32_e32 v160, v6, v4
	v_and_b32_e32 v4, 0xc0, v5
	v_sub_u32_e32 v0, v0, v4
	v_mov_b32_e32 v4, 1
	v_lshlrev_b32_e32 v3, 5, v3
	v_ashrrev_i16_sdwa v0, v4, sext(v0) dst_sel:DWORD dst_unused:UNUSED_PAD src0_sel:DWORD src1_sel:BYTE_0
	v_and_b32_e32 v3, 32, v3
	v_bfe_i32 v0, v0, 0, 16
	v_add_lshl_u32 v161, v3, v0, 1
	v_add_u32_e32 v0, 0x2000, v1
	v_ashrrev_i32_e32 v1, 31, v0
	v_lshrrev_b32_e32 v1, 22, v1
	v_add_u32_e32 v1, v0, v1
	s_ashr_i32 s5, s2, 31
	v_ashrrev_i32_e32 v1, 10, v1
	s_lshr_b32 s5, s5, 29
	v_mul_i32_i24_e32 v3, 0x400, v1
	s_add_i32 s5, s2, s5
	v_sub_u32_e32 v0, v0, v3
	s_ashr_i32 s19, s5, 3
	s_and_b32 s5, s5, -8
	v_lshrrev_b32_e32 v3, 4, v0
	s_sub_i32 s2, s2, s5
	s_lshl_b32 s5, s68, 10
	v_bitop3_b32 v0, v3, v0, 32 bitop3:0x6c
	s_ashr_i32 s18, s4, 6
	s_add_i32 s5, s5, 0
	s_ashr_i32 s3, s4, 8
	v_ashrrev_i32_e32 v5, 31, v0
	s_lshl_b32 s17, s18, 10
	s_add_i32 s20, s5, 0x20000
	s_or_b32 s22, s63, 1
	v_lshrrev_b32_e32 v5, 26, v5
	s_cmp_lt_i32 s2, 0
	v_lshlrev_b32_e32 v3, 3, v1
	v_add_u32_e32 v5, v0, v5
	s_cselect_b32 s21, s22, s63
	v_and_b32_e32 v3, -16, v3
	v_ashrrev_i32_e32 v7, 6, v5
	s_mul_i32 s2, s21, s2
	v_add_u32_e32 v162, v7, v3
	v_and_b32_e32 v3, 0xc0, v5
	s_add_i32 s19, s2, s19
	v_sub_u32_e32 v0, v0, v3
	s_ashr_i32 s2, s19, 31
	v_lshlrev_b32_e32 v1, 5, v1
	v_ashrrev_i16_sdwa v0, v4, sext(v0) dst_sel:DWORD dst_unused:UNUSED_PAD src0_sel:DWORD src1_sel:BYTE_0
	s_lshr_b32 s2, s2, 28
	v_and_b32_e32 v1, 32, v1
	v_bfe_i32 v0, v0, 0, 16
	s_add_i32 s2, s19, s2
	v_add_lshl_u32 v163, v1, v0, 1
	v_and_b32_e32 v0, 3, v7
	s_mov_b32 s5, 0x1ffffe0
	v_lshrrev_b32_e32 v1, 2, v162
	v_lshlrev_b32_e32 v3, 1, v162
	s_ashr_i32 s2, s2, 4
	v_and_or_b32 v0, v162, s5, v0
	v_and_b32_e32 v1, 4, v1
	v_and_b32_e32 v3, 24, v3
	s_lshl_b32 s2, s2, 2
	s_add_i32 s23, 0, 0x26c00
	v_or3_b32 v0, v0, v1, v3
	s_add_i32 s2, s23, s2
	v_lshl_add_u32 v144, v0, 7, v163
	v_mov_b32_e32 v0, s2
	ds_read_b32 v88, v0
	v_and_b32_e32 v0, 3, v6
	v_and_or_b32 v3, v160, s5, v0
	v_lshrrev_b32_e32 v0, 2, v160
	v_and_b32_e32 v4, 4, v0
	s_waitcnt lgkmcnt(0)
	v_lshlrev_b32_e32 v0, 2, v88
	v_add_u32_e32 v0, s23, v0
	ds_read2st64_b32 v[0:1], v0 offset0:4 offset1:5
	v_lshlrev_b32_e32 v5, 1, v160
	v_and_b32_e32 v5, 24, v5
	v_or3_b32 v3, v3, v4, v5
	v_lshl_add_u32 v146, v3, 7, v161
	s_waitcnt lgkmcnt(0)
	v_readfirstlane_b32 s2, v1
	s_addk_i32 s2, 0xff
	s_ashr_i32 s2, s2, 8
	s_abs_i32 s21, s2
	v_cvt_f32_u32_e32 v1, s21
	v_readfirstlane_b32 s5, v0
	s_ashr_i32 s5, s5, 8
	s_sub_i32 s28, 0, s21
	v_rcp_iflag_f32_e32 v0, v1
	s_lshl_b32 s24, s5, 4
	s_sub_i32 s19, s19, s24
	s_abs_i32 s25, s19
	v_mul_f32_e32 v0, 0x4f7ffffe, v0
	v_cvt_u32_f32_e32 v0, v0
	s_xor_b32 s24, s19, s2
	s_ashr_i32 s24, s24, 31
	v_lshl_add_u32 v3, v162, 2, s20
	v_readfirstlane_b32 s29, v0
	s_mul_i32 s28, s28, s29
	s_mul_hi_u32 s28, s29, s28
	s_add_i32 s29, s29, s28
	s_mul_hi_u32 s28, s25, s29
	s_mul_i32 s29, s28, s21
	s_sub_i32 s25, s25, s29
	s_add_i32 s29, s28, 1
	s_sub_i32 s30, s25, s21
	s_cmp_ge_u32 s25, s21
	s_cselect_b32 s28, s29, s28
	s_cselect_b32 s25, s30, s25
	s_add_i32 s29, s28, 1
	s_cmp_ge_u32 s25, s21
	v_lshl_add_u32 v0, v160, 2, s20
	s_cselect_b32 s20, s29, s28
	ds_read2st64_b32 v[0:1], v0 offset1:2
	s_xor_b32 s20, s20, s24
	s_sub_i32 s56, s20, s24
	s_ashr_i32 s57, s56, 31
	ds_read2st64_b32 v[4:5], v3 offset1:2
	s_lshl_b64 s[20:21], s[56:57], 20
	v_ashrrev_i32_e32 v89, 31, v88
	s_add_u32 s20, s64, s20
	s_waitcnt lgkmcnt(1)
	v_lshl_add_u32 v148, v0, 12, v161
	v_lshl_add_u32 v92, v1, 12, v161
	s_addc_u32 s21, s65, s21
	v_lshlrev_b64 v[0:1], 24, v[88:89]
	v_lshl_add_u64 v[0:1], s[20:21], 0, v[0:1]
	s_add_i32 s24, s17, 0
	s_add_i32 m0, s24, 0x10000
	v_readfirstlane_b32 s20, v0
	v_readfirstlane_b32 s21, v1
	s_mov_b64 s[28:29], 0x4000
	s_waitcnt lgkmcnt(0)
	v_lshl_add_u32 v94, v4, 12, v163
	v_lshl_add_u32 v90, v5, 12, v163
	v_lshl_add_u64 v[4:5], v[0:1], 0, s[28:29]
	s_add_i32 s25, s24, 0x2000
	global_load_lds_dwordx4 v146, s[20:21]
	s_add_i32 m0, s24, 0x12000
	s_add_i32 s57, s24, 0x4000
	global_load_lds_dwordx4 v144, s[20:21]
	s_add_i32 m0, s24, 0x14000
	v_readfirstlane_b32 s20, v4
	v_readfirstlane_b32 s21, v5
	s_add_i32 s67, s24, 0x6000
	v_mov_b32_e32 v149, 0
	s_mov_b32 s69, 0
	v_mov_b32_e32 v147, v149
	v_mov_b32_e32 v145, v149
	global_load_lds_dwordx4 v146, s[20:21]
	s_add_i32 m0, s24, 0x16000
	s_cmp_eq_u32 s3, 1
	global_load_lds_dwordx4 v144, s[20:21]
	s_mov_b32 m0, s24
	s_cselect_b64 s[30:31], -1, 0
	global_load_lds_dwordx4 v148, s[14:15]
	s_mov_b32 m0, s25
	s_cmp_lg_u32 s3, 1
	global_load_lds_dwordx4 v94, s[14:15]
	s_mov_b32 m0, s57
	v_mov_b32_e32 v95, v149
	global_load_lds_dwordx4 v92, s[14:15]
	s_mov_b32 m0, s67
	s_nop 0
	global_load_lds_dwordx4 v90, s[14:15]
	s_setprio 0
	s_cbranch_scc1 .LBB0_2291
	s_setprio 1
	s_barrier

; #define PG8_STAGE(bufoff, gbase, voff) do { _Pragma("unroll") for (int _i = 0; _i < 2; ++_i) \
;         __builtin_amdgcn_global_load_lds((const unsigned*)((const char*)(gbase) + (voff)[_i]), (PG8_LAS unsigned*)(lds + (bufoff) + ldsw + _i * 8192), 16, 0, 0); } while (0)
; #define PG8_STAGE_A(bufoff, base, h, isnext) do { if constexpr (Sched::GATHER) { unsigned vv_[2] = {(isnext) ? vn[h][0] : vc[h][0], (isnext) ? vn[h][1] : vc[h][1]}; PG8_STAGE(bufoff, base, vv_); } else { PG8_STAGE(bufoff, (base) + (h) * hstep, voffA); } } while (0)
; #define PG8_LDA(dst, b, h) do { _Pragma("unroll") for (int m = 0; m < 4; ++m) _Pragma("unroll") for (int k = 0; k < 2; ++k) dst[m][k] = *(const PG8_LAS bf16x8*)(lds + PG8_SA(b, h) + aoff + m * 2048 + k * 1024); } while (0)
; #define PG8_LDB(dst, b, h) do { _Pragma("unroll") for (int n = 0; n < 2; ++n) _Pragma("unroll") for (int k = 0; k < 2; ++k) dst[n][k] = *(const PG8_LAS bf16x8*)(lds + PG8_SB(b, h) + boff + n * 2048 + k * 1024); } while (0)
; #define PG8_WAIT_V(n) asm volatile("s_waitcnt vmcnt(" #n ")" ::: "memory")
; #define PG8_WAIT_L(n) asm volatile("s_waitcnt lgkmcnt(" #n ")" ::: "memory")
; #define PG8_BAR __builtin_amdgcn_s_barrier()
; #define PG8_SCHED __builtin_amdgcn_sched_barrier(0)
; template <class Epi, class Sched, bool ALIGN_EPI = false, bool SP2 = false>
; __device__ __forceinline__ void gemm_phase(PG8_LAS unsigned char* lds, const Gemm g, const Sched& S, const Epi& E, const int tid_in) {
;     ...
;             const bool last = (t == nt - 2);
;             const char* a1 = cA + (size_t)(t + 1) * kstep;
;             const char* a2 = last ? nA : cA + (size_t)(t + 2) * kstep; const char* b2 = last ? nB : cB + (size_t)(t + 2) * kstepB;
;             const char* a3 = a2 + kstep; const char* b3 = b2 + kstepB;
;             if (last && has_next) S.a_ready(nxt);
;             if constexpr (SP2) {
;             PG8_LDB(B0, 0, 0); PG8_LDB(B1, 0, 1); PG8_SCHED; PG8_LDA(At, 0, 0); PG8_STAGE_A(PG8_SA(1, 1), a1, 1, false);
;             PG8_WAIT_V(8); PG8_WAIT_L(0); PG8_BAR; PG8_MMA(0, 0, At, B0); PG8_MMA(0, 1, At, B1); PG8_BAR; PG8_SCHED;
;             PG8_LDA(At, 0, 1); PG8_STAGE(PG8_SB(0, 0), b2, voffB); PG8_STAGE(PG8_SB(0, 1), b2 + hstepB, voffB); PG8_STAGE_A(PG8_SA(0, 0), a2, 0, last);
;             PG8_WAIT_V(8); PG8_WAIT_L(0); PG8_BAR; PG8_MMA(1, 0, At, B0); PG8_MMA(1, 1, At, B1); PG8_BAR; PG8_SCHED;
.LBB0_2300:
	s_add_u32 s4, s8, s58
	ds_read_b128 v[154:157], v167
	ds_read_b128 v[176:179], v167 offset:1024
	ds_read_b128 v[180:183], v167 offset:2048
	ds_read_b128 v[184:187], v167 offset:3072
	ds_read_b128 v[188:191], v168
	ds_read_b128 v[192:195], v168 offset:1024
	ds_read_b128 v[196:199], v168 offset:2048
	ds_read_b128 v[200:203], v168 offset:3072
	s_addc_u32 s19, s9, s59
	s_add_u32 s4, s4, 0x36000100
	s_addc_u32 s19, s19, 0
	s_cmpk_eq_i32 s58, 0xf00
	s_cselect_b64 vcc, -1, 0
	s_and_b64 s[20:21], vcc, exec
	v_cndmask_b32_e32 v159, v105, v95, vcc
	s_cselect_b32 s61, s15, s19
	s_cselect_b32 s60, s14, s4
	v_cndmask_b32_e32 v158, v104, v110, vcc
	v_lshl_add_u64 v[236:237], v[108:109], 0, s[58:59]
	s_add_i32 m0, s24, 0xc000
	ds_read_b128 v[204:207], v169
	ds_read_b128 v[208:211], v169 offset:1024
	ds_read_b128 v[212:215], v169 offset:2048
	ds_read_b128 v[216:219], v169 offset:3072
	ds_read_b128 v[220:223], v169 offset:4096
	ds_read_b128 v[224:227], v169 offset:5120
	ds_read_b128 v[228:231], v169 offset:6144
	ds_read_b128 v[232:235], v169 offset:7168
	global_load_lds_dwordx4 v[236:237], off
	v_lshl_add_u64 v[236:237], v[106:107], 0, s[58:59]
	s_add_i32 m0, s24, 0xe000
	s_nop 0
	global_load_lds_dwordx4 v[236:237], off
	s_waitcnt vmcnt(8)
	s_waitcnt lgkmcnt(0)
	s_barrier
	s_waitcnt lgkmcnt(0)
	v_mfma_f32_16x16x32_bf16 v[140:143], v[154:157], v[204:207], v[140:143]
	v_mfma_f32_16x16x32_bf16 v[136:139], v[180:183], v[204:207], v[136:139]
	v_mfma_f32_16x16x32_bf16 v[124:127], v[154:157], v[212:215], v[124:127]
	v_mfma_f32_16x16x32_bf16 v[120:123], v[180:183], v[212:215], v[120:123]
	v_mfma_f32_16x16x32_bf16 v[100:103], v[154:157], v[220:223], v[100:103]
	v_mfma_f32_16x16x32_bf16 v[96:99], v[180:183], v[220:223], v[96:99]
	v_mfma_f32_16x16x32_bf16 v[76:79], v[154:157], v[228:231], v[76:79]
	v_mfma_f32_16x16x32_bf16 v[72:75], v[180:183], v[228:231], v[72:75]
	v_mfma_f32_16x16x32_bf16 v[140:143], v[176:179], v[208:211], v[140:143]
	v_mfma_f32_16x16x32_bf16 v[136:139], v[184:187], v[208:211], v[136:139]
	v_mfma_f32_16x16x32_bf16 v[124:127], v[176:179], v[216:219], v[124:127]
	v_mfma_f32_16x16x32_bf16 v[120:123], v[184:187], v[216:219], v[120:123]
	v_mfma_f32_16x16x32_bf16 v[100:103], v[176:179], v[224:227], v[100:103]
	v_mfma_f32_16x16x32_bf16 v[96:99], v[184:187], v[224:227], v[96:99]
	v_mfma_f32_16x16x32_bf16 v[76:79], v[176:179], v[232:235], v[76:79]
	v_mfma_f32_16x16x32_bf16 v[72:75], v[184:187], v[232:235], v[72:75]
	v_mfma_f32_16x16x32_bf16 v[132:135], v[188:191], v[204:207], v[132:135]
	v_mfma_f32_16x16x32_bf16 v[128:131], v[196:199], v[204:207], v[128:131]
	v_mfma_f32_16x16x32_bf16 v[116:119], v[188:191], v[212:215], v[116:119]
	v_mfma_f32_16x16x32_bf16 v[112:115], v[196:199], v[212:215], v[112:115]
	v_mfma_f32_16x16x32_bf16 v[84:87], v[188:191], v[220:223], v[84:87]
	v_mfma_f32_16x16x32_bf16 v[80:83], v[196:199], v[220:223], v[80:83]
	v_mfma_f32_16x16x32_bf16 v[68:71], v[188:191], v[228:231], v[68:71]
	v_mfma_f32_16x16x32_bf16 v[64:67], v[196:199], v[228:231], v[64:67]
	v_mfma_f32_16x16x32_bf16 v[132:135], v[192:195], v[208:211], v[132:135]
	v_mfma_f32_16x16x32_bf16 v[128:131], v[200:203], v[208:211], v[128:131]
	v_mfma_f32_16x16x32_bf16 v[116:119], v[192:195], v[216:219], v[116:119]
	v_mfma_f32_16x16x32_bf16 v[112:115], v[200:203], v[216:219], v[112:115]
	v_mfma_f32_16x16x32_bf16 v[84:87], v[192:195], v[224:227], v[84:87]
	v_mfma_f32_16x16x32_bf16 v[80:83], v[200:203], v[224:227], v[80:83]
	v_mfma_f32_16x16x32_bf16 v[68:71], v[192:195], v[232:235], v[68:71]
	v_mfma_f32_16x16x32_bf16 v[64:67], v[200:203], v[232:235], v[64:67]
	s_barrier
	s_add_i32 s4, s72, s17
	v_lshl_add_u64 v[236:237], v[158:159], 0, v[146:147]
	s_mov_b32 m0, s4
	ds_read_b128 v[204:207], v169 offset:16384
	ds_read_b128 v[208:211], v169 offset:17408
	ds_read_b128 v[212:215], v169 offset:18432
	ds_read_b128 v[216:219], v169 offset:19456
	ds_read_b128 v[220:223], v169 offset:20480
	ds_read_b128 v[224:227], v169 offset:21504
	ds_read_b128 v[228:231], v169 offset:22528
	ds_read_b128 v[232:235], v169 offset:23552
	global_load_lds_dwordx4 v[236:237], off
	v_lshl_add_u64 v[236:237], v[158:159], 0, v[144:145]
	s_add_i32 m0, s4, 0x2000
	s_add_i32 s4, s73, s17
	global_load_lds_dwordx4 v[236:237], off
	v_lshl_add_u64 v[236:237], v[158:159], 0, s[28:29]
	v_lshl_add_u64 v[238:239], v[236:237], 0, v[146:147]
	s_mov_b32 m0, s4
	v_lshl_add_u64 v[236:237], v[236:237], 0, v[144:145]
	global_load_lds_dwordx4 v[238:239], off
	s_add_i32 m0, s4, 0x2000
	v_cndmask_b32_e32 v148, v89, v171, vcc
	global_load_lds_dwordx4 v[236:237], off
	s_mov_b32 m0, s24
	v_cndmask_b32_e32 v236, v94, v172, vcc
	global_load_lds_dwordx4 v148, s[60:61]
	s_mov_b32 m0, s25
	v_mov_b32_e32 v237, v149
	global_load_lds_dwordx4 v236, s[60:61]
	s_waitcnt vmcnt(8)
	s_waitcnt lgkmcnt(0)
	v_lshl_add_u64 v[238:239], s[60:61], 0, v[148:149]
	v_lshl_add_u64 v[236:237], s[60:61], 0, v[236:237]
	s_barrier
; #define PG8_STAGE_A(bufoff, base, h, isnext) do { if constexpr (Sched::GATHER) { unsigned vv_[2] = {(isnext) ? vn[h][0] : vc[h][0], (isnext) ? vn[h][1] : vc[h][1]}; PG8_STAGE(bufoff, base, vv_); } else { PG8_STAGE(bufoff, (base) + (h) * hstep, voffA); } } while (0)
; #define PG8_LDA(dst, b, h) do { _Pragma("unroll") for (int m = 0; m < 4; ++m) _Pragma("unroll") for (int k = 0; k < 2; ++k) dst[m][k] = *(const PG8_LAS bf16x8*)(lds + PG8_SA(b, h) + aoff + m * 2048 + k * 1024); } while (0)
; #define PG8_LDB(dst, b, h) do { _Pragma("unroll") for (int n = 0; n < 2; ++n) _Pragma("unroll") for (int k = 0; k < 2; ++k) dst[n][k] = *(const PG8_LAS bf16x8*)(lds + PG8_SB(b, h) + boff + n * 2048 + k * 1024); } while (0)
; #define PG8_MMA(ai, bj, At, Bt) do { __builtin_amdgcn_s_setprio(1); _Pragma("unroll") for (int m = 0; m < 4; ++m) _Pragma("unroll") for (int n = 0; n < 2; ++n) _Pragma("unroll") for (int k = 0; k < 2; ++k) \
;         acc[ai][bj][m][n] = __builtin_amdgcn_mfma_f32_16x16x32_bf16(Bt[n][k], At[m][k], acc[ai][bj][m][n], 0, 0, 0); __builtin_amdgcn_s_setprio(0); } while (0)
; #define PG8_WAIT_V(n) asm volatile("s_waitcnt vmcnt(" #n ")" ::: "memory")
; #define PG8_WAIT_L(n) asm volatile("s_waitcnt lgkmcnt(" #n ")" ::: "memory")
; #define PG8_BAR __builtin_amdgcn_s_barrier()
; #define PG8_SCHED __builtin_amdgcn_sched_barrier(0)
; template <class Epi, class Sched, bool ALIGN_EPI = false, bool SP2 = false>
; __device__ __forceinline__ void gemm_phase(PG8_LAS unsigned char* lds, const Gemm g, const Sched& S, const Epi& E, const int tid_in) {
;     ...
;             PG8_WAIT_V(8); PG8_WAIT_L(0); PG8_BAR; PG8_MMA(1, 0, At, B0); PG8_MMA(1, 1, At, B1); PG8_BAR; PG8_SCHED;
;             PG8_LDB(B0, 1, 0); PG8_LDB(B1, 1, 1); PG8_SCHED; PG8_LDA(At, 1, 0); PG8_STAGE_A(PG8_SA(0, 1), a2, 1, last);
;             PG8_WAIT_V(8); PG8_WAIT_L(0); PG8_BAR; PG8_MMA(0, 0, At, B0); PG8_MMA(0, 1, At, B1); PG8_BAR; PG8_SCHED;
	s_waitcnt lgkmcnt(0)
	v_mfma_f32_16x16x32_bf16 v[60:63], v[154:157], v[204:207], v[60:63]
	v_mfma_f32_16x16x32_bf16 v[56:59], v[180:183], v[204:207], v[56:59]
	v_mfma_f32_16x16x32_bf16 v[44:47], v[154:157], v[212:215], v[44:47]
	v_mfma_f32_16x16x32_bf16 v[32:35], v[180:183], v[212:215], v[32:35]
	v_mfma_f32_16x16x32_bf16 v[20:23], v[154:157], v[220:223], v[20:23]
	v_mfma_f32_16x16x32_bf16 v[16:19], v[180:183], v[220:223], v[16:19]
	v_mfma_f32_16x16x32_bf16 v[4:7], v[154:157], v[228:231], v[4:7]
	v_mfma_f32_16x16x32_bf16 v[0:3], v[180:183], v[228:231], v[0:3]
	v_mfma_f32_16x16x32_bf16 v[60:63], v[176:179], v[208:211], v[60:63]
	v_mfma_f32_16x16x32_bf16 v[56:59], v[184:187], v[208:211], v[56:59]
	v_mfma_f32_16x16x32_bf16 v[44:47], v[176:179], v[216:219], v[44:47]
	v_mfma_f32_16x16x32_bf16 v[32:35], v[184:187], v[216:219], v[32:35]
	v_mfma_f32_16x16x32_bf16 v[20:23], v[176:179], v[224:227], v[20:23]
	v_mfma_f32_16x16x32_bf16 v[16:19], v[184:187], v[224:227], v[16:19]
	v_mfma_f32_16x16x32_bf16 v[4:7], v[176:179], v[232:235], v[4:7]
	v_mfma_f32_16x16x32_bf16 v[0:3], v[184:187], v[232:235], v[0:3]
	v_mfma_f32_16x16x32_bf16 v[52:55], v[188:191], v[204:207], v[52:55]
	v_mfma_f32_16x16x32_bf16 v[48:51], v[196:199], v[204:207], v[48:51]
	v_mfma_f32_16x16x32_bf16 v[36:39], v[188:191], v[212:215], v[36:39]
	v_mfma_f32_16x16x32_bf16 v[40:43], v[196:199], v[212:215], v[40:43]
	v_mfma_f32_16x16x32_bf16 v[24:27], v[188:191], v[220:223], v[24:27]
	v_mfma_f32_16x16x32_bf16 v[28:31], v[196:199], v[220:223], v[28:31]
	v_mfma_f32_16x16x32_bf16 v[8:11], v[188:191], v[228:231], v[8:11]
	v_mfma_f32_16x16x32_bf16 v[12:15], v[196:199], v[228:231], v[12:15]
	v_mfma_f32_16x16x32_bf16 v[52:55], v[192:195], v[208:211], v[52:55]
	v_mfma_f32_16x16x32_bf16 v[48:51], v[200:203], v[208:211], v[48:51]
	v_mfma_f32_16x16x32_bf16 v[36:39], v[192:195], v[216:219], v[36:39]
	v_mfma_f32_16x16x32_bf16 v[40:43], v[200:203], v[216:219], v[40:43]
	v_mfma_f32_16x16x32_bf16 v[24:27], v[192:195], v[224:227], v[24:27]
	v_mfma_f32_16x16x32_bf16 v[28:31], v[200:203], v[224:227], v[28:31]
	v_mfma_f32_16x16x32_bf16 v[8:11], v[192:195], v[232:235], v[8:11]
	v_mfma_f32_16x16x32_bf16 v[12:15], v[200:203], v[232:235], v[12:15]
	s_barrier
	s_add_i32 s4, 0, 0x18000
	v_add_u32_e32 v91, s4, v165
	s_add_i32 s19, 0, 0x1c000
	ds_read_b128 v[154:157], v91
	ds_read_b128 v[176:179], v91 offset:1024
	ds_read_b128 v[180:183], v91 offset:2048
	ds_read_b128 v[184:187], v91 offset:3072
	v_add_u32_e32 v91, s19, v165
	ds_read_b128 v[188:191], v91
	ds_read_b128 v[192:195], v91 offset:1024
	ds_read_b128 v[196:199], v91 offset:2048
	ds_read_b128 v[200:203], v91 offset:3072
	s_mov_b32 m0, s57
	v_cndmask_b32_e32 v91, v92, v173, vcc
	ds_read_b128 v[204:207], v169 offset:32768
	ds_read_b128 v[208:211], v169 offset:33792
	ds_read_b128 v[212:215], v169 offset:34816
	ds_read_b128 v[216:219], v169 offset:35840
	ds_read_b128 v[220:223], v169 offset:36864
	ds_read_b128 v[224:227], v169 offset:37888
	ds_read_b128 v[228:231], v169 offset:38912
	ds_read_b128 v[232:235], v169 offset:39936
	v_cndmask_b32_e32 v93, v90, v174, vcc
	global_load_lds_dwordx4 v91, s[60:61]
	s_mov_b32 m0, s67
	s_nop 0
	global_load_lds_dwordx4 v93, s[60:61]
	s_waitcnt vmcnt(8)
	s_waitcnt lgkmcnt(0)
	s_barrier
	s_waitcnt lgkmcnt(0)
	v_mfma_f32_16x16x32_bf16 v[140:143], v[154:157], v[204:207], v[140:143]
	v_mfma_f32_16x16x32_bf16 v[136:139], v[180:183], v[204:207], v[136:139]
	v_mfma_f32_16x16x32_bf16 v[124:127], v[154:157], v[212:215], v[124:127]
	v_mfma_f32_16x16x32_bf16 v[120:123], v[180:183], v[212:215], v[120:123]
	v_mfma_f32_16x16x32_bf16 v[100:103], v[154:157], v[220:223], v[100:103]
	v_mfma_f32_16x16x32_bf16 v[96:99], v[180:183], v[220:223], v[96:99]
	v_mfma_f32_16x16x32_bf16 v[76:79], v[154:157], v[228:231], v[76:79]
	v_mfma_f32_16x16x32_bf16 v[72:75], v[180:183], v[228:231], v[72:75]
	v_mfma_f32_16x16x32_bf16 v[140:143], v[176:179], v[208:211], v[140:143]
	v_mfma_f32_16x16x32_bf16 v[136:139], v[184:187], v[208:211], v[136:139]
	v_mfma_f32_16x16x32_bf16 v[124:127], v[176:179], v[216:219], v[124:127]
	v_mfma_f32_16x16x32_bf16 v[120:123], v[184:187], v[216:219], v[120:123]
	v_mfma_f32_16x16x32_bf16 v[100:103], v[176:179], v[224:227], v[100:103]
	v_mfma_f32_16x16x32_bf16 v[96:99], v[184:187], v[224:227], v[96:99]
	v_mfma_f32_16x16x32_bf16 v[76:79], v[176:179], v[232:235], v[76:79]
	v_mfma_f32_16x16x32_bf16 v[72:75], v[184:187], v[232:235], v[72:75]
	v_mfma_f32_16x16x32_bf16 v[132:135], v[188:191], v[204:207], v[132:135]
	v_mfma_f32_16x16x32_bf16 v[128:131], v[196:199], v[204:207], v[128:131]
	v_mfma_f32_16x16x32_bf16 v[116:119], v[188:191], v[212:215], v[116:119]
	v_mfma_f32_16x16x32_bf16 v[112:115], v[196:199], v[212:215], v[112:115]
	v_mfma_f32_16x16x32_bf16 v[84:87], v[188:191], v[220:223], v[84:87]
	v_mfma_f32_16x16x32_bf16 v[80:83], v[196:199], v[220:223], v[80:83]
	v_mfma_f32_16x16x32_bf16 v[68:71], v[188:191], v[228:231], v[68:71]
	v_mfma_f32_16x16x32_bf16 v[64:67], v[196:199], v[228:231], v[64:67]
	v_mfma_f32_16x16x32_bf16 v[132:135], v[192:195], v[208:211], v[132:135]
	v_mfma_f32_16x16x32_bf16 v[128:131], v[200:203], v[208:211], v[128:131]
	v_mfma_f32_16x16x32_bf16 v[116:119], v[192:195], v[216:219], v[116:119]
	v_mfma_f32_16x16x32_bf16 v[112:115], v[200:203], v[216:219], v[112:115]
	v_mfma_f32_16x16x32_bf16 v[84:87], v[192:195], v[224:227], v[84:87]
	v_mfma_f32_16x16x32_bf16 v[80:83], v[200:203], v[224:227], v[80:83]
	v_mfma_f32_16x16x32_bf16 v[68:71], v[192:195], v[232:235], v[68:71]
	v_mfma_f32_16x16x32_bf16 v[64:67], v[200:203], v[232:235], v[64:67]
	s_barrier
; #define PG8_STAGE(bufoff, gbase, voff) do { _Pragma("unroll") for (int _i = 0; _i < 2; ++_i) \
;         __builtin_amdgcn_global_load_lds((const unsigned*)((const char*)(gbase) + (voff)[_i]), (PG8_LAS unsigned*)(lds + (bufoff) + ldsw + _i * 8192), 16, 0, 0); } while (0)
; #define PG8_STAGE_A(bufoff, base, h, isnext) do { if constexpr (Sched::GATHER) { unsigned vv_[2] = {(isnext) ? vn[h][0] : vc[h][0], (isnext) ? vn[h][1] : vc[h][1]}; PG8_STAGE(bufoff, base, vv_); } else { PG8_STAGE(bufoff, (base) + (h) * hstep, voffA); } } while (0)
; #define PG8_LDA(dst, b, h) do { _Pragma("unroll") for (int m = 0; m < 4; ++m) _Pragma("unroll") for (int k = 0; k < 2; ++k) dst[m][k] = *(const PG8_LAS bf16x8*)(lds + PG8_SA(b, h) + aoff + m * 2048 + k * 1024); } while (0)
; #define PG8_MMA(ai, bj, At, Bt) do { __builtin_amdgcn_s_setprio(1); _Pragma("unroll") for (int m = 0; m < 4; ++m) _Pragma("unroll") for (int n = 0; n < 2; ++n) _Pragma("unroll") for (int k = 0; k < 2; ++k) \
;         acc[ai][bj][m][n] = __builtin_amdgcn_mfma_f32_16x16x32_bf16(Bt[n][k], At[m][k], acc[ai][bj][m][n], 0, 0, 0); __builtin_amdgcn_s_setprio(0); } while (0)
; #define PG8_WAIT_V(n) asm volatile("s_waitcnt vmcnt(" #n ")" ::: "memory")
; #define PG8_WAIT_L(n) asm volatile("s_waitcnt lgkmcnt(" #n ")" ::: "memory")
; #define PG8_BAR __builtin_amdgcn_s_barrier()
; #define PG8_SCHED __builtin_amdgcn_sched_barrier(0)
; template <class Epi, class Sched, bool ALIGN_EPI = false, bool SP2 = false>
; __device__ __forceinline__ void gemm_phase(PG8_LAS unsigned char* lds, const Gemm g, const Sched& S, const Epi& E, const int tid_in) {
;     ...
;         for (int t = (Epi::HAS_MID && seg == 1) ? nt / 2 : 0; t < ((Epi::HAS_MID && seg == 0) ? nt / 2 : nt); t += 2) {
;     ...
;             PG8_LDA(At, 1, 1); PG8_STAGE(PG8_SB(1, 0), b3, voffB); PG8_STAGE(PG8_SB(1, 1), b3 + hstepB, voffB); PG8_STAGE_A(PG8_SA(1, 0), a3, 0, last);
;             PG8_WAIT_V(8); PG8_WAIT_L(0); PG8_BAR; PG8_MMA(1, 0, At, B0); PG8_MMA(1, 1, At, B1); PG8_BAR; PG8_SCHED;
	v_lshl_add_u64 v[240:241], v[158:159], 0, s[34:35]
	s_add_i32 s4, s4, s17
	v_lshl_add_u64 v[242:243], v[240:241], 0, v[146:147]
	s_mov_b32 m0, s4
	ds_read_b128 v[204:207], v169 offset:49152
	ds_read_b128 v[208:211], v169 offset:50176
	ds_read_b128 v[212:215], v169 offset:51200
	ds_read_b128 v[216:219], v169 offset:52224
	ds_read_b128 v[220:223], v169 offset:53248
	ds_read_b128 v[224:227], v169 offset:54272
	ds_read_b128 v[228:231], v169 offset:55296
	ds_read_b128 v[232:235], v169 offset:56320
	global_load_lds_dwordx4 v[242:243], off
	v_lshl_add_u64 v[240:241], v[240:241], 0, v[144:145]
	s_add_i32 m0, s4, 0x2000
	v_lshl_add_u64 v[158:159], v[158:159], 0, s[38:39]
	s_add_i32 s4, s19, s17
	global_load_lds_dwordx4 v[240:241], off
	v_lshl_add_u64 v[240:241], v[158:159], 0, v[146:147]
	s_mov_b32 m0, s4
	v_lshl_add_u64 v[158:159], v[158:159], 0, v[144:145]
	global_load_lds_dwordx4 v[240:241], off
	s_add_i32 m0, s4, 0x2000
	s_nop 0
	global_load_lds_dwordx4 v[158:159], off
	v_lshl_add_u64 v[158:159], v[238:239], 0, s[44:45]
	s_mov_b32 m0, s70
	s_nop 0
	global_load_lds_dwordx4 v[158:159], off
	v_lshl_add_u64 v[158:159], v[236:237], 0, s[44:45]
	s_mov_b32 m0, s71
	s_nop 0
	global_load_lds_dwordx4 v[158:159], off
	s_waitcnt vmcnt(8)
	s_waitcnt lgkmcnt(0)
	s_barrier
	s_waitcnt lgkmcnt(0)
	v_mfma_f32_16x16x32_bf16 v[60:63], v[154:157], v[204:207], v[60:63]
	v_mfma_f32_16x16x32_bf16 v[56:59], v[180:183], v[204:207], v[56:59]
	v_mfma_f32_16x16x32_bf16 v[44:47], v[154:157], v[212:215], v[44:47]
	v_mfma_f32_16x16x32_bf16 v[32:35], v[180:183], v[212:215], v[32:35]
	v_mfma_f32_16x16x32_bf16 v[20:23], v[154:157], v[220:223], v[20:23]
	v_mfma_f32_16x16x32_bf16 v[16:19], v[180:183], v[220:223], v[16:19]
	v_mfma_f32_16x16x32_bf16 v[4:7], v[154:157], v[228:231], v[4:7]
	v_mfma_f32_16x16x32_bf16 v[0:3], v[180:183], v[228:231], v[0:3]
	v_mfma_f32_16x16x32_bf16 v[60:63], v[176:179], v[208:211], v[60:63]
	v_mfma_f32_16x16x32_bf16 v[56:59], v[184:187], v[208:211], v[56:59]
	v_mfma_f32_16x16x32_bf16 v[44:47], v[176:179], v[216:219], v[44:47]
	v_mfma_f32_16x16x32_bf16 v[32:35], v[184:187], v[216:219], v[32:35]
	v_mfma_f32_16x16x32_bf16 v[20:23], v[176:179], v[224:227], v[20:23]
	v_mfma_f32_16x16x32_bf16 v[16:19], v[184:187], v[224:227], v[16:19]
	v_mfma_f32_16x16x32_bf16 v[4:7], v[176:179], v[232:235], v[4:7]
	v_mfma_f32_16x16x32_bf16 v[0:3], v[184:187], v[232:235], v[0:3]
	v_mfma_f32_16x16x32_bf16 v[52:55], v[188:191], v[204:207], v[52:55]
	v_mfma_f32_16x16x32_bf16 v[48:51], v[196:199], v[204:207], v[48:51]
	v_mfma_f32_16x16x32_bf16 v[36:39], v[188:191], v[212:215], v[36:39]
	v_mfma_f32_16x16x32_bf16 v[40:43], v[196:199], v[212:215], v[40:43]
	v_mfma_f32_16x16x32_bf16 v[24:27], v[188:191], v[220:223], v[24:27]
	v_mfma_f32_16x16x32_bf16 v[28:31], v[196:199], v[220:223], v[28:31]
	v_mfma_f32_16x16x32_bf16 v[8:11], v[188:191], v[228:231], v[8:11]
	v_mfma_f32_16x16x32_bf16 v[12:15], v[196:199], v[228:231], v[12:15]
	v_mfma_f32_16x16x32_bf16 v[52:55], v[192:195], v[208:211], v[52:55]
	v_mfma_f32_16x16x32_bf16 v[48:51], v[200:203], v[208:211], v[48:51]
	v_mfma_f32_16x16x32_bf16 v[36:39], v[192:195], v[216:219], v[36:39]
	v_mfma_f32_16x16x32_bf16 v[40:43], v[200:203], v[216:219], v[40:43]
	v_mfma_f32_16x16x32_bf16 v[24:27], v[192:195], v[224:227], v[24:27]
	v_mfma_f32_16x16x32_bf16 v[28:31], v[200:203], v[224:227], v[28:31]
	v_mfma_f32_16x16x32_bf16 v[8:11], v[192:195], v[232:235], v[8:11]
	v_mfma_f32_16x16x32_bf16 v[12:15], v[200:203], v[232:235], v[12:15]
	s_barrier
	s_add_i32 s18, s18, 2
	s_add_u32 s58, s58, 0x100
	s_addc_u32 s59, s59, 0
	s_cmp_gt_u32 s18, 29
	v_lshl_add_u64 v[104:105], v[104:105], 0, s[42:43]
	s_cbranch_scc0 .LBB0_2300
	s_and_b64 vcc, exec, s[40:41]
	s_cbranch_vccz .LBB0_2303
	s_barrier

; #define PG8_BAR __builtin_amdgcn_s_barrier()
;     __device__ __forceinline__ bool next(int i, Unit& u) const {
;         if (i + i0 >= imax) return false; const long L = (long)(i + i0) * G + c; if (L >= nwg) return false;
; template <class Epi, class Sched, bool ALIGN_EPI = false, bool SP2 = false>
; __device__ __forceinline__ void gemm_phase(PG8_LAS unsigned char* lds, const Gemm g, const Sched& S, const Epi& E, const int tid_in) {
;     const int tid = tid_in, wid = __builtin_amdgcn_readfirstlane(tid >> 6), lane = tid & 63, wr = wid >> 2, wc = wid & 3, fr = lane & 15, fq = lane >> 4;
;     const int K = g.K, nt = K / BK, LDB = g.btiled ? 64 : K;
;     unsigned voffA[2], voffB[2]; unsigned vc[2][2] = {{0u, 0u}, {0u, 0u}}, vn[2][2] = {{0u, 0u}, {0u, 0u}}; int gR[2], gC[2];
; #pragma unroll
;     for (int i = 0; i < 2; ++i) { int R, C; stage_rc(tid * 16 + i * 8192, R, C); const int Rb = Epi::PERM ? ((R & ~31) + perm32(R & 31)) : R;
;         voffA[i] = (unsigned)(R * K + C) * 2u; voffB[i] = (unsigned)(Rb * LDB + C) * 2u; gR[i] = R; gC[i] = C * 2; }
;     const size_t kstep = (size_t)(BK * 2);
;     const size_t hstep = (size_t)HALF * K * 2;
;     const size_t tstep = 2 * hstep; const size_t kstepB = g.btiled ? (size_t)32768 : kstep, hstepB = g.btiled ? (size_t)16384 : hstep;
;     const unsigned ldsw = (unsigned)wid * 1024u;
;     const int aoff = lds_byte(wr * 64 + fr, fq * 8), boff = lds_byte(wc * 32 + fr, fq * 8);
;     ...
;     Unit cur, nxt; int ui = 0;
;     if (!S.next(0, cur)) return;
;     f32x4 acc[2][2][4][2];
; #pragma unroll
;     for (int a = 0; a < 2; ++a)
; #pragma unroll
;         for (int b = 0; b < 2; ++b)
; #pragma unroll
;             for (int m = 0; m < 4; ++m)
; #pragma unroll
;                 for (int n = 0; n < 2; ++n) acc[a][b][m][n] = (f32x4){0.f, 0.f, 0.f, 0.f};
;     bf16x8 At[4][2], B0[2][2], B1[2][2];
;     const char* cA = (const char*)g.A + (Sched::GATHER ? (size_t)0 : (size_t)cur.pm * tstep); if constexpr (Sched::GATHER) PG8_GFILL(vc, 0); const char* cB = (const char*)g.Bt + (size_t)cur.pn * tstep + (size_t)cur.e * g.estride;
;     S.a_ready(cur);
;     if constexpr (SP2) {
;         PG8_STAGE(PG8_SB(0, 0), cB, voffB); PG8_STAGE(PG8_SB(0, 1), cB + hstepB, voffB); PG8_STAGE_A(PG8_SA(0, 0), cA, 0, false); PG8_STAGE_A(PG8_SA(0, 1), cA, 1, false);
;         if (wr == 1) PG8_BAR;
.LBB0_3485:
	s_add_i32 s4, 0, 0x26e80
	s_waitcnt vmcnt(0)
	v_mov_b32_e32 v0, s4
	ds_read_b32 v0, v0
	s_waitcnt lgkmcnt(0)
	v_mbcnt_lo_u32_b32 v6, -1, 0
	v_mbcnt_hi_u32_b32 v6, -1, v6
	v_lshlrev_b32_e32 v144, 3, v0
	v_readfirstlane_b32 s17, v0
	v_add_u32_e32 v0, s33, v6
	v_cmp_ge_i32_e32 vcc, s81, v144
	v_readfirstlane_b32 s4, v0
	s_cbranch_vccnz .LBB0_3502
	v_lshlrev_b32_e32 v1, 4, v0
	v_add_u32_e32 v2, 0x2000, v1
	v_ashrrev_i32_e32 v3, 31, v2
	v_lshrrev_b32_e32 v3, 22, v3
	v_add_u32_e32 v3, v2, v3
	v_ashrrev_i32_e32 v7, 10, v3
	v_mul_i32_i24_e32 v3, 0x400, v7
	v_sub_u32_e32 v2, v2, v3
	v_lshrrev_b32_e32 v3, 4, v2
	v_bitop3_b32 v2, v3, v2, 32 bitop3:0x6c
	v_ashrrev_i32_e32 v3, 31, v2
	v_lshrrev_b32_e32 v3, 26, v3
	v_add_u32_e32 v3, v2, v3
	v_lshlrev_b32_e32 v4, 3, v7
	v_ashrrev_i32_e32 v8, 6, v3
	v_and_b32_e32 v4, -16, v4
	v_add_u32_e32 v4, v8, v4
	v_and_b32_e32 v5, 3, v8
	s_mov_b32 s12, 0x1ffffe0
	v_lshrrev_b32_e32 v9, 2, v4
	v_lshlrev_b32_e32 v10, 1, v4
	v_and_b32_e32 v3, 0xc0, v3
	v_and_or_b32 v5, v4, s12, v5
	v_and_b32_e32 v9, 4, v9
	v_and_b32_e32 v10, 24, v10
	v_sub_u32_e32 v2, v2, v3
	v_mov_b32_e32 v3, 1
	v_or3_b32 v5, v5, v9, v10
	v_lshlrev_b32_e32 v9, 5, v7
	v_ashrrev_i16_sdwa v2, v3, sext(v2) dst_sel:DWORD dst_unused:UNUSED_PAD src0_sel:DWORD src1_sel:BYTE_0
	v_and_b32_e32 v10, 32, v9
	v_bfe_i32 v9, v2, 0, 16
	v_add_lshl_u32 v2, v10, v9, 1
	v_lshl_add_u32 v146, v5, 7, v2
	v_lshl_add_u32 v148, v4, 12, v2
	v_bfe_i32 v2, v0, 27, 1
	v_lshrrev_b32_e32 v2, 22, v2
	v_add_u32_e32 v2, v1, v2
	s_add_u32 s22, s8, 0x64000000
	v_and_b32_e32 v2, 0xfffffc00, v2
	s_addc_u32 s23, s9, 0
	v_sub_u32_e32 v1, v1, v2
	s_add_u32 s24, s8, 0x26000000
	v_lshrrev_b32_e32 v2, 4, v1
	v_ashrrev_i32_e32 v4, 31, v0
	s_addc_u32 s25, s9, 0
	s_ashr_i32 s61, s81, 31
	v_bitop3_b32 v1, v2, v1, 32 bitop3:0x6c
	v_lshrrev_b32_e32 v4, 26, v4
	s_lshr_b32 s6, s61, 29
	v_ashrrev_i32_e32 v2, 31, v1
	v_add_u32_e32 v0, v0, v4
	s_add_i32 s6, s81, s6
	v_lshrrev_b32_e32 v2, 26, v2
	v_ashrrev_i32_e32 v11, 6, v0
	s_ashr_i32 s5, s4, 6
	s_ashr_i32 s7, s6, 3
	s_and_b32 s6, s6, -8
	v_add_u32_e32 v2, v1, v2
	v_lshlrev_b32_e32 v0, 3, v11
	s_ashr_i32 s20, s4, 8
	s_lshl_b32 s60, s5, 10
	s_sub_i32 s6, s81, s6
	s_add_i32 s62, s17, 1
	v_ashrrev_i32_e32 v10, 6, v2
	v_and_b32_e32 v0, -16, v0
	s_cmp_lt_i32 s6, 0
	v_add_u32_e32 v4, v10, v0
	v_and_b32_e32 v0, 3, v10
	v_and_or_b32 v0, v4, s12, v0
	s_cselect_b32 s12, s62, s17
	s_mul_i32 s6, s12, s6
	s_add_i32 s6, s6, s7
	s_ashr_i32 s7, s6, 31
	s_lshr_b32 s7, s7, 29
	s_add_i32 s7, s6, s7
	s_ashr_i32 s7, s7, 3
	v_lshrrev_b32_e32 v5, 2, v4
	v_lshlrev_b32_e32 v12, 1, v4
	s_lshl_b32 s7, s7, 2
	s_add_i32 s63, 0, 0x26c00
	v_and_b32_e32 v5, 4, v5
	v_and_b32_e32 v12, 24, v12
	s_add_i32 s7, s63, s7
	v_or3_b32 v5, v0, v5, v12
	v_mov_b32_e32 v12, s7
	ds_read_b32 v128, v12
	v_lshlrev_b32_e32 v0, 5, v11
	v_and_b32_e32 v13, 32, v0
	v_and_b32_e32 v0, 0xc0, v2
	v_sub_u32_e32 v0, v1, v0
	v_ashrrev_i16_sdwa v2, v3, sext(v0) dst_sel:DWORD dst_unused:UNUSED_PAD src0_sel:DWORD src1_sel:BYTE_0
	s_waitcnt lgkmcnt(0)
	v_lshlrev_b32_e32 v0, 2, v128
	v_add_u32_e32 v0, s63, v0
	ds_read2st64_b32 v[0:1], v0 offset0:4 offset1:5
	v_ashrrev_i32_e32 v129, 31, v128
	v_bfe_i32 v12, v2, 0, 16
	v_add_lshl_u32 v2, v13, v12, 1
	v_lshl_add_u32 v150, v5, 7, v2
	s_waitcnt lgkmcnt(0)
	v_readfirstlane_b32 s7, v1
	s_addk_i32 s7, 0xff
	s_ashr_i32 s7, s7, 8
	s_abs_i32 s12, s7
	v_cvt_f32_u32_e32 v1, s12
	v_readfirstlane_b32 s13, v0
	s_ashr_i32 s13, s13, 8
	s_sub_i32 s18, 0, s12
	v_rcp_iflag_f32_e32 v0, v1
	s_lshl_b32 s14, s13, 3
	s_sub_i32 s6, s6, s14
	s_abs_i32 s15, s6
	v_mul_f32_e32 v0, 0x4f7ffffe, v0
	v_cvt_u32_f32_e32 v0, v0
	s_xor_b32 s14, s6, s7
	s_ashr_i32 s14, s14, 31
	v_lshl_add_u32 v152, v4, 12, v2
	v_readfirstlane_b32 s19, v0
	s_mul_i32 s18, s18, s19
	s_mul_hi_u32 s18, s19, s18
	s_add_i32 s19, s19, s18
	s_mul_hi_u32 s18, s15, s19
	s_mul_i32 s19, s18, s12
	s_sub_i32 s15, s15, s19
	s_add_i32 s19, s18, 1
	s_sub_i32 s21, s15, s12
	s_cmp_ge_u32 s15, s12
	s_cselect_b32 s18, s19, s18
	s_cselect_b32 s15, s21, s15
	s_add_i32 s19, s18, 1
	s_cmp_ge_u32 s15, s12
	s_cselect_b32 s12, s19, s18
	s_xor_b32 s12, s12, s14
	s_sub_i32 s54, s12, s14
	s_mul_i32 s7, s54, s7
	s_sub_i32 s6, s6, s7
	s_add_i32 s52, s6, s13
	s_ashr_i32 s53, s52, 31
	s_ashr_i32 s55, s54, 31
	s_lshl_b64 s[12:13], s[52:53], 20
	s_lshl_b64 s[6:7], s[54:55], 20
	s_add_u32 s6, s24, s6
	s_addc_u32 s7, s25, s7
	v_lshlrev_b64 v[0:1], 23, v[128:129]
	v_lshl_add_u64 v[0:1], s[6:7], 0, v[0:1]
	s_add_i32 s18, s60, 0
	s_add_i32 m0, s18, 0x10000
	v_readfirstlane_b32 s6, v0
	v_readfirstlane_b32 s7, v1
	s_load_dwordx2 s[10:11], s[10:11], 0xb0
	v_mov_b32_e32 v151, 0
	v_mov_b32_e32 v153, v151
	v_mov_b32_e32 v149, v151
	v_mov_b32_e32 v147, v151
	global_load_lds_dwordx4 v150, s[6:7]
	s_add_i32 m0, s18, 0x12000
	s_nop 0
	global_load_lds_dwordx4 v146, s[6:7]
	s_mov_b64 s[6:7], 0x4000
	v_lshl_add_u64 v[2:3], v[0:1], 0, s[6:7]
	s_add_i32 m0, s18, 0x14000
	v_readfirstlane_b32 s14, v2
	v_readfirstlane_b32 s15, v3
	s_nop 4
	global_load_lds_dwordx4 v150, s[14:15]
	s_add_i32 m0, s18, 0x16000
	s_add_u32 s56, s22, s12
	s_addc_u32 s57, s23, s13
	s_add_i32 s19, s18, 0x2000
	global_load_lds_dwordx4 v146, s[14:15]
	s_mov_b32 m0, s18
	s_add_u32 s12, s56, 0x80000
	global_load_lds_dwordx4 v152, s[56:57]
	s_mov_b32 m0, s19
	s_addc_u32 s13, s57, 0
	s_add_i32 s53, s18, 0x4000
	global_load_lds_dwordx4 v148, s[56:57]
	s_mov_b32 m0, s53
	s_add_i32 s55, s18, 0x6000
	global_load_lds_dwordx4 v152, s[12:13]
	s_mov_b32 m0, s55
	s_cmp_eq_u32 s20, 1
	global_load_lds_dwordx4 v148, s[12:13]
	v_lshl_add_u64 v[4:5], s[56:57], 0, v[152:153]
	v_lshl_add_u64 v[2:3], s[56:57], 0, v[148:149]
	s_cselect_b64 s[12:13], -1, 0
	s_cmp_lg_u32 s20, 1
	s_mov_b64 s[14:15], 0x80000
	s_setprio 0
	s_cbranch_scc1 .LBB0_3488
	s_setprio 1
	s_barrier

; #define PG8_STAGE(bufoff, gbase, voff) do { _Pragma("unroll") for (int _i = 0; _i < 2; ++_i) \
;         __builtin_amdgcn_global_load_lds((const unsigned*)((const char*)(gbase) + (voff)[_i]), (PG8_LAS unsigned*)(lds + (bufoff) + ldsw + _i * 8192), 16, 0, 0); } while (0)
; #define PG8_STAGE_A(bufoff, base, h, isnext) do { if constexpr (Sched::GATHER) { unsigned vv_[2] = {(isnext) ? vn[h][0] : vc[h][0], (isnext) ? vn[h][1] : vc[h][1]}; PG8_STAGE(bufoff, base, vv_); } else { PG8_STAGE(bufoff, (base) + (h) * hstep, voffA); } } while (0)
; #define PG8_LDA(dst, b, h) do { _Pragma("unroll") for (int m = 0; m < 4; ++m) _Pragma("unroll") for (int k = 0; k < 2; ++k) dst[m][k] = *(const PG8_LAS bf16x8*)(lds + PG8_SA(b, h) + aoff + m * 2048 + k * 1024); } while (0)
; #define PG8_LDB(dst, b, h) do { _Pragma("unroll") for (int n = 0; n < 2; ++n) _Pragma("unroll") for (int k = 0; k < 2; ++k) dst[n][k] = *(const PG8_LAS bf16x8*)(lds + PG8_SB(b, h) + boff + n * 2048 + k * 1024); } while (0)
; #define PG8_WAIT_V(n) asm volatile("s_waitcnt vmcnt(" #n ")" ::: "memory")
; #define PG8_WAIT_L(n) asm volatile("s_waitcnt lgkmcnt(" #n ")" ::: "memory")
; #define PG8_BAR __builtin_amdgcn_s_barrier()
; #define PG8_SCHED __builtin_amdgcn_sched_barrier(0)
; template <class Epi, class Sched, bool ALIGN_EPI = false, bool SP2 = false>
; __device__ __forceinline__ void gemm_phase(PG8_LAS unsigned char* lds, const Gemm g, const Sched& S, const Epi& E, const int tid_in) {
;     ...
;             const bool last = (t == nt - 2);
;             const char* a1 = cA + (size_t)(t + 1) * kstep;
;             const char* a2 = last ? nA : cA + (size_t)(t + 2) * kstep; const char* b2 = last ? nB : cB + (size_t)(t + 2) * kstepB;
;             const char* a3 = a2 + kstep; const char* b3 = b2 + kstepB;
;             if (last && has_next) S.a_ready(nxt);
;             if constexpr (SP2) {
;             PG8_LDB(B0, 0, 0); PG8_LDB(B1, 0, 1); PG8_SCHED; PG8_LDA(At, 0, 0); PG8_STAGE_A(PG8_SA(1, 1), a1, 1, false);
;             PG8_WAIT_V(8); PG8_WAIT_L(0); PG8_BAR; PG8_MMA(0, 0, At, B0); PG8_MMA(0, 1, At, B1); PG8_BAR; PG8_SCHED;
;             PG8_LDA(At, 0, 1); PG8_STAGE(PG8_SB(0, 0), b2, voffB); PG8_STAGE(PG8_SB(0, 1), b2 + hstepB, voffB); PG8_STAGE_A(PG8_SA(0, 0), a2, 0, last);
;             PG8_WAIT_V(8); PG8_WAIT_L(0); PG8_BAR; PG8_MMA(1, 0, At, B0); PG8_MMA(1, 1, At, B1); PG8_BAR; PG8_SCHED;
.LBB0_3495:
	ds_read_b128 v[134:137], v167
	ds_read_b128 v[138:141], v167 offset:1024
	ds_read_b128 v[170:173], v167 offset:2048
	ds_read_b128 v[174:177], v167 offset:3072
	ds_read_b128 v[178:181], v168
	ds_read_b128 v[182:185], v168 offset:1024
	ds_read_b128 v[186:189], v168 offset:2048
	ds_read_b128 v[190:193], v168 offset:3072
	s_add_u32 s4, s56, 0xfff80080
	s_addc_u32 s45, s57, -1
	s_cmp_eq_u32 s21, 28
	s_cselect_b64 vcc, -1, 0
	s_cselect_b32 s59, s5, s45
	s_cselect_b32 s58, s20, s4
	v_cndmask_b32_e32 v143, v131, v129, vcc
	v_cndmask_b32_e32 v142, v130, v132, vcc
	v_lshl_add_u64 v[162:163], s[56:57], 0, v[154:155]
	s_add_i32 m0, s18, 0xc000
	ds_read_b128 v[194:197], v169
	ds_read_b128 v[198:201], v169 offset:1024
	ds_read_b128 v[202:205], v169 offset:2048
	ds_read_b128 v[206:209], v169 offset:3072
	ds_read_b128 v[210:213], v169 offset:4096
	ds_read_b128 v[214:217], v169 offset:5120
	ds_read_b128 v[218:221], v169 offset:6144
	ds_read_b128 v[222:225], v169 offset:7168
	global_load_lds_dwordx4 v[162:163], off
	v_lshl_add_u64 v[162:163], s[56:57], 0, v[156:157]
	s_add_i32 m0, s18, 0xe000
	s_nop 0
	global_load_lds_dwordx4 v[162:163], off
	s_waitcnt vmcnt(8)
	s_waitcnt lgkmcnt(0)
	s_barrier
	s_waitcnt lgkmcnt(0)
	v_mfma_f32_16x16x32_bf16 v[124:127], v[134:137], v[194:197], v[124:127]
	v_mfma_f32_16x16x32_bf16 v[120:123], v[170:173], v[194:197], v[120:123]
	v_mfma_f32_16x16x32_bf16 v[116:119], v[134:137], v[202:205], v[116:119]
	v_mfma_f32_16x16x32_bf16 v[112:115], v[170:173], v[202:205], v[112:115]
	v_mfma_f32_16x16x32_bf16 v[108:111], v[134:137], v[210:213], v[108:111]
	v_mfma_f32_16x16x32_bf16 v[100:103], v[170:173], v[210:213], v[100:103]
	v_mfma_f32_16x16x32_bf16 v[92:95], v[134:137], v[218:221], v[92:95]
	v_mfma_f32_16x16x32_bf16 v[84:87], v[170:173], v[218:221], v[84:87]
	v_mfma_f32_16x16x32_bf16 v[124:127], v[138:141], v[198:201], v[124:127]
	v_mfma_f32_16x16x32_bf16 v[120:123], v[174:177], v[198:201], v[120:123]
	v_mfma_f32_16x16x32_bf16 v[116:119], v[138:141], v[206:209], v[116:119]
	v_mfma_f32_16x16x32_bf16 v[112:115], v[174:177], v[206:209], v[112:115]
	v_mfma_f32_16x16x32_bf16 v[108:111], v[138:141], v[214:217], v[108:111]
	v_mfma_f32_16x16x32_bf16 v[100:103], v[174:177], v[214:217], v[100:103]
	v_mfma_f32_16x16x32_bf16 v[92:95], v[138:141], v[222:225], v[92:95]
	v_mfma_f32_16x16x32_bf16 v[84:87], v[174:177], v[222:225], v[84:87]
	v_mfma_f32_16x16x32_bf16 v[104:107], v[178:181], v[194:197], v[104:107]
	v_mfma_f32_16x16x32_bf16 v[96:99], v[186:189], v[194:197], v[96:99]
	v_mfma_f32_16x16x32_bf16 v[88:91], v[178:181], v[202:205], v[88:91]
	v_mfma_f32_16x16x32_bf16 v[80:83], v[186:189], v[202:205], v[80:83]
	v_mfma_f32_16x16x32_bf16 v[76:79], v[178:181], v[210:213], v[76:79]
	v_mfma_f32_16x16x32_bf16 v[72:75], v[186:189], v[210:213], v[72:75]
	v_mfma_f32_16x16x32_bf16 v[68:71], v[178:181], v[218:221], v[68:71]
	v_mfma_f32_16x16x32_bf16 v[64:67], v[186:189], v[218:221], v[64:67]
	v_mfma_f32_16x16x32_bf16 v[104:107], v[182:185], v[198:201], v[104:107]
	v_mfma_f32_16x16x32_bf16 v[96:99], v[190:193], v[198:201], v[96:99]
	v_mfma_f32_16x16x32_bf16 v[88:91], v[182:185], v[206:209], v[88:91]
	v_mfma_f32_16x16x32_bf16 v[80:83], v[190:193], v[206:209], v[80:83]
	v_mfma_f32_16x16x32_bf16 v[76:79], v[182:185], v[214:217], v[76:79]
	v_mfma_f32_16x16x32_bf16 v[72:75], v[190:193], v[214:217], v[72:75]
	v_mfma_f32_16x16x32_bf16 v[68:71], v[182:185], v[222:225], v[68:71]
	v_mfma_f32_16x16x32_bf16 v[64:67], v[190:193], v[222:225], v[64:67]
	s_barrier
	s_add_i32 s4, s68, s60
	v_lshl_add_u64 v[162:163], v[142:143], 0, v[150:151]
	s_mov_b32 m0, s4
	ds_read_b128 v[194:197], v169 offset:16384
	ds_read_b128 v[198:201], v169 offset:17408
	ds_read_b128 v[202:205], v169 offset:18432
	ds_read_b128 v[206:209], v169 offset:19456
	ds_read_b128 v[210:213], v169 offset:20480
	ds_read_b128 v[214:217], v169 offset:21504
	ds_read_b128 v[218:221], v169 offset:22528
	ds_read_b128 v[222:225], v169 offset:23552
	global_load_lds_dwordx4 v[162:163], off
	v_lshl_add_u64 v[162:163], v[142:143], 0, v[146:147]
	s_add_i32 m0, s4, 0x2000
	s_add_i32 s4, s69, s60
	global_load_lds_dwordx4 v[162:163], off
	v_lshl_add_u64 v[162:163], v[142:143], 0, s[6:7]
	v_lshl_add_u64 v[226:227], v[162:163], 0, v[150:151]
	s_mov_b32 m0, s4
	v_lshl_add_u64 v[162:163], v[162:163], 0, v[146:147]
	global_load_lds_dwordx4 v[226:227], off
	s_add_i32 m0, s4, 0x2000
	v_lshl_add_u64 v[226:227], s[58:59], 0, v[148:149]
	global_load_lds_dwordx4 v[162:163], off
	v_lshl_add_u64 v[162:163], s[58:59], 0, v[152:153]
	s_mov_b32 m0, s18
	s_nop 0
	global_load_lds_dwordx4 v[162:163], off
	s_mov_b32 m0, s19
	s_nop 0
	global_load_lds_dwordx4 v[226:227], off
	s_waitcnt vmcnt(8)
	s_waitcnt lgkmcnt(0)
	s_barrier
; #define PG8_STAGE_A(bufoff, base, h, isnext) do { if constexpr (Sched::GATHER) { unsigned vv_[2] = {(isnext) ? vn[h][0] : vc[h][0], (isnext) ? vn[h][1] : vc[h][1]}; PG8_STAGE(bufoff, base, vv_); } else { PG8_STAGE(bufoff, (base) + (h) * hstep, voffA); } } while (0)
; #define PG8_LDA(dst, b, h) do { _Pragma("unroll") for (int m = 0; m < 4; ++m) _Pragma("unroll") for (int k = 0; k < 2; ++k) dst[m][k] = *(const PG8_LAS bf16x8*)(lds + PG8_SA(b, h) + aoff + m * 2048 + k * 1024); } while (0)
; #define PG8_LDB(dst, b, h) do { _Pragma("unroll") for (int n = 0; n < 2; ++n) _Pragma("unroll") for (int k = 0; k < 2; ++k) dst[n][k] = *(const PG8_LAS bf16x8*)(lds + PG8_SB(b, h) + boff + n * 2048 + k * 1024); } while (0)
; #define PG8_MMA(ai, bj, At, Bt) do { __builtin_amdgcn_s_setprio(1); _Pragma("unroll") for (int m = 0; m < 4; ++m) _Pragma("unroll") for (int n = 0; n < 2; ++n) _Pragma("unroll") for (int k = 0; k < 2; ++k) \
;         acc[ai][bj][m][n] = __builtin_amdgcn_mfma_f32_16x16x32_bf16(Bt[n][k], At[m][k], acc[ai][bj][m][n], 0, 0, 0); __builtin_amdgcn_s_setprio(0); } while (0)
; #define PG8_WAIT_V(n) asm volatile("s_waitcnt vmcnt(" #n ")" ::: "memory")
; #define PG8_WAIT_L(n) asm volatile("s_waitcnt lgkmcnt(" #n ")" ::: "memory")
; #define PG8_BAR __builtin_amdgcn_s_barrier()
; #define PG8_SCHED __builtin_amdgcn_sched_barrier(0)
; template <class Epi, class Sched, bool ALIGN_EPI = false, bool SP2 = false>
; __device__ __forceinline__ void gemm_phase(PG8_LAS unsigned char* lds, const Gemm g, const Sched& S, const Epi& E, const int tid_in) {
;     ...
;             PG8_WAIT_V(8); PG8_WAIT_L(0); PG8_BAR; PG8_MMA(1, 0, At, B0); PG8_MMA(1, 1, At, B1); PG8_BAR; PG8_SCHED;
;             PG8_LDB(B0, 1, 0); PG8_LDB(B1, 1, 1); PG8_SCHED; PG8_LDA(At, 1, 0); PG8_STAGE_A(PG8_SA(0, 1), a2, 1, last);
;             PG8_WAIT_V(8); PG8_WAIT_L(0); PG8_BAR; PG8_MMA(0, 0, At, B0); PG8_MMA(0, 1, At, B1); PG8_BAR; PG8_SCHED;
	s_waitcnt lgkmcnt(0)
	v_mfma_f32_16x16x32_bf16 v[60:63], v[134:137], v[194:197], v[60:63]
	v_mfma_f32_16x16x32_bf16 v[56:59], v[170:173], v[194:197], v[56:59]
	v_mfma_f32_16x16x32_bf16 v[48:51], v[134:137], v[202:205], v[48:51]
	v_mfma_f32_16x16x32_bf16 v[40:43], v[170:173], v[202:205], v[40:43]
	v_mfma_f32_16x16x32_bf16 v[32:35], v[134:137], v[210:213], v[32:35]
	v_mfma_f32_16x16x32_bf16 v[24:27], v[170:173], v[210:213], v[24:27]
	v_mfma_f32_16x16x32_bf16 v[16:19], v[134:137], v[218:221], v[16:19]
	v_mfma_f32_16x16x32_bf16 v[8:11], v[170:173], v[218:221], v[8:11]
	v_mfma_f32_16x16x32_bf16 v[60:63], v[138:141], v[198:201], v[60:63]
	v_mfma_f32_16x16x32_bf16 v[56:59], v[174:177], v[198:201], v[56:59]
	v_mfma_f32_16x16x32_bf16 v[48:51], v[138:141], v[206:209], v[48:51]
	v_mfma_f32_16x16x32_bf16 v[40:43], v[174:177], v[206:209], v[40:43]
	v_mfma_f32_16x16x32_bf16 v[32:35], v[138:141], v[214:217], v[32:35]
	v_mfma_f32_16x16x32_bf16 v[24:27], v[174:177], v[214:217], v[24:27]
	v_mfma_f32_16x16x32_bf16 v[16:19], v[138:141], v[222:225], v[16:19]
	v_mfma_f32_16x16x32_bf16 v[8:11], v[174:177], v[222:225], v[8:11]
	v_mfma_f32_16x16x32_bf16 v[52:55], v[178:181], v[194:197], v[52:55]
	v_mfma_f32_16x16x32_bf16 v[44:47], v[186:189], v[194:197], v[44:47]
	v_mfma_f32_16x16x32_bf16 v[36:39], v[178:181], v[202:205], v[36:39]
	v_mfma_f32_16x16x32_bf16 v[28:31], v[186:189], v[202:205], v[28:31]
	v_mfma_f32_16x16x32_bf16 v[20:23], v[178:181], v[210:213], v[20:23]
	v_mfma_f32_16x16x32_bf16 v[12:15], v[186:189], v[210:213], v[12:15]
	v_mfma_f32_16x16x32_bf16 v[4:7], v[178:181], v[218:221], v[4:7]
	v_mfma_f32_16x16x32_bf16 v[0:3], v[186:189], v[218:221], v[0:3]
	v_mfma_f32_16x16x32_bf16 v[52:55], v[182:185], v[198:201], v[52:55]
	v_mfma_f32_16x16x32_bf16 v[44:47], v[190:193], v[198:201], v[44:47]
	v_mfma_f32_16x16x32_bf16 v[36:39], v[182:185], v[206:209], v[36:39]
	v_mfma_f32_16x16x32_bf16 v[28:31], v[190:193], v[206:209], v[28:31]
	v_mfma_f32_16x16x32_bf16 v[20:23], v[182:185], v[214:217], v[20:23]
	v_mfma_f32_16x16x32_bf16 v[12:15], v[190:193], v[214:217], v[12:15]
	v_mfma_f32_16x16x32_bf16 v[4:7], v[182:185], v[222:225], v[4:7]
	v_mfma_f32_16x16x32_bf16 v[0:3], v[190:193], v[222:225], v[0:3]
	s_barrier
	s_add_i32 s4, 0, 0x18000
	v_add_u32_e32 v133, s4, v165
	s_add_i32 s45, 0, 0x1c000
	ds_read_b128 v[134:137], v133
	ds_read_b128 v[138:141], v133 offset:1024
	ds_read_b128 v[170:173], v133 offset:2048
	ds_read_b128 v[174:177], v133 offset:3072
	v_add_u32_e32 v133, s45, v165
	ds_read_b128 v[178:181], v133
	ds_read_b128 v[182:185], v133 offset:1024
	ds_read_b128 v[186:189], v133 offset:2048
	ds_read_b128 v[190:193], v133 offset:3072
	s_add_u32 s58, s58, 0x80000
	s_addc_u32 s59, s59, 0
	s_mov_b32 m0, s53
	v_lshl_add_u64 v[228:229], s[58:59], 0, v[152:153]
	ds_read_b128 v[194:197], v169 offset:32768
	ds_read_b128 v[198:201], v169 offset:33792
	ds_read_b128 v[202:205], v169 offset:34816
	ds_read_b128 v[206:209], v169 offset:35840
	ds_read_b128 v[210:213], v169 offset:36864
	ds_read_b128 v[214:217], v169 offset:37888
	ds_read_b128 v[218:221], v169 offset:38912
	ds_read_b128 v[222:225], v169 offset:39936
	global_load_lds_dwordx4 v[228:229], off
	v_lshl_add_u64 v[228:229], s[58:59], 0, v[148:149]
	s_mov_b32 m0, s55
	s_nop 0
	global_load_lds_dwordx4 v[228:229], off
	s_waitcnt vmcnt(8)
	s_waitcnt lgkmcnt(0)
	s_barrier
	s_waitcnt lgkmcnt(0)
	v_mfma_f32_16x16x32_bf16 v[124:127], v[134:137], v[194:197], v[124:127]
	v_mfma_f32_16x16x32_bf16 v[120:123], v[170:173], v[194:197], v[120:123]
	v_mfma_f32_16x16x32_bf16 v[116:119], v[134:137], v[202:205], v[116:119]
	v_mfma_f32_16x16x32_bf16 v[112:115], v[170:173], v[202:205], v[112:115]
	v_mfma_f32_16x16x32_bf16 v[108:111], v[134:137], v[210:213], v[108:111]
	v_mfma_f32_16x16x32_bf16 v[100:103], v[170:173], v[210:213], v[100:103]
	v_mfma_f32_16x16x32_bf16 v[92:95], v[134:137], v[218:221], v[92:95]
	v_mfma_f32_16x16x32_bf16 v[84:87], v[170:173], v[218:221], v[84:87]
	v_mfma_f32_16x16x32_bf16 v[124:127], v[138:141], v[198:201], v[124:127]
	v_mfma_f32_16x16x32_bf16 v[120:123], v[174:177], v[198:201], v[120:123]
	v_mfma_f32_16x16x32_bf16 v[116:119], v[138:141], v[206:209], v[116:119]
	v_mfma_f32_16x16x32_bf16 v[112:115], v[174:177], v[206:209], v[112:115]
	v_mfma_f32_16x16x32_bf16 v[108:111], v[138:141], v[214:217], v[108:111]
	v_mfma_f32_16x16x32_bf16 v[100:103], v[174:177], v[214:217], v[100:103]
	v_mfma_f32_16x16x32_bf16 v[92:95], v[138:141], v[222:225], v[92:95]
	v_mfma_f32_16x16x32_bf16 v[84:87], v[174:177], v[222:225], v[84:87]
	v_mfma_f32_16x16x32_bf16 v[104:107], v[178:181], v[194:197], v[104:107]
	v_mfma_f32_16x16x32_bf16 v[96:99], v[186:189], v[194:197], v[96:99]
	v_mfma_f32_16x16x32_bf16 v[88:91], v[178:181], v[202:205], v[88:91]
	v_mfma_f32_16x16x32_bf16 v[80:83], v[186:189], v[202:205], v[80:83]
	v_mfma_f32_16x16x32_bf16 v[76:79], v[178:181], v[210:213], v[76:79]
	v_mfma_f32_16x16x32_bf16 v[72:75], v[186:189], v[210:213], v[72:75]
	v_mfma_f32_16x16x32_bf16 v[68:71], v[178:181], v[218:221], v[68:71]
	v_mfma_f32_16x16x32_bf16 v[64:67], v[186:189], v[218:221], v[64:67]
	v_mfma_f32_16x16x32_bf16 v[104:107], v[182:185], v[198:201], v[104:107]
	v_mfma_f32_16x16x32_bf16 v[96:99], v[190:193], v[198:201], v[96:99]
	v_mfma_f32_16x16x32_bf16 v[88:91], v[182:185], v[206:209], v[88:91]
	v_mfma_f32_16x16x32_bf16 v[80:83], v[190:193], v[206:209], v[80:83]
	v_mfma_f32_16x16x32_bf16 v[76:79], v[182:185], v[214:217], v[76:79]
	v_mfma_f32_16x16x32_bf16 v[72:75], v[190:193], v[214:217], v[72:75]
	v_mfma_f32_16x16x32_bf16 v[68:71], v[182:185], v[222:225], v[68:71]
	v_mfma_f32_16x16x32_bf16 v[64:67], v[190:193], v[222:225], v[64:67]
	s_barrier
; #define PG8_STAGE(bufoff, gbase, voff) do { _Pragma("unroll") for (int _i = 0; _i < 2; ++_i) \
;         __builtin_amdgcn_global_load_lds((const unsigned*)((const char*)(gbase) + (voff)[_i]), (PG8_LAS unsigned*)(lds + (bufoff) + ldsw + _i * 8192), 16, 0, 0); } while (0)
; #define PG8_STAGE_A(bufoff, base, h, isnext) do { if constexpr (Sched::GATHER) { unsigned vv_[2] = {(isnext) ? vn[h][0] : vc[h][0], (isnext) ? vn[h][1] : vc[h][1]}; PG8_STAGE(bufoff, base, vv_); } else { PG8_STAGE(bufoff, (base) + (h) * hstep, voffA); } } while (0)
; #define PG8_LDA(dst, b, h) do { _Pragma("unroll") for (int m = 0; m < 4; ++m) _Pragma("unroll") for (int k = 0; k < 2; ++k) dst[m][k] = *(const PG8_LAS bf16x8*)(lds + PG8_SA(b, h) + aoff + m * 2048 + k * 1024); } while (0)
; #define PG8_MMA(ai, bj, At, Bt) do { __builtin_amdgcn_s_setprio(1); _Pragma("unroll") for (int m = 0; m < 4; ++m) _Pragma("unroll") for (int n = 0; n < 2; ++n) _Pragma("unroll") for (int k = 0; k < 2; ++k) \
;         acc[ai][bj][m][n] = __builtin_amdgcn_mfma_f32_16x16x32_bf16(Bt[n][k], At[m][k], acc[ai][bj][m][n], 0, 0, 0); __builtin_amdgcn_s_setprio(0); } while (0)
; #define PG8_WAIT_V(n) asm volatile("s_waitcnt vmcnt(" #n ")" ::: "memory")
; #define PG8_WAIT_L(n) asm volatile("s_waitcnt lgkmcnt(" #n ")" ::: "memory")
; #define PG8_BAR __builtin_amdgcn_s_barrier()
; #define PG8_SCHED __builtin_amdgcn_sched_barrier(0)
; template <class Epi, class Sched, bool ALIGN_EPI = false, bool SP2 = false>
; __device__ __forceinline__ void gemm_phase(PG8_LAS unsigned char* lds, const Gemm g, const Sched& S, const Epi& E, const int tid_in) {
;     ...
;         for (int t = (Epi::HAS_MID && seg == 1) ? nt / 2 : 0; t < ((Epi::HAS_MID && seg == 0) ? nt / 2 : nt); t += 2) {
;     ...
;             PG8_LDA(At, 1, 1); PG8_STAGE(PG8_SB(1, 0), b3, voffB); PG8_STAGE(PG8_SB(1, 1), b3 + hstepB, voffB); PG8_STAGE_A(PG8_SA(1, 0), a3, 0, last);
;             PG8_WAIT_V(8); PG8_WAIT_L(0); PG8_BAR; PG8_MMA(1, 0, At, B0); PG8_MMA(1, 1, At, B1); PG8_BAR; PG8_SCHED;
	v_lshl_add_u64 v[228:229], v[142:143], 0, s[26:27]
	s_add_i32 s4, s4, s60
	v_lshl_add_u64 v[230:231], v[228:229], 0, v[150:151]
	s_mov_b32 m0, s4
	ds_read_b128 v[194:197], v169 offset:49152
	ds_read_b128 v[198:201], v169 offset:50176
	ds_read_b128 v[202:205], v169 offset:51200
	ds_read_b128 v[206:209], v169 offset:52224
	ds_read_b128 v[210:213], v169 offset:53248
	ds_read_b128 v[214:217], v169 offset:54272
	ds_read_b128 v[218:221], v169 offset:55296
	ds_read_b128 v[222:225], v169 offset:56320
	global_load_lds_dwordx4 v[230:231], off
	v_lshl_add_u64 v[228:229], v[228:229], 0, v[146:147]
	s_add_i32 m0, s4, 0x2000
	v_lshl_add_u64 v[142:143], v[142:143], 0, s[30:31]
	s_add_i32 s4, s45, s60
	global_load_lds_dwordx4 v[228:229], off
	v_lshl_add_u64 v[228:229], v[142:143], 0, v[150:151]
	s_mov_b32 m0, s4
	v_lshl_add_u64 v[142:143], v[142:143], 0, v[146:147]
	global_load_lds_dwordx4 v[228:229], off
	s_add_i32 m0, s4, 0x2000
	s_nop 0
	global_load_lds_dwordx4 v[142:143], off
	v_lshl_add_u64 v[142:143], v[162:163], 0, s[28:29]
	s_mov_b32 m0, s64
	s_nop 0
	global_load_lds_dwordx4 v[142:143], off
	v_lshl_add_u64 v[142:143], v[226:227], 0, s[28:29]
	s_mov_b32 m0, s65
	s_nop 0
	global_load_lds_dwordx4 v[142:143], off
	s_waitcnt vmcnt(8)
	s_waitcnt lgkmcnt(0)
	s_barrier
	s_waitcnt lgkmcnt(0)
	v_mfma_f32_16x16x32_bf16 v[60:63], v[134:137], v[194:197], v[60:63]
	v_mfma_f32_16x16x32_bf16 v[56:59], v[170:173], v[194:197], v[56:59]
	v_mfma_f32_16x16x32_bf16 v[48:51], v[134:137], v[202:205], v[48:51]
	v_mfma_f32_16x16x32_bf16 v[40:43], v[170:173], v[202:205], v[40:43]
	v_mfma_f32_16x16x32_bf16 v[32:35], v[134:137], v[210:213], v[32:35]
	v_mfma_f32_16x16x32_bf16 v[24:27], v[170:173], v[210:213], v[24:27]
	v_mfma_f32_16x16x32_bf16 v[16:19], v[134:137], v[218:221], v[16:19]
	v_mfma_f32_16x16x32_bf16 v[8:11], v[170:173], v[218:221], v[8:11]
	v_mfma_f32_16x16x32_bf16 v[60:63], v[138:141], v[198:201], v[60:63]
	v_mfma_f32_16x16x32_bf16 v[56:59], v[174:177], v[198:201], v[56:59]
	v_mfma_f32_16x16x32_bf16 v[48:51], v[138:141], v[206:209], v[48:51]
	v_mfma_f32_16x16x32_bf16 v[40:43], v[174:177], v[206:209], v[40:43]
	v_mfma_f32_16x16x32_bf16 v[32:35], v[138:141], v[214:217], v[32:35]
	v_mfma_f32_16x16x32_bf16 v[24:27], v[174:177], v[214:217], v[24:27]
	v_mfma_f32_16x16x32_bf16 v[16:19], v[138:141], v[222:225], v[16:19]
	v_mfma_f32_16x16x32_bf16 v[8:11], v[174:177], v[222:225], v[8:11]
	v_mfma_f32_16x16x32_bf16 v[52:55], v[178:181], v[194:197], v[52:55]
	v_mfma_f32_16x16x32_bf16 v[44:47], v[186:189], v[194:197], v[44:47]
	v_mfma_f32_16x16x32_bf16 v[36:39], v[178:181], v[202:205], v[36:39]
	v_mfma_f32_16x16x32_bf16 v[28:31], v[186:189], v[202:205], v[28:31]
	v_mfma_f32_16x16x32_bf16 v[20:23], v[178:181], v[210:213], v[20:23]
	v_mfma_f32_16x16x32_bf16 v[12:15], v[186:189], v[210:213], v[12:15]
	v_mfma_f32_16x16x32_bf16 v[4:7], v[178:181], v[218:221], v[4:7]
	v_mfma_f32_16x16x32_bf16 v[0:3], v[186:189], v[218:221], v[0:3]
	v_mfma_f32_16x16x32_bf16 v[52:55], v[182:185], v[198:201], v[52:55]
	v_mfma_f32_16x16x32_bf16 v[44:47], v[190:193], v[198:201], v[44:47]
	v_mfma_f32_16x16x32_bf16 v[36:39], v[182:185], v[206:209], v[36:39]
	v_mfma_f32_16x16x32_bf16 v[28:31], v[190:193], v[206:209], v[28:31]
	v_mfma_f32_16x16x32_bf16 v[20:23], v[182:185], v[214:217], v[20:23]
	v_mfma_f32_16x16x32_bf16 v[12:15], v[190:193], v[214:217], v[12:15]
	v_mfma_f32_16x16x32_bf16 v[4:7], v[182:185], v[222:225], v[4:7]
	v_mfma_f32_16x16x32_bf16 v[0:3], v[190:193], v[222:225], v[0:3]
	s_barrier
	s_add_i32 s21, s21, 2
	s_add_u32 s56, s56, 0x100
	s_addc_u32 s57, s57, 0
	s_cmp_gt_u32 s21, 29
	v_lshl_add_u64 v[130:131], v[130:131], 0, s[36:37]
	s_cbranch_scc0 .LBB0_3495
	s_and_b64 vcc, exec, s[34:35]
	s_cbranch_vccz .LBB0_3498
	s_barrier
